# v12 + s_setprio flips removed from the four GEMM main loops
# speedup vs baseline: 1.0103x; 1.0103x over previous
.LBB0_236:
	ds_read_b128 v[146:149], v156
	ds_read_b128 v[160:163], v156 offset:1024
	ds_read_b128 v[164:167], v156 offset:2048
	ds_read_b128 v[168:171], v156 offset:3072
	s_add_u32 s30, s28, 0xfff80080
	s_addc_u32 s31, s29, -1
	s_cmp_eq_u32 s75, 28
	s_cselect_b32 s35, s7, s31
	s_cselect_b32 s34, s21, s30
	s_cselect_b32 s31, s19, s74
	s_cselect_b32 s30, s72, s73
	v_lshl_add_u64 v[206:207], s[28:29], 0, v[138:139]
	s_add_i32 m0, s9, 0xc000
	ds_read_b128 v[172:175], v157
	ds_read_b128 v[176:179], v157 offset:1024
	ds_read_b128 v[180:183], v157 offset:2048
	ds_read_b128 v[184:187], v157 offset:3072
	ds_read_b128 v[188:191], v157 offset:4096
	ds_read_b128 v[192:195], v157 offset:5120
	ds_read_b128 v[198:201], v157 offset:6144
	ds_read_b128 v[202:205], v157 offset:7168
	global_load_lds_dwordx4 v[206:207], off
	v_lshl_add_u64 v[206:207], s[28:29], 0, v[140:141]
	s_add_i32 m0, s9, 0xe000
	s_nop 0
	global_load_lds_dwordx4 v[206:207], off
	s_waitcnt lgkmcnt(8)
	s_barrier
	s_waitcnt lgkmcnt(0)
	s_waitcnt lgkmcnt(0)
	v_mfma_f32_16x16x32_bf16 v[126:129], v[146:149], v[172:175], v[126:129]
	v_mfma_f32_16x16x32_bf16 v[122:125], v[164:167], v[172:175], v[122:125]
	v_mfma_f32_16x16x32_bf16 v[110:113], v[146:149], v[180:183], v[110:113]
	v_mfma_f32_16x16x32_bf16 v[106:109], v[164:167], v[180:183], v[106:109]
	v_mfma_f32_16x16x32_bf16 v[94:97], v[146:149], v[188:191], v[94:97]
	v_mfma_f32_16x16x32_bf16 v[90:93], v[164:167], v[188:191], v[90:93]
	v_mfma_f32_16x16x32_bf16 v[78:81], v[146:149], v[198:201], v[78:81]
	v_mfma_f32_16x16x32_bf16 v[74:77], v[164:167], v[198:201], v[74:77]
	v_mfma_f32_16x16x32_bf16 v[126:129], v[160:163], v[176:179], v[126:129]
	v_mfma_f32_16x16x32_bf16 v[122:125], v[168:171], v[176:179], v[122:125]
	v_mfma_f32_16x16x32_bf16 v[110:113], v[160:163], v[184:187], v[110:113]
	v_mfma_f32_16x16x32_bf16 v[106:109], v[168:171], v[184:187], v[106:109]
	v_mfma_f32_16x16x32_bf16 v[94:97], v[160:163], v[192:195], v[94:97]
	v_mfma_f32_16x16x32_bf16 v[90:93], v[168:171], v[192:195], v[90:93]
	v_mfma_f32_16x16x32_bf16 v[78:81], v[160:163], v[202:205], v[78:81]
	v_mfma_f32_16x16x32_bf16 v[74:77], v[168:171], v[202:205], v[74:77]
	s_barrier
	s_add_i32 s76, s69, s40
	v_lshl_add_u64 v[222:223], s[30:31], 0, v[132:133]
	s_mov_b32 m0, s76
	ds_read_b128 v[206:209], v158
	ds_read_b128 v[210:213], v158 offset:1024
	ds_read_b128 v[214:217], v158 offset:2048
	ds_read_b128 v[218:221], v158 offset:3072
	global_load_lds_dwordx4 v[222:223], off
	v_lshl_add_u64 v[224:225], s[30:31], 0, v[136:137]
	s_add_i32 m0, s76, 0x2000
	s_nop 0
	global_load_lds_dwordx4 v[224:225], off
	s_barrier
	s_waitcnt lgkmcnt(0)
	s_waitcnt lgkmcnt(0)
	v_mfma_f32_16x16x32_bf16 v[118:121], v[206:209], v[172:175], v[118:121]
	v_mfma_f32_16x16x32_bf16 v[114:117], v[214:217], v[172:175], v[114:117]
	v_mfma_f32_16x16x32_bf16 v[102:105], v[206:209], v[180:183], v[102:105]
	v_mfma_f32_16x16x32_bf16 v[98:101], v[214:217], v[180:183], v[98:101]
	v_mfma_f32_16x16x32_bf16 v[86:89], v[206:209], v[188:191], v[86:89]
	v_mfma_f32_16x16x32_bf16 v[82:85], v[214:217], v[188:191], v[82:85]
	v_mfma_f32_16x16x32_bf16 v[70:73], v[206:209], v[198:201], v[70:73]
	v_mfma_f32_16x16x32_bf16 v[66:69], v[214:217], v[198:201], v[66:69]
	v_mfma_f32_16x16x32_bf16 v[118:121], v[210:213], v[176:179], v[118:121]
	v_mfma_f32_16x16x32_bf16 v[114:117], v[218:221], v[176:179], v[114:117]
	v_mfma_f32_16x16x32_bf16 v[102:105], v[210:213], v[184:187], v[102:105]
	v_mfma_f32_16x16x32_bf16 v[98:101], v[218:221], v[184:187], v[98:101]
	v_mfma_f32_16x16x32_bf16 v[86:89], v[210:213], v[192:195], v[86:89]
	v_mfma_f32_16x16x32_bf16 v[82:85], v[218:221], v[192:195], v[82:85]
	v_mfma_f32_16x16x32_bf16 v[70:73], v[210:213], v[202:205], v[70:73]
	v_mfma_f32_16x16x32_bf16 v[66:69], v[218:221], v[202:205], v[66:69]
	s_mov_b32 m0, s9
	v_lshl_add_u64 v[226:227], s[34:35], 0, v[130:131]
	s_barrier
	ds_read_b128 v[172:175], v157 offset:16384
	ds_read_b128 v[176:179], v157 offset:17408
	ds_read_b128 v[180:183], v157 offset:18432
	ds_read_b128 v[184:187], v157 offset:19456
	ds_read_b128 v[188:191], v157 offset:20480
	ds_read_b128 v[192:195], v157 offset:21504
	ds_read_b128 v[198:201], v157 offset:22528
	ds_read_b128 v[202:205], v157 offset:23552
	global_load_lds_dwordx4 v[226:227], off
	v_lshl_add_u64 v[228:229], s[34:35], 0, v[134:135]
	s_mov_b32 m0, s53
	s_nop 0
	global_load_lds_dwordx4 v[228:229], off
	s_barrier
	s_waitcnt lgkmcnt(0)
	s_waitcnt lgkmcnt(0)
	v_mfma_f32_16x16x32_bf16 v[62:65], v[146:149], v[172:175], v[62:65]
	v_mfma_f32_16x16x32_bf16 v[58:61], v[164:167], v[172:175], v[58:61]
	v_mfma_f32_16x16x32_bf16 v[46:49], v[146:149], v[180:183], v[46:49]
	v_mfma_f32_16x16x32_bf16 v[42:45], v[164:167], v[180:183], v[42:45]
	v_mfma_f32_16x16x32_bf16 v[30:33], v[146:149], v[188:191], v[30:33]
	v_mfma_f32_16x16x32_bf16 v[26:29], v[164:167], v[188:191], v[26:29]
	v_mfma_f32_16x16x32_bf16 v[14:17], v[146:149], v[198:201], v[14:17]
	v_mfma_f32_16x16x32_bf16 v[10:13], v[164:167], v[198:201], v[10:13]
	v_mfma_f32_16x16x32_bf16 v[62:65], v[160:163], v[176:179], v[62:65]
	v_mfma_f32_16x16x32_bf16 v[58:61], v[168:171], v[176:179], v[58:61]
	v_mfma_f32_16x16x32_bf16 v[46:49], v[160:163], v[184:187], v[46:49]
	v_mfma_f32_16x16x32_bf16 v[42:45], v[168:171], v[184:187], v[42:45]
	v_mfma_f32_16x16x32_bf16 v[30:33], v[160:163], v[192:195], v[30:33]
	v_mfma_f32_16x16x32_bf16 v[26:29], v[168:171], v[192:195], v[26:29]
	v_mfma_f32_16x16x32_bf16 v[14:17], v[160:163], v[202:205], v[14:17]
	v_mfma_f32_16x16x32_bf16 v[10:13], v[168:171], v[202:205], v[10:13]
	s_barrier
	s_add_u32 s76, s30, 0x80000
	s_addc_u32 s77, s31, 0
	s_add_i32 s78, s70, s40
	v_lshl_add_u64 v[146:147], s[76:77], 0, v[132:133]
	s_mov_b32 m0, s78
	s_nop 0
	global_load_lds_dwordx4 v[146:147], off
	v_lshl_add_u64 v[146:147], s[76:77], 0, v[136:137]
	s_add_i32 m0, s78, 0x2000
	s_nop 0
	global_load_lds_dwordx4 v[146:147], off
	s_waitcnt vmcnt(6)
	s_barrier
	v_mfma_f32_16x16x32_bf16 v[54:57], v[206:209], v[172:175], v[54:57]
	v_mfma_f32_16x16x32_bf16 v[50:53], v[214:217], v[172:175], v[50:53]
	v_mfma_f32_16x16x32_bf16 v[38:41], v[206:209], v[180:183], v[38:41]
	v_mfma_f32_16x16x32_bf16 v[34:37], v[214:217], v[180:183], v[34:37]
	v_mfma_f32_16x16x32_bf16 v[22:25], v[206:209], v[188:191], v[22:25]
	v_mfma_f32_16x16x32_bf16 v[18:21], v[214:217], v[188:191], v[18:21]
	v_mfma_f32_16x16x32_bf16 v[6:9], v[206:209], v[198:201], v[6:9]
	v_mfma_f32_16x16x32_bf16 v[2:5], v[214:217], v[198:201], v[2:5]
	v_mfma_f32_16x16x32_bf16 v[54:57], v[210:213], v[176:179], v[54:57]
	v_mfma_f32_16x16x32_bf16 v[50:53], v[218:221], v[176:179], v[50:53]
	v_mfma_f32_16x16x32_bf16 v[38:41], v[210:213], v[184:187], v[38:41]
	v_mfma_f32_16x16x32_bf16 v[34:37], v[218:221], v[184:187], v[34:37]
	v_mfma_f32_16x16x32_bf16 v[22:25], v[210:213], v[192:195], v[22:25]
	v_mfma_f32_16x16x32_bf16 v[18:21], v[218:221], v[192:195], v[18:21]
	v_mfma_f32_16x16x32_bf16 v[6:9], v[210:213], v[202:205], v[6:9]
	v_mfma_f32_16x16x32_bf16 v[2:5], v[218:221], v[202:205], v[2:5]
	s_add_i32 s76, 0, 0x18000
	v_add_u32_e32 v159, s76, v153
	s_barrier
	ds_read_b128 v[146:149], v159
	ds_read_b128 v[160:163], v159 offset:1024
	ds_read_b128 v[164:167], v159 offset:2048
	ds_read_b128 v[168:171], v159 offset:3072
	s_add_u32 s34, s34, 0x80000
	s_addc_u32 s35, s35, 0
	s_mov_b32 m0, s54
	v_lshl_add_u64 v[206:207], s[34:35], 0, v[130:131]
	ds_read_b128 v[172:175], v157 offset:32768
	ds_read_b128 v[176:179], v157 offset:33792
	ds_read_b128 v[180:183], v157 offset:34816
	ds_read_b128 v[184:187], v157 offset:35840
	ds_read_b128 v[188:191], v157 offset:36864
	ds_read_b128 v[192:195], v157 offset:37888
	ds_read_b128 v[198:201], v157 offset:38912
	ds_read_b128 v[202:205], v157 offset:39936
	global_load_lds_dwordx4 v[206:207], off
	v_lshl_add_u64 v[206:207], s[34:35], 0, v[134:135]
	s_mov_b32 m0, s55
	s_nop 0
	global_load_lds_dwordx4 v[206:207], off
	s_waitcnt lgkmcnt(8)
	s_barrier
	s_waitcnt lgkmcnt(0)
	s_waitcnt lgkmcnt(0)
	v_mfma_f32_16x16x32_bf16 v[126:129], v[146:149], v[172:175], v[126:129]
	v_mfma_f32_16x16x32_bf16 v[122:125], v[164:167], v[172:175], v[122:125]
	v_mfma_f32_16x16x32_bf16 v[110:113], v[146:149], v[180:183], v[110:113]
	v_mfma_f32_16x16x32_bf16 v[106:109], v[164:167], v[180:183], v[106:109]
	v_mfma_f32_16x16x32_bf16 v[94:97], v[146:149], v[188:191], v[94:97]
	v_mfma_f32_16x16x32_bf16 v[90:93], v[164:167], v[188:191], v[90:93]
	v_mfma_f32_16x16x32_bf16 v[78:81], v[146:149], v[198:201], v[78:81]
	v_mfma_f32_16x16x32_bf16 v[74:77], v[164:167], v[198:201], v[74:77]
	v_mfma_f32_16x16x32_bf16 v[126:129], v[160:163], v[176:179], v[126:129]
	v_mfma_f32_16x16x32_bf16 v[122:125], v[168:171], v[176:179], v[122:125]
	v_mfma_f32_16x16x32_bf16 v[110:113], v[160:163], v[184:187], v[110:113]
	v_mfma_f32_16x16x32_bf16 v[106:109], v[168:171], v[184:187], v[106:109]
	v_mfma_f32_16x16x32_bf16 v[94:97], v[160:163], v[192:195], v[94:97]
	v_mfma_f32_16x16x32_bf16 v[90:93], v[168:171], v[192:195], v[90:93]
	v_mfma_f32_16x16x32_bf16 v[78:81], v[160:163], v[202:205], v[78:81]
	v_mfma_f32_16x16x32_bf16 v[74:77], v[168:171], v[202:205], v[74:77]
	s_barrier
	s_add_i32 s34, 0, 0x1c000
	s_add_i32 s35, s76, s40
	v_add_u32_e32 v159, s34, v153
	v_lshl_add_u64 v[222:223], v[222:223], 0, s[14:15]
	s_mov_b32 m0, s35
	ds_read_b128 v[206:209], v159
	ds_read_b128 v[210:213], v159 offset:1024
	ds_read_b128 v[214:217], v159 offset:2048
	ds_read_b128 v[218:221], v159 offset:3072
	global_load_lds_dwordx4 v[222:223], off
	v_lshl_add_u64 v[222:223], v[224:225], 0, s[14:15]
	s_add_i32 m0, s35, 0x2000
	s_nop 0
	global_load_lds_dwordx4 v[222:223], off
	s_barrier
	s_waitcnt lgkmcnt(0)
	s_waitcnt lgkmcnt(0)
	v_mfma_f32_16x16x32_bf16 v[118:121], v[206:209], v[172:175], v[118:121]
	v_mfma_f32_16x16x32_bf16 v[114:117], v[214:217], v[172:175], v[114:117]
	v_mfma_f32_16x16x32_bf16 v[102:105], v[206:209], v[180:183], v[102:105]
	v_mfma_f32_16x16x32_bf16 v[98:101], v[214:217], v[180:183], v[98:101]
	v_mfma_f32_16x16x32_bf16 v[86:89], v[206:209], v[188:191], v[86:89]
	v_mfma_f32_16x16x32_bf16 v[82:85], v[214:217], v[188:191], v[82:85]
	v_mfma_f32_16x16x32_bf16 v[70:73], v[206:209], v[198:201], v[70:73]
	v_mfma_f32_16x16x32_bf16 v[66:69], v[214:217], v[198:201], v[66:69]
	v_mfma_f32_16x16x32_bf16 v[118:121], v[210:213], v[176:179], v[118:121]
	v_mfma_f32_16x16x32_bf16 v[114:117], v[218:221], v[176:179], v[114:117]
	v_mfma_f32_16x16x32_bf16 v[102:105], v[210:213], v[184:187], v[102:105]
	v_mfma_f32_16x16x32_bf16 v[98:101], v[218:221], v[184:187], v[98:101]
	v_mfma_f32_16x16x32_bf16 v[86:89], v[210:213], v[192:195], v[86:89]
	v_mfma_f32_16x16x32_bf16 v[82:85], v[218:221], v[192:195], v[82:85]
	v_mfma_f32_16x16x32_bf16 v[70:73], v[210:213], v[202:205], v[70:73]
	v_mfma_f32_16x16x32_bf16 v[66:69], v[218:221], v[202:205], v[66:69]
	s_mov_b32 m0, s67
	v_lshl_add_u64 v[222:223], v[226:227], 0, s[14:15]
	s_barrier
	ds_read_b128 v[172:175], v157 offset:49152
	ds_read_b128 v[176:179], v157 offset:50176
	ds_read_b128 v[180:183], v157 offset:51200
	ds_read_b128 v[184:187], v157 offset:52224
	ds_read_b128 v[188:191], v157 offset:53248
	ds_read_b128 v[192:195], v157 offset:54272
	ds_read_b128 v[198:201], v157 offset:55296
	ds_read_b128 v[202:205], v157 offset:56320
	global_load_lds_dwordx4 v[222:223], off
	v_lshl_add_u64 v[222:223], v[228:229], 0, s[14:15]
	s_mov_b32 m0, s68
	s_nop 0
	global_load_lds_dwordx4 v[222:223], off
	s_barrier
	s_waitcnt lgkmcnt(0)
	s_waitcnt lgkmcnt(0)
	v_mfma_f32_16x16x32_bf16 v[62:65], v[146:149], v[172:175], v[62:65]
	v_mfma_f32_16x16x32_bf16 v[58:61], v[164:167], v[172:175], v[58:61]
	v_mfma_f32_16x16x32_bf16 v[46:49], v[146:149], v[180:183], v[46:49]
	v_mfma_f32_16x16x32_bf16 v[42:45], v[164:167], v[180:183], v[42:45]
	v_mfma_f32_16x16x32_bf16 v[30:33], v[146:149], v[188:191], v[30:33]
	v_mfma_f32_16x16x32_bf16 v[26:29], v[164:167], v[188:191], v[26:29]
	v_mfma_f32_16x16x32_bf16 v[14:17], v[146:149], v[198:201], v[14:17]
	v_mfma_f32_16x16x32_bf16 v[10:13], v[164:167], v[198:201], v[10:13]
	v_mfma_f32_16x16x32_bf16 v[62:65], v[160:163], v[176:179], v[62:65]
	v_mfma_f32_16x16x32_bf16 v[58:61], v[168:171], v[176:179], v[58:61]
	v_mfma_f32_16x16x32_bf16 v[46:49], v[160:163], v[184:187], v[46:49]
	v_mfma_f32_16x16x32_bf16 v[42:45], v[168:171], v[184:187], v[42:45]
	v_mfma_f32_16x16x32_bf16 v[30:33], v[160:163], v[192:195], v[30:33]
	v_mfma_f32_16x16x32_bf16 v[26:29], v[168:171], v[192:195], v[26:29]
	v_mfma_f32_16x16x32_bf16 v[14:17], v[160:163], v[202:205], v[14:17]
	v_mfma_f32_16x16x32_bf16 v[10:13], v[168:171], v[202:205], v[10:13]
	s_barrier
	s_add_u32 s30, s30, 0x80080
	s_addc_u32 s31, s31, 0
	s_add_i32 s34, s34, s40
	v_lshl_add_u64 v[146:147], s[30:31], 0, v[132:133]
	s_mov_b32 m0, s34
	s_nop 0
	global_load_lds_dwordx4 v[146:147], off
	v_lshl_add_u64 v[146:147], s[30:31], 0, v[136:137]
	s_add_i32 m0, s34, 0x2000
	s_nop 0
	global_load_lds_dwordx4 v[146:147], off
	s_waitcnt vmcnt(6)
	s_barrier
	v_mfma_f32_16x16x32_bf16 v[54:57], v[206:209], v[172:175], v[54:57]
	v_mfma_f32_16x16x32_bf16 v[50:53], v[214:217], v[172:175], v[50:53]
	v_mfma_f32_16x16x32_bf16 v[38:41], v[206:209], v[180:183], v[38:41]
	v_mfma_f32_16x16x32_bf16 v[34:37], v[214:217], v[180:183], v[34:37]
	v_mfma_f32_16x16x32_bf16 v[22:25], v[206:209], v[188:191], v[22:25]
	v_mfma_f32_16x16x32_bf16 v[18:21], v[214:217], v[188:191], v[18:21]
	v_mfma_f32_16x16x32_bf16 v[6:9], v[206:209], v[198:201], v[6:9]
	v_mfma_f32_16x16x32_bf16 v[2:5], v[214:217], v[198:201], v[2:5]
	v_mfma_f32_16x16x32_bf16 v[54:57], v[210:213], v[176:179], v[54:57]
	v_mfma_f32_16x16x32_bf16 v[50:53], v[218:221], v[176:179], v[50:53]
	v_mfma_f32_16x16x32_bf16 v[38:41], v[210:213], v[184:187], v[38:41]
	v_mfma_f32_16x16x32_bf16 v[34:37], v[218:221], v[184:187], v[34:37]
	v_mfma_f32_16x16x32_bf16 v[22:25], v[210:213], v[192:195], v[22:25]
	v_mfma_f32_16x16x32_bf16 v[18:21], v[218:221], v[192:195], v[18:21]
	v_mfma_f32_16x16x32_bf16 v[6:9], v[210:213], v[202:205], v[6:9]
	v_mfma_f32_16x16x32_bf16 v[2:5], v[218:221], v[202:205], v[2:5]
	s_add_i32 s75, s75, 2
	s_add_u32 s28, s28, 0x100
	s_addc_u32 s29, s29, 0
	s_add_u32 s73, s73, 0x100
	s_addc_u32 s74, s74, 0
	s_cmp_gt_u32 s75, 29
	s_barrier
	s_cbranch_scc0 .LBB0_236
	s_add_i32 s7, s8, -12
	s_cmp_lt_u32 s7, 8
	v_lshl_add_u32 v159, s6, 8, v152
	s_cselect_b64 s[28:29], -1, 0
	s_cmp_lt_i32 s6, 64
	v_lshrrev_b32_e32 v160, 6, v159
	s_cselect_b64 s[30:31], -1, 0
	v_cndmask_b32_e64 v146, v151, v160, s[0:1]
	v_lshlrev_b32_e32 v146, 5, v146
	s_and_b64 s[28:29], s[28:29], s[30:31]
	v_and_b32_e32 v146, 0x7e0, v146
	v_cndmask_b32_e64 v147, 0, 1, s[28:29]
	v_cmp_ne_u32_e64 s[6:7], 1, v147
	s_andn2_b64 vcc, exec, s[28:29]
	v_lshl_add_u32 v161, v146, 2, v154
	s_cbranch_vccnz .LBB0_239
	ds_read_b128 v[146:149], v161
	ds_read_b128 v[162:165], v161 offset:16
	v_mov_b32_e32 v166, v129
	s_cmp_lt_u32 s8, 16
	s_cselect_b64 vcc, -1, 0
	s_waitcnt lgkmcnt(0)
	v_pk_mul_f32 v[168:169], v[126:127], v[146:147] op_sel:[1,1] op_sel_hi:[1,0]
	v_pk_mul_f32 v[166:167], v[166:167], v[148:149] op_sel:[0,1] op_sel_hi:[0,0]
	v_pk_fma_f32 v[170:171], v[126:127], v[146:147], v[168:169] op_sel_hi:[0,1,1] neg_lo:[0,0,1] neg_hi:[0,0,1]
	v_pk_fma_f32 v[126:127], v[126:127], v[146:147], v[168:169] op_sel_hi:[0,1,1]
	v_pk_fma_f32 v[146:147], v[128:129], v[148:149], v[166:167] op_sel_hi:[0,1,1] neg_lo:[0,0,1] neg_hi:[0,0,1]
	v_pk_fma_f32 v[128:129], v[128:129], v[148:149], v[166:167] op_sel_hi:[0,1,1]
	v_pk_mul_f32 v[148:149], v[122:123], v[162:163] op_sel:[1,1] op_sel_hi:[1,0]
	v_mov_b32_e32 v147, v129
	v_pk_fma_f32 v[166:167], v[122:123], v[162:163], v[148:149] op_sel_hi:[0,1,1] neg_lo:[0,0,1] neg_hi:[0,0,1]
	v_pk_fma_f32 v[122:123], v[122:123], v[162:163], v[148:149] op_sel_hi:[0,1,1]
	v_mov_b32_e32 v122, v125
	v_pk_mul_f32 v[148:149], v[122:123], v[164:165] op_sel:[0,1] op_sel_hi:[0,0]
	v_pk_fma_f32 v[162:163], v[124:125], v[164:165], v[148:149] op_sel_hi:[0,1,1] neg_lo:[0,0,1] neg_hi:[0,0,1]
	v_pk_fma_f32 v[124:125], v[124:125], v[164:165], v[148:149] op_sel_hi:[0,1,1]
	v_mov_b32_e32 v171, v127
	v_mov_b32_e32 v163, v125
	v_mov_b32_e32 v167, v123
	v_pk_mul_f32 v[148:149], v[146:147], s[16:17] op_sel_hi:[1,0]
	v_pk_mul_f32 v[164:165], v[170:171], s[16:17] op_sel_hi:[1,0]
	v_pk_mul_f32 v[168:169], v[162:163], s[16:17] op_sel_hi:[1,0]
	v_pk_mul_f32 v[172:173], v[166:167], s[16:17] op_sel_hi:[1,0]
	v_cndmask_b32_e32 v124, v162, v168, vcc
	v_cndmask_b32_e32 v125, v125, v169, vcc
	v_cndmask_b32_e32 v122, v166, v172, vcc
	v_cndmask_b32_e32 v123, v123, v173, vcc
	v_cndmask_b32_e32 v128, v146, v148, vcc
	v_cndmask_b32_e32 v129, v129, v149, vcc
	v_cndmask_b32_e32 v126, v170, v164, vcc
	v_cndmask_b32_e32 v127, v127, v165, vcc

.LBB0_636:
	s_cmpk_gt_i32 s33, 0x1ff
	s_cbranch_scc1 .LBB0_653
	v_mov_b32_e32 v1, 0x52000
	global_load_dword v1, v1, s[88:89] offset:2048
	s_and_b32 s1, s96, 0x3fffffc0
	s_waitcnt vmcnt(0)
	v_lshrrev_b32_e32 v4, 4, v196
	v_and_b32_e32 v5, 15, v0
	s_lshl_b32 s0, s79, 13
	s_lshl_b32 s1, s1, 2
	v_bitop3_b32 v5, v4, v5, 4 bitop3:0x36
	s_add_i32 s23, s1, 0
	s_add_i32 s24, s0, 0
	s_movk_i32 s0, 0x3200
	v_bitop3_b32 v6, v4, v0, 15 bitop3:0x78
	v_lshlrev_b32_e32 v168, 4, v5
	v_mov_b32_e32 v5, 0x25800
	s_lshl_b32 s1, s79, 1
	v_lshlrev_b32_e32 v164, 4, v6
	v_mov_b32_e32 v6, 0xc800
	v_mad_u32_u24 v170, v4, s0, v5
	v_mov_b32_e32 v5, 0x3e800
	s_or_b32 s1, s1, 1
	v_lshrrev_b32_e32 v177, 5, v196
	v_and_b32_e32 v176, 31, v0
	v_lshlrev_b32_e32 v2, 4, v0
	v_mad_u32_u24 v166, v4, s0, v6
	v_mad_u32_u24 v172, v4, s0, v5
	v_mov_b32_e32 v5, 0x57800
	s_lshl_b32 s28, s1, 2
	s_lshl_b32 s29, s1, 1
	s_lshl_b32 s30, s1, 10
	v_lshlrev_b32_e32 v6, 4, v177
	s_movk_i32 s1, 0xf0
	v_mul_u32_u24_e32 v162, 0x3200, v4
	v_mad_u32_u24 v174, v4, s0, v5
	v_and_b32_e32 v4, 0xc0, v2
	v_lshlrev_b32_e32 v178, 8, v176
	v_and_b32_e32 v7, 0xf0, v2
	v_bitop3_b32 v179, v6, v2, s1 bitop3:0x78
	v_or_b32_e32 v2, 32, v6
	v_bitop3_b32 v182, v2, v178, v7 bitop3:0xde
	v_or_b32_e32 v2, 64, v6
	v_bitop3_b32 v184, v2, v178, v7 bitop3:0xde
	v_or_b32_e32 v2, 0x60, v6
	s_lshl_b32 s22, s79, 5
	s_add_i32 s23, s23, 0x20000
	s_add_i32 s24, s24, 0x10000
	s_lshl_b32 s25, s79, 3
	s_lshl_b32 s26, s79, 2
	s_lshl_b32 s27, s79, 11
	v_bitop3_b32 v186, v2, v178, v7 bitop3:0xde
	v_or_b32_e32 v2, 0x80, v6
	s_add_u32 s31, s88, 0x8000
	v_bitop3_b32 v188, v2, v178, v7 bitop3:0xde
	v_or_b32_e32 v2, 0xa0, v6
	s_movk_i32 s0, 0xc0
	v_lshlrev_b32_e32 v5, 3, v0
	s_addc_u32 s34, s89, 0
	v_bitop3_b32 v190, v2, v178, v7 bitop3:0xde
	v_or_b32_e32 v2, 0xc0, v6
	v_lshlrev_b32_e32 v3, 1, v0
	v_and_b32_e32 v5, 0x118, v5
	s_movk_i32 s1, 0x60
	v_bitop3_b32 v191, v6, v7, s0 bitop3:0x36
	v_bitop3_b32 v192, v2, v178, v7 bitop3:0xde
	s_movk_i32 s0, 0xe0
	v_or_b32_e32 v2, 0xe0, v6
	s_cmp_lg_u32 0, -1
	v_bitop3_b32 v185, v6, v7, s1 bitop3:0x36
	s_movk_i32 s1, 0x80
	v_bitop3_b32 v193, v6, v7, s0 bitop3:0x36
	v_bitop3_b32 v194, v2, v178, v7 bitop3:0xde
	v_and_or_b32 v2, v3, 32, v5
	s_cselect_b32 s0, 0, 0
	v_mov_b32_e32 v163, 0
	v_bitop3_b32 v187, v6, v7, s1 bitop3:0x36
	s_movk_i32 s1, 0xa0
	v_add3_u32 v195, v4, s0, v2
	v_mbcnt_lo_u32_b32 v2, -1, 0
	s_add_i32 s53, s27, 0
	s_add_i32 s55, s30, 0
	v_mov_b32_e32 v165, v163
	v_mov_b32_e32 v167, v163
	v_mov_b32_e32 v169, v163
	v_mov_b32_e32 v171, v163
	v_mov_b32_e32 v173, v163
	v_mov_b32_e32 v175, v163
	v_bitop3_b32 v180, v6, v178, v7 bitop3:0xde
	v_bitop3_b32 v181, v6, v7, 32 bitop3:0x36
	v_bitop3_b32 v183, v6, v7, 64 bitop3:0x36
	v_bitop3_b32 v189, v6, v7, s1 bitop3:0x36
	v_cmp_gt_u32_e64 s[0:1], 32, v196
	v_lshl_add_u32 v197, v176, 2, s23
	s_add_i32 s35, s24, 0x400
	s_mov_b64 s[6:7], 0x19000
	s_add_i32 s36, s24, 0x800
	s_add_i32 s37, s24, 0xc00
	s_mov_b64 s[8:9], 0x32000
	s_add_i32 s38, s24, 0x1000
	s_add_i32 s39, s24, 0x1400
	s_mov_b64 s[10:11], 0x4b000
	s_add_i32 s40, s24, 0x1800
	s_add_i32 s41, s24, 0x1c00
	s_movk_i32 s44, 0x1900
	v_mov_b32_e32 v198, 0x2800
	v_mov_b32_e32 v199, 0x8000
	s_mov_b32 s45, 0xf800000
	v_mov_b32_e32 v200, 0x260
	v_mov_b32_e32 v201, 0xc2700000
	v_mbcnt_hi_u32_b32 v202, -1, v2
	s_mov_b64 s[14:15], 0x2bf00800
	v_mov_b32_e32 v203, 0x358637bd
	s_mov_b32 s52, 0x800000
	s_add_i32 s54, s53, 0x8000
	s_add_i32 s64, s55, 0x8000
	s_branch .LBB0_639

.LBB0_639:
	s_ashr_i32 s18, s33, 7
	s_lshl_b32 s68, s18, 12
	s_lshl_b32 s4, s33, 8
	s_and_b32 s4, s4, 0xf00
	s_add_i32 s5, s68, s22
	s_add_i32 s16, s5, s4
	s_bfe_u32 s19, s33, 0x30004
	s_ashr_i32 s17, s16, 31
	s_mul_i32 s5, s16, 0x3200
	s_mul_hi_i32 s4, s16, 0x3200
	s_add_u32 s5, s20, s5
	s_addc_u32 s4, s21, s4
	s_lshl_b32 s65, s19, 8
	s_add_u32 s5, s5, s65
	s_addc_u32 s65, s4, 0
	s_add_u32 s4, s5, 0x1800
	s_addc_u32 s5, s65, 0
	v_xor_b32_e32 v6, 0x80, v164
	v_mov_b32_e32 v7, 0
	v_xor_b32_e32 v8, 0x80, v168
	v_mov_b32_e32 v9, 0
	v_lshl_add_u64 v[2:3], s[4:5], 0, v[162:163]
	s_mov_b32 m0, s24
	v_lshl_add_u64 v[4:5], v[2:3], 0, v[164:165]
	s_lshl_b32 s66, s18, 8
	global_load_lds_dwordx4 v[4:5], off
	v_lshl_add_u64 v[4:5], s[4:5], 0, v[166:167]
	v_lshl_add_u64 v[4:5], v[4:5], 0, v[168:169]
	s_mov_b32 m0, s35
	s_addk_i32 s66, 0x4000
	global_load_lds_dwordx4 v[4:5], off
	v_lshl_add_u64 v[4:5], v[2:3], 0, s[6:7]
	v_lshl_add_u64 v[4:5], v[4:5], 0, v[6:7]
	s_mov_b32 m0, s36
	s_lshl_b32 s65, s19, 7
	global_load_lds_dwordx4 v[4:5], off
	v_lshl_add_u64 v[4:5], s[4:5], 0, v[170:171]
	v_lshl_add_u64 v[4:5], v[4:5], 0, v[8:9]
	s_mov_b32 m0, s37
	v_mov_b32_e32 v12, v177
	global_load_lds_dwordx4 v[4:5], off
	v_lshl_add_u64 v[4:5], v[2:3], 0, s[8:9]
	v_lshl_add_u64 v[4:5], v[4:5], 0, v[164:165]
	s_mov_b32 m0, s38
	s_mov_b32 s70, 0
	global_load_lds_dwordx4 v[4:5], off
	v_lshl_add_u64 v[4:5], s[4:5], 0, v[172:173]
	v_lshl_add_u64 v[4:5], v[4:5], 0, v[168:169]
	s_mov_b32 m0, s39
	s_nop 0
	global_load_lds_dwordx4 v[4:5], off
	v_lshl_add_u64 v[4:5], v[2:3], 0, s[10:11]
	v_lshl_add_u64 v[4:5], v[4:5], 0, v[6:7]
	s_mov_b32 m0, s40
	s_nop 0
	global_load_lds_dwordx4 v[4:5], off
	v_lshl_add_u64 v[4:5], s[4:5], 0, v[174:175]
	v_lshl_add_u64 v[4:5], v[4:5], 0, v[8:9]
	s_mov_b32 m0, s41
	s_mul_i32 s4, s66, 0x3200
	global_load_lds_dwordx4 v[4:5], off
	v_mov_b32_e32 v2, v196
	s_mul_hi_i32 s5, s66, 0x3200
	v_ashrrev_i32_e32 v3, 4, v2
	s_add_u32 s4, s20, s4
	v_and_b32_e32 v4, 15, v2
	v_add_u32_e32 v8, s25, v3
	s_addc_u32 s5, s21, s5
	s_or_b32 s67, s65, 0x1000
	v_bitop3_b32 v9, v8, v4, 15 bitop3:0x6c
	v_mul_lo_u32 v8, v8, s44
	v_ashrrev_i32_e32 v5, 5, v2
	v_add_u32_e32 v8, s67, v8
	v_lshlrev_b32_e32 v9, 4, v9
	v_bfe_u32 v6, v2, 2, 2
	v_lshrrev_b32_e32 v7, 1, v2
	v_lshl_or_b32 v8, v8, 1, v9
	v_add_u32_e32 v9, s26, v5
	v_and_or_b32 v6, v7, 8, v6
	v_lshlrev_b32_e32 v7, 3, v2
	v_lshlrev_b32_e32 v10, 1, v9
	v_and_b32_e32 v7, 24, v7
	v_and_b32_e32 v10, 0xfffff0, v10
	v_and_b32_e32 v9, 4, v9
	v_and_b32_e32 v2, 0x60, v2
	v_or3_b32 v9, v9, v10, v6
	v_or3_b32 v2, s65, v2, v7
	v_mad_u32_u24 v2, v9, s44, v2
	s_mov_b32 m0, s54
	v_lshl_add_u32 v2, v2, 1, v198
	global_load_lds_dwordx4 v8, s[4:5]
	s_mov_b32 m0, s53
	s_mov_b32 s71, 64
	global_load_lds_dwordx4 v2, s[4:5]
	v_add_u32_e32 v2, s28, v3
	v_mul_lo_u32 v3, v2, s44
	v_bitop3_b32 v2, v2, v4, 15 bitop3:0x6c
	v_add_u32_e32 v3, s67, v3
	v_lshlrev_b32_e32 v2, 4, v2
	v_lshl_or_b32 v2, v3, 1, v2
	v_add_u32_e32 v3, s29, v5
	v_lshlrev_b32_e32 v4, 1, v3
	v_and_b32_e32 v5, 4, v3
	v_lshlrev_b32_e32 v3, 5, v3
	v_and_b32_e32 v4, 0xfffff0, v4
	v_and_b32_e32 v3, 0x60, v3
	v_or3_b32 v4, v5, v4, v6
	v_or3_b32 v3, v7, v3, s65
	v_mad_u32_u24 v3, v4, s44, v3
	s_mov_b32 m0, s64
	v_lshl_add_u32 v3, v3, 1, v198
	global_load_lds_dwordx4 v2, s[4:5]
	s_mov_b32 m0, s55
	v_mov_b32_e32 v2, v176
	global_load_lds_dwordx4 v3, s[4:5]
	s_lshl_b32 s4, s18, 4
	s_lshl_b32 s5, s19, 1
	s_or_b32 s4, s5, s4
	s_ashr_i32 s5, s4, 31
	s_lshl_b64 s[4:5], s[4:5], 2
	s_add_u32 s18, s31, s4
	s_addc_u32 s19, s34, s5
	s_add_u32 s4, s88, s4
	s_addc_u32 s5, s89, s5
	global_load_dword v10, v163, s[18:19]
	global_load_dword v11, v199, s[4:5] offset:4
	s_waitcnt vmcnt(0)
	s_waitcnt vmcnt(0) lgkmcnt(0)
	s_barrier
	v_mov_b32_e32 v207, 0
	v_lshlrev_b32_e32 v3, 4, v2
	v_lshlrev_b32_e32 v13, 7, v12
	v_and_b32_e32 v14, 0xf0, v3
	v_lshl_add_u32 v15, v2, 8, s24
	v_xad_u32 v2, v13, v14, v15
	ds_read_b128 v[2:5], v2
	v_or_b32_e32 v6, 16, v13
	v_xad_u32 v6, v6, v14, v15
	ds_read_b128 v[6:9], v6
	v_cmp_eq_u32_e32 vcc, 0, v12
	s_waitcnt lgkmcnt(1)
	v_lshlrev_b32_e32 v16, 16, v2
	v_and_b32_e32 v2, 0xffff0000, v2
	v_mul_f32_e32 v2, v2, v2
	v_fmac_f32_e32 v2, v16, v16
	v_lshlrev_b32_e32 v16, 16, v3
	v_and_b32_e32 v3, 0xffff0000, v3
	v_mul_f32_e32 v3, v3, v3
	v_fmac_f32_e32 v3, v16, v16
	v_add_f32_e32 v2, v2, v3
	v_lshlrev_b32_e32 v3, 16, v4
	v_and_b32_e32 v4, 0xffff0000, v4
	v_mul_f32_e32 v4, v4, v4
	v_fmac_f32_e32 v4, v3, v3
	v_add_f32_e32 v2, v4, v2
	v_and_b32_e32 v4, 0xffff0000, v5
	v_lshlrev_b32_e32 v3, 16, v5
	v_mul_f32_e32 v4, v4, v4
	v_fmac_f32_e32 v4, v3, v3
	v_add_f32_e32 v2, v4, v2
	s_waitcnt lgkmcnt(0)
	v_and_b32_e32 v4, 0xffff0000, v6
	v_lshlrev_b32_e32 v3, 16, v6
	v_mul_f32_e32 v4, v4, v4
	v_fmac_f32_e32 v4, v3, v3
	v_add_f32_e32 v2, v4, v2
	v_and_b32_e32 v4, 0xffff0000, v7
	v_lshlrev_b32_e32 v3, 16, v7
	v_mul_f32_e32 v4, v4, v4
	v_fmac_f32_e32 v4, v3, v3
	v_add_f32_e32 v2, v4, v2
	v_and_b32_e32 v4, 0xffff0000, v8
	v_lshlrev_b32_e32 v3, 16, v8
	v_mul_f32_e32 v4, v4, v4
	v_fmac_f32_e32 v4, v3, v3
	v_and_b32_e32 v3, 0xffff0000, v9
	v_add_f32_e32 v6, v4, v2
	v_lshlrev_b32_e32 v2, 16, v9
	v_mul_f32_e32 v7, v3, v3
	v_fmac_f32_e32 v7, v2, v2
	v_or_b32_e32 v2, 32, v13
	v_xad_u32 v2, v2, v14, v15
	ds_read_b128 v[2:5], v2
	v_add_f32_e32 v16, v7, v6
	v_or_b32_e32 v6, 48, v13
	v_xad_u32 v6, v6, v14, v15
	ds_read_b128 v[6:9], v6
	s_waitcnt lgkmcnt(1)
	v_lshlrev_b32_e32 v17, 16, v2
	v_and_b32_e32 v2, 0xffff0000, v2
	v_mul_f32_e32 v2, v2, v2
	v_fmac_f32_e32 v2, v17, v17
	v_add_f32_e32 v2, v2, v16
	v_lshlrev_b32_e32 v16, 16, v3
	v_and_b32_e32 v3, 0xffff0000, v3
	v_mul_f32_e32 v3, v3, v3
	v_fmac_f32_e32 v3, v16, v16
	v_add_f32_e32 v2, v3, v2
	v_lshlrev_b32_e32 v3, 16, v4
	v_and_b32_e32 v4, 0xffff0000, v4
	v_mul_f32_e32 v4, v4, v4
	v_fmac_f32_e32 v4, v3, v3
	v_add_f32_e32 v2, v4, v2
	v_and_b32_e32 v4, 0xffff0000, v5
	v_lshlrev_b32_e32 v3, 16, v5
	v_mul_f32_e32 v4, v4, v4
	v_fmac_f32_e32 v4, v3, v3
	v_add_f32_e32 v2, v4, v2
	s_waitcnt lgkmcnt(0)
	v_and_b32_e32 v4, 0xffff0000, v6
	v_lshlrev_b32_e32 v3, 16, v6
	v_mul_f32_e32 v4, v4, v4
	v_fmac_f32_e32 v4, v3, v3
	v_add_f32_e32 v2, v4, v2
	v_and_b32_e32 v4, 0xffff0000, v7
	v_lshlrev_b32_e32 v3, 16, v7
	v_mul_f32_e32 v4, v4, v4
	v_fmac_f32_e32 v4, v3, v3
	v_add_f32_e32 v2, v4, v2
	v_and_b32_e32 v4, 0xffff0000, v8
	v_lshlrev_b32_e32 v3, 16, v8
	v_mul_f32_e32 v4, v4, v4
	v_fmac_f32_e32 v4, v3, v3
	v_and_b32_e32 v3, 0xffff0000, v9
	v_add_f32_e32 v6, v4, v2
	v_lshlrev_b32_e32 v2, 16, v9
	v_mul_f32_e32 v7, v3, v3
	v_fmac_f32_e32 v7, v2, v2
	v_or_b32_e32 v2, 64, v13
	v_xad_u32 v2, v2, v14, v15
	ds_read_b128 v[2:5], v2
	v_add_f32_e32 v16, v7, v6
	v_or_b32_e32 v6, 0x50, v13
	v_xad_u32 v6, v6, v14, v15
	ds_read_b128 v[6:9], v6
	s_waitcnt lgkmcnt(1)
	v_lshlrev_b32_e32 v17, 16, v2
	v_and_b32_e32 v2, 0xffff0000, v2
	v_mul_f32_e32 v2, v2, v2
	v_fmac_f32_e32 v2, v17, v17
	v_add_f32_e32 v2, v2, v16
	v_lshlrev_b32_e32 v16, 16, v3
	v_and_b32_e32 v3, 0xffff0000, v3
	v_mul_f32_e32 v3, v3, v3
	v_fmac_f32_e32 v3, v16, v16
	v_add_f32_e32 v2, v3, v2
	v_lshlrev_b32_e32 v3, 16, v4
	v_and_b32_e32 v4, 0xffff0000, v4
	v_mul_f32_e32 v4, v4, v4
	v_fmac_f32_e32 v4, v3, v3
	v_add_f32_e32 v2, v4, v2
	v_and_b32_e32 v4, 0xffff0000, v5
	v_lshlrev_b32_e32 v3, 16, v5
	v_mul_f32_e32 v4, v4, v4
	v_fmac_f32_e32 v4, v3, v3
	v_add_f32_e32 v2, v4, v2
	s_waitcnt lgkmcnt(0)
	v_and_b32_e32 v4, 0xffff0000, v6
	v_lshlrev_b32_e32 v3, 16, v6
	v_mul_f32_e32 v4, v4, v4
	v_fmac_f32_e32 v4, v3, v3
	v_add_f32_e32 v2, v4, v2
	v_and_b32_e32 v4, 0xffff0000, v7
	v_lshlrev_b32_e32 v3, 16, v7
	v_mul_f32_e32 v4, v4, v4
	v_fmac_f32_e32 v4, v3, v3
	v_add_f32_e32 v2, v4, v2
	v_and_b32_e32 v4, 0xffff0000, v8
	v_lshlrev_b32_e32 v3, 16, v8
	v_mul_f32_e32 v4, v4, v4
	v_fmac_f32_e32 v4, v3, v3
	v_and_b32_e32 v3, 0xffff0000, v9
	v_add_f32_e32 v6, v4, v2
	v_lshlrev_b32_e32 v2, 16, v9
	v_mul_f32_e32 v7, v3, v3
	v_fmac_f32_e32 v7, v2, v2
	v_or_b32_e32 v2, 0x60, v13
	v_xad_u32 v2, v2, v14, v15
	ds_read_b128 v[2:5], v2
	v_add_f32_e32 v16, v7, v6
	v_or_b32_e32 v6, 0x70, v13
	v_xad_u32 v6, v6, v14, v15
	ds_read_b128 v[6:9], v6
	s_waitcnt lgkmcnt(1)
	v_lshlrev_b32_e32 v13, 16, v2
	v_and_b32_e32 v2, 0xffff0000, v2
	v_mul_f32_e32 v2, v2, v2
	v_fmac_f32_e32 v2, v13, v13
	v_lshlrev_b32_e32 v13, 16, v3
	v_and_b32_e32 v3, 0xffff0000, v3
	v_mul_f32_e32 v3, v3, v3
	v_add_f32_e32 v2, v2, v16
	v_fmac_f32_e32 v3, v13, v13
	v_add_f32_e32 v2, v3, v2
	v_lshlrev_b32_e32 v3, 16, v4
	v_and_b32_e32 v4, 0xffff0000, v4
	v_mul_f32_e32 v4, v4, v4
	v_fmac_f32_e32 v4, v3, v3
	v_add_f32_e32 v2, v4, v2
	v_and_b32_e32 v4, 0xffff0000, v5
	v_lshlrev_b32_e32 v3, 16, v5
	v_mul_f32_e32 v4, v4, v4
	v_fmac_f32_e32 v4, v3, v3
	v_add_f32_e32 v13, v4, v2
	s_waitcnt lgkmcnt(0)
	v_and_b32_e32 v5, 0xffff0000, v7
	v_and_b32_e32 v4, 0xffff0000, v6
	v_lshlrev_b32_e32 v3, 16, v7
	v_lshlrev_b32_e32 v2, 16, v6
	v_pk_mul_f32 v[4:5], v[4:5], v[4:5]
	v_mov_b32_e32 v206, 0
	v_pk_fma_f32 v[2:3], v[2:3], v[2:3], v[4:5]
	v_and_b32_e32 v5, 0xffff0000, v9
	v_add_f32_e32 v2, v2, v13
	v_and_b32_e32 v4, 0xffff0000, v8
	v_add_f32_e32 v6, v3, v2
	v_lshlrev_b32_e32 v3, 16, v9
	v_lshlrev_b32_e32 v2, 16, v8
	v_pk_mul_f32 v[4:5], v[4:5], v[4:5]
	s_mov_b32 s72, 0
	v_pk_fma_f32 v[2:3], v[2:3], v[2:3], v[4:5]
	v_mov_b32_e32 v7, v163
	v_add_f32_e32 v2, v2, v6
	v_add_f32_e32 v2, v3, v2
	v_cndmask_b32_e32 v3, v11, v10, vcc
	v_mul_f32_e32 v2, v3, v2
	v_mul_f32_e32 v3, 0x4f800000, v2
	v_cmp_gt_f32_e32 vcc, s45, v2
	v_mov_b32_e32 v6, v163
	v_mov_b32_e32 v8, v163
	v_cndmask_b32_e32 v2, v2, v3, vcc
	v_sqrt_f32_e32 v3, v2
	v_mov_b32_e32 v9, v163
	v_mov_b32_e32 v10, v163
	v_mov_b32_e32 v11, v163
	v_add_u32_e32 v4, -1, v3
	v_fma_f32 v5, -v4, v3, v2
	v_cmp_ge_f32_e64 s[4:5], 0, v5
	v_add_u32_e32 v5, 1, v3
	v_mov_b32_e32 v12, v163
	v_cndmask_b32_e64 v4, v3, v4, s[4:5]
	v_fma_f32 v3, -v5, v3, v2
	v_cmp_lt_f32_e64 s[4:5], 0, v3
	v_mov_b32_e32 v13, v163
	v_mov_b32_e32 v14, v163
	v_cndmask_b32_e64 v3, v4, v5, s[4:5]
	v_mul_f32_e32 v4, 0x37800000, v3
	v_cndmask_b32_e32 v3, v3, v4, vcc
	v_cmp_class_f32_e32 vcc, v2, v200
	v_mov_b32_e32 v4, v163
	v_mov_b32_e32 v5, v163
	v_cndmask_b32_e32 v2, v3, v2, vcc
	v_mov_b32_e32 v3, v2
	s_nop 1
	v_permlane32_swap_b32_e32 v2, v3
	v_fmamk_f32 v2, v2, 0x3f8147ae, v201
	v_max_f32_e32 v204, 0, v2
	v_fmamk_f32 v2, v3, 0x3f8147ae, v201
	v_max_f32_e32 v205, 0, v2
	v_cmp_eq_f32_e32 vcc, 0, v204
	v_cmp_eq_f32_e64 s[4:5], 0, v205
	s_and_b64 s[4:5], vcc, s[4:5]
	v_mov_b32_e32 v3, v163
	v_cndmask_b32_e64 v2, 0, 1, s[4:5]
	v_cmp_ne_u32_e32 vcc, 0, v2
	s_cmp_eq_u64 vcc, exec
	s_cselect_b64 s[4:5], -1, 0
	v_cndmask_b32_e64 v2, 0, 1, s[4:5]
	v_mov_b32_e32 v15, v163
	v_readfirstlane_b32 s4, v2
	s_bitcmp1_b32 s4, 0
	s_cselect_b64 s[4:5], -1, 0
	s_xor_b64 s[4:5], s[4:5], -1
	v_cndmask_b32_e64 v208, 0, 1, s[4:5]
	s_addk_i32 s68, 0xff00
	s_or_b32 s69, s65, 0x1400
	v_mov_b32_e32 v2, 0
	v_mov_b32_e32 v16, v163
	v_mov_b32_e32 v17, v163
	v_mov_b32_e32 v18, 0
	v_mov_b32_e32 v19, v163
	v_mov_b32_e32 v20, v163
	v_mov_b32_e32 v21, v163
	v_mov_b32_e32 v22, v163
	v_mov_b32_e32 v23, v163
	v_mov_b32_e32 v24, v163
	v_mov_b32_e32 v25, v163
	v_mov_b32_e32 v26, v163
	v_mov_b32_e32 v27, v163
	v_mov_b32_e32 v28, v163
	v_mov_b32_e32 v29, v163
	v_mov_b32_e32 v30, v163
	v_mov_b32_e32 v31, v163
	v_mov_b32_e32 v32, v163
	v_mov_b32_e32 v33, v163
	v_mov_b32_e32 v34, 0
	v_mov_b32_e32 v35, v163
	v_mov_b32_e32 v36, v163
	v_mov_b32_e32 v37, v163
	v_mov_b32_e32 v38, v163
	v_mov_b32_e32 v39, v163
	v_mov_b32_e32 v40, v163
	v_mov_b32_e32 v41, v163
	v_mov_b32_e32 v42, v163
	v_mov_b32_e32 v43, v163
	v_mov_b32_e32 v44, v163
	v_mov_b32_e32 v45, v163
	v_mov_b32_e32 v46, v163
	v_mov_b32_e32 v47, v163
	v_mov_b32_e32 v48, v163
	v_mov_b32_e32 v49, v163
	v_mov_b32_e32 v50, 0
	v_mov_b32_e32 v51, v163
	v_mov_b32_e32 v52, v163
	v_mov_b32_e32 v53, v163
	v_mov_b32_e32 v54, v163
	v_mov_b32_e32 v55, v163
	v_mov_b32_e32 v56, v163
	v_mov_b32_e32 v57, v163
	v_mov_b32_e32 v58, v163
	v_mov_b32_e32 v59, v163
	v_mov_b32_e32 v60, v163
	v_mov_b32_e32 v61, v163
	v_mov_b32_e32 v62, v163
	v_mov_b32_e32 v63, v163
	v_mov_b32_e32 v64, v163
	v_mov_b32_e32 v65, v163
	v_mov_b32_e32 v82, 0
	v_mov_b32_e32 v83, v163
	v_mov_b32_e32 v84, v163
	v_mov_b32_e32 v85, v163
	v_mov_b32_e32 v86, v163
	v_mov_b32_e32 v87, v163
	v_mov_b32_e32 v88, v163
	v_mov_b32_e32 v89, v163
	v_mov_b32_e32 v90, v163
	v_mov_b32_e32 v91, v163
	v_mov_b32_e32 v92, v163
	v_mov_b32_e32 v93, v163
	v_mov_b32_e32 v94, v163
	v_mov_b32_e32 v95, v163
	v_mov_b32_e32 v96, v163
	v_mov_b32_e32 v97, v163
	v_mov_b32_e32 v66, 0
	v_mov_b32_e32 v67, v163
	v_mov_b32_e32 v68, v163
	v_mov_b32_e32 v69, v163
	v_mov_b32_e32 v70, v163
	v_mov_b32_e32 v71, v163
	v_mov_b32_e32 v72, v163
	v_mov_b32_e32 v73, v163
	v_mov_b32_e32 v74, v163
	v_mov_b32_e32 v75, v163
	v_mov_b32_e32 v76, v163
	v_mov_b32_e32 v77, v163
	v_mov_b32_e32 v78, v163
	v_mov_b32_e32 v79, v163
	v_mov_b32_e32 v80, v163
	v_mov_b32_e32 v81, v163
	v_mov_b32_e32 v98, 0
	v_mov_b32_e32 v99, v163
	v_mov_b32_e32 v100, v163
	v_mov_b32_e32 v101, v163
	v_mov_b32_e32 v102, v163
	v_mov_b32_e32 v103, v163
	v_mov_b32_e32 v104, v163
	v_mov_b32_e32 v105, v163
	v_mov_b32_e32 v106, v163
	v_mov_b32_e32 v107, v163
	v_mov_b32_e32 v108, v163
	v_mov_b32_e32 v109, v163
	v_mov_b32_e32 v110, v163
	v_mov_b32_e32 v111, v163
	v_mov_b32_e32 v112, v163
	v_mov_b32_e32 v113, v163
	v_mov_b32_e32 v114, 0
	v_mov_b32_e32 v115, v163
	v_mov_b32_e32 v116, v163
	v_mov_b32_e32 v117, v163
	v_mov_b32_e32 v118, v163
	v_mov_b32_e32 v119, v163
	v_mov_b32_e32 v120, v163
	v_mov_b32_e32 v121, v163
	v_mov_b32_e32 v122, v163
	v_mov_b32_e32 v123, v163
	v_mov_b32_e32 v124, v163
	v_mov_b32_e32 v125, v163
	v_mov_b32_e32 v126, v163
	v_mov_b32_e32 v127, v163
	v_mov_b32_e32 v128, v163
	v_mov_b32_e32 v129, v163
	v_readfirstlane_b32 s4, v208
	s_nop 3
	s_cmp_lg_u32 s4, 0
	s_cbranch_scc1 .LBB0_640
	s_mul_i32 s4, s79, 0x700
	s_add_i32 s4, s4, 0x20800
	v_lshl_add_u32 v250, v196, 2, s4
	ds_write_b32 v250, v162 offset:0
	ds_write_b32 v250, v164 offset:256
	ds_write_b32 v250, v166 offset:512
	ds_write_b32 v250, v168 offset:768
	ds_write_b32 v250, v170 offset:1024
	ds_write_b32 v250, v172 offset:1280
	ds_write_b32 v250, v174 offset:1536
	v_add_u32_e32 v178, s24, v180
	v_add_u32_e32 v179, s24, v182
	v_add_u32_e32 v181, s24, v184
	v_add_u32_e32 v183, s24, v186
	v_add_u32_e32 v251, s24, v188
	v_add_u32_e32 v174, s24, v190
	v_add_u32_e32 v175, s24, v192
	v_add_u32_e32 v203, s24, v194
	v_mov_b32_e32 v130, v196
	v_ashrrev_i32_e32 v131, 4, v130
	v_and_b32_e32 v132, 15, v130
	v_add_u32_e32 v136, s25, v131
	v_bitop3_b32 v137, v136, v132, 15 bitop3:0x6c
	v_mul_lo_u32 v136, v136, s44
	v_ashrrev_i32_e32 v133, 5, v130
	v_add_u32_e32 v136, s67, v136
	v_lshlrev_b32_e32 v137, 4, v137
	v_lshl_or_b32 v136, v136, 1, v137
	v_add_u32_e32 v137, s26, v133
	v_bfe_u32 v134, v130, 2, 2
	v_lshrrev_b32_e32 v135, 1, v130
	v_lshlrev_b32_e32 v138, 1, v137
	v_and_or_b32 v134, v135, 8, v134
	v_lshlrev_b32_e32 v135, 3, v130
	v_and_b32_e32 v138, 0xfffff0, v138
	v_and_b32_e32 v137, 4, v137
	v_and_b32_e32 v135, 24, v135
	v_or3_b32 v137, v137, v138, v134
	v_and_b32_e32 v130, 0x60, v130
	v_mul_u32_u24_e32 v137, 0x1900, v137
	v_or3_b32 v130, s69, v130, v135
	v_add_lshl_u32 v130, v130, v137, 1
	v_mov_b32_e32 v185, v136
	v_mov_b32_e32 v187, v130
	v_add_u32_e32 v130, s28, v131
	v_mul_lo_u32 v131, v130, s44
	v_bitop3_b32 v130, v130, v132, 15 bitop3:0x6c
	v_add_u32_e32 v131, s67, v131
	v_lshlrev_b32_e32 v130, 4, v130
	v_lshl_or_b32 v130, v131, 1, v130
	v_mov_b32_e32 v189, v130
	v_add_u32_e32 v131, s29, v133
	v_lshlrev_b32_e32 v132, 1, v131
	v_and_b32_e32 v132, 0xfffff0, v132
	v_and_b32_e32 v133, 4, v131
	v_lshlrev_b32_e32 v131, 5, v131
	v_or3_b32 v132, v133, v132, v134
	v_and_b32_e32 v131, 0x60, v131
	v_mul_u32_u24_e32 v132, 0x1900, v132
	v_or3_b32 v131, s69, v131, v135
	v_add_lshl_u32 v131, v131, v132, 1
	v_mov_b32_e32 v191, v131
	v_mov_b32_e32 v193, 0
	v_mov_b32_e32 v209, 0
	s_waitcnt lgkmcnt(0)
.Lfa_loop:
	ds_read_b128 v[162:165], v180 offset:32768
	ds_read_b128 v[170:173], v178 offset:0
	ds_read_b128 v[166:169], v180 offset:40960
	ds_read_b128 v[242:245], v182 offset:32768
	ds_read_b128 v[214:217], v179 offset:0
	ds_read_b128 v[210:213], v182 offset:40960
	ds_read_b128 v[218:221], v184 offset:32768
	ds_read_b128 v[226:229], v181 offset:0
	ds_read_b128 v[222:225], v184 offset:40960
	ds_read_b128 v[230:233], v186 offset:32768
	ds_read_b128 v[238:241], v183 offset:0
	ds_read_b128 v[234:237], v186 offset:40960
	s_waitcnt lgkmcnt(10)
	v_mfma_f32_32x32x16_bf16 v[146:161], v[162:165], v[170:173], 0
	s_waitcnt lgkmcnt(9)
	v_mfma_f32_32x32x16_bf16 v[130:145], v[166:169], v[170:173], 0
	ds_read_b128 v[162:165], v188 offset:32768
	ds_read_b128 v[170:173], v251 offset:0
	ds_read_b128 v[166:169], v188 offset:40960
	s_cmpk_eq_i32 s72, 0x43
	s_cbranch_scc1 .Lfa_skip0
	s_cmp_lt_u32 s72, 3
	s_cselect_b32 s5, s66, s68
	s_add_i32 s5, s5, s71
	s_mul_hi_i32 s19, s5, 0x3200
	s_mulk_i32 s5, 0x3200
	s_add_u32 s18, s20, s5
	s_addc_u32 s19, s21, s19
	s_add_i32 s75, s27, 0x4000
	s_add_i32 s5, s30, 0x4000
	s_add_i32 m0, s75, 0x8000
	s_nop 0
	global_load_lds_dwordx4 v185, s[18:19]
	s_mov_b32 m0, s75
	s_nop 0
	global_load_lds_dwordx4 v187, s[18:19]
	s_add_i32 m0, s5, 0x8000
	s_nop 0
	global_load_lds_dwordx4 v189, s[18:19]
	s_mov_b32 m0, s5
	s_nop 0
	global_load_lds_dwordx4 v191, s[18:19]
.Lfa_skip0:
	s_waitcnt lgkmcnt(10)
	v_mfma_f32_32x32x16_bf16 v[146:161], v[242:245], v[214:217], v[146:161]
	s_waitcnt lgkmcnt(9)
	v_mfma_f32_32x32x16_bf16 v[130:145], v[210:213], v[214:217], v[130:145]
	ds_read_b128 v[242:245], v190 offset:32768
	ds_read_b128 v[198:201], v174 offset:0
	ds_read_b128 v[246:249], v190 offset:40960
	s_waitcnt lgkmcnt(10)
	v_mfma_f32_32x32x16_bf16 v[146:161], v[218:221], v[226:229], v[146:161]
	s_waitcnt lgkmcnt(9)
	v_mfma_f32_32x32x16_bf16 v[130:145], v[222:225], v[226:229], v[130:145]
	s_waitcnt lgkmcnt(7)
	v_mfma_f32_32x32x16_bf16 v[146:161], v[230:233], v[238:241], v[146:161]
	s_waitcnt lgkmcnt(6)
	v_mfma_f32_32x32x16_bf16 v[130:145], v[234:237], v[238:241], v[130:145]
	s_waitcnt lgkmcnt(4)
	v_mfma_f32_32x32x16_bf16 v[210:225], v[162:165], v[170:173], 0
	s_waitcnt lgkmcnt(3)
	v_mfma_f32_32x32x16_bf16 v[226:241], v[166:169], v[170:173], 0
	ds_read_b128 v[162:165], v192 offset:32768
	ds_read_b128 v[170:173], v175 offset:0
	ds_read_b128 v[166:169], v192 offset:40960
	s_waitcnt lgkmcnt(4)
	v_mfma_f32_32x32x16_bf16 v[210:225], v[242:245], v[198:201], v[210:225]
	s_nop 0
	v_exp_f32_e32 v146, v146
	v_exp_f32_e32 v147, v147
	v_exp_f32_e32 v148, v148
	v_exp_f32_e32 v149, v149
	v_exp_f32_e32 v150, v150
	v_exp_f32_e32 v151, v151
	s_waitcnt lgkmcnt(3)
	v_mfma_f32_32x32x16_bf16 v[226:241], v[246:249], v[198:201], v[226:241]
	ds_read_b128 v[242:245], v194 offset:32768
	ds_read_b128 v[198:201], v203 offset:0
	ds_read_b128 v[246:249], v194 offset:40960
	v_exp_f32_e32 v152, v152
	v_exp_f32_e32 v153, v153
	v_add_f32_e32 v207, v207, v146
	v_add_f32_e32 v193, v193, v147
	v_add_f32_e32 v207, v207, v148
	v_add_f32_e32 v193, v193, v149
	s_waitcnt lgkmcnt(4)
	v_mfma_f32_32x32x16_bf16 v[210:225], v[162:165], v[170:173], v[210:225]
	v_add_f32_e32 v207, v207, v150
	v_add_f32_e32 v193, v193, v151
	v_add_f32_e32 v207, v207, v152
	v_add_f32_e32 v193, v193, v153
	v_cvt_pk_bf16_f32 v146, v146, v147
	v_cvt_pk_bf16_f32 v147, v148, v149
	s_waitcnt lgkmcnt(3)
	v_mfma_f32_32x32x16_bf16 v[226:241], v[166:169], v[170:173], v[226:241]
	v_cvt_pk_bf16_f32 v148, v150, v151
	v_cvt_pk_bf16_f32 v149, v152, v153
	ds_read_b64_tr_b16 v[162:163], v195 offset:0
	ds_read_b64_tr_b16 v[164:165], v195 offset:2048
	ds_read_b64_tr_b16 v[166:167], v195 offset:512
	ds_read_b64_tr_b16 v[168:169], v195 offset:2560
	ds_read_b64_tr_b16 v[170:171], v195 offset:1024
	ds_read_b64_tr_b16 v[172:173], v195 offset:3072
	v_permlane32_swap_b32_e32 v146, v148
	v_permlane32_swap_b32_e32 v147, v149
	s_waitcnt lgkmcnt(7)
	v_mfma_f32_32x32x16_bf16 v[210:225], v[242:245], v[198:201], v[210:225]
	s_waitcnt lgkmcnt(6)
	v_mfma_f32_32x32x16_bf16 v[226:241], v[246:249], v[198:201], v[226:241]
	ds_read_b64_tr_b16 v[242:243], v195 offset:1536
	ds_read_b64_tr_b16 v[244:245], v195 offset:3584
	ds_read_b64_tr_b16 v[246:247], v195 offset:4096
	ds_read_b64_tr_b16 v[248:249], v195 offset:6144
	ds_read_b64_tr_b16 v[198:199], v195 offset:4608
	ds_read_b64_tr_b16 v[200:201], v195 offset:6656
	s_nop 3
	v_exp_f32_e32 v210, v210
	v_exp_f32_e32 v211, v211
	v_exp_f32_e32 v212, v212
	v_exp_f32_e32 v213, v213
	v_exp_f32_e32 v214, v214
	v_exp_f32_e32 v215, v215
	v_exp_f32_e32 v216, v216
	v_exp_f32_e32 v217, v217
	v_add_f32_e32 v206, v206, v210
	v_add_f32_e32 v209, v209, v211
	v_add_f32_e32 v206, v206, v212
	v_add_f32_e32 v209, v209, v213
	v_add_f32_e32 v206, v206, v214
	v_add_f32_e32 v209, v209, v215
	v_add_f32_e32 v206, v206, v216
	v_add_f32_e32 v209, v209, v217
	v_cvt_pk_bf16_f32 v210, v210, v211
	v_cvt_pk_bf16_f32 v211, v212, v213
	v_cvt_pk_bf16_f32 v212, v214, v215
	v_cvt_pk_bf16_f32 v213, v216, v217
	s_nop 1
	v_permlane32_swap_b32_e32 v210, v212
	v_permlane32_swap_b32_e32 v211, v213
	s_waitcnt lgkmcnt(10)
	v_mfma_f32_32x32x16_bf16 v[82:97], v[146:149], v[162:165], v[82:97]
	v_exp_f32_e32 v154, v154
	v_exp_f32_e32 v155, v155
	v_exp_f32_e32 v156, v156
	v_exp_f32_e32 v157, v157
	v_exp_f32_e32 v158, v158
	v_exp_f32_e32 v159, v159
	v_mfma_f32_32x32x16_bf16 v[50:65], v[210:213], v[162:165], v[50:65]
	v_exp_f32_e32 v160, v160
	v_exp_f32_e32 v161, v161
	v_add_f32_e32 v207, v207, v154
	v_add_f32_e32 v193, v193, v155
	v_add_f32_e32 v207, v207, v156
	v_add_f32_e32 v193, v193, v157
	ds_read_b64_tr_b16 v[162:163], v195 offset:5120
	ds_read_b64_tr_b16 v[164:165], v195 offset:7168
	s_waitcnt lgkmcnt(10)
	v_mfma_f32_32x32x16_bf16 v[66:81], v[146:149], v[166:169], v[66:81]
	v_add_f32_e32 v207, v207, v158
	v_add_f32_e32 v193, v193, v159
	v_add_f32_e32 v207, v207, v160
	v_add_f32_e32 v193, v193, v161
	v_cvt_pk_bf16_f32 v154, v154, v155
	v_cvt_pk_bf16_f32 v155, v156, v157
	v_mfma_f32_32x32x16_bf16 v[34:49], v[210:213], v[166:169], v[34:49]
	v_cvt_pk_bf16_f32 v156, v158, v159
	v_cvt_pk_bf16_f32 v157, v160, v161
	ds_read_b64_tr_b16 v[166:167], v195 offset:5632
	ds_read_b64_tr_b16 v[168:169], v195 offset:7680
	v_permlane32_swap_b32_e32 v154, v156
	v_permlane32_swap_b32_e32 v155, v157
	s_waitcnt lgkmcnt(10)
	v_mfma_f32_32x32x16_bf16 v[98:113], v[146:149], v[170:173], v[98:113]
	v_exp_f32_e32 v218, v218
	v_exp_f32_e32 v219, v219
	v_exp_f32_e32 v220, v220
	v_exp_f32_e32 v221, v221
	v_exp_f32_e32 v222, v222
	v_exp_f32_e32 v223, v223
	v_mfma_f32_32x32x16_bf16 v[18:33], v[210:213], v[170:173], v[18:33]
	v_exp_f32_e32 v224, v224
	v_exp_f32_e32 v225, v225
	v_add_f32_e32 v206, v206, v218
	v_add_f32_e32 v209, v209, v219
	v_add_f32_e32 v206, v206, v220
	v_add_f32_e32 v209, v209, v221
	ds_read_b64_tr_b16 v[170:171], v195 offset:8192
	ds_read_b64_tr_b16 v[172:173], v195 offset:10240
	s_waitcnt lgkmcnt(10)
	v_mfma_f32_32x32x16_bf16 v[114:129], v[146:149], v[242:245], v[114:129]
	v_add_f32_e32 v206, v206, v222
	v_add_f32_e32 v209, v209, v223
	v_add_f32_e32 v206, v206, v224
	v_add_f32_e32 v209, v209, v225
	v_cvt_pk_bf16_f32 v218, v218, v219
	v_cvt_pk_bf16_f32 v219, v220, v221
	v_mfma_f32_32x32x16_bf16 v[2:17], v[210:213], v[242:245], v[2:17]
	v_cvt_pk_bf16_f32 v220, v222, v223
	v_cvt_pk_bf16_f32 v221, v224, v225
	ds_read_b64_tr_b16 v[242:243], v195 offset:8704
	ds_read_b64_tr_b16 v[244:245], v195 offset:10752
	v_permlane32_swap_b32_e32 v218, v220
	v_permlane32_swap_b32_e32 v219, v221
	s_waitcnt lgkmcnt(10)
	v_mfma_f32_32x32x16_bf16 v[82:97], v[154:157], v[246:249], v[82:97]
	v_exp_f32_e32 v130, v130
	v_exp_f32_e32 v131, v131
	v_exp_f32_e32 v132, v132
	v_exp_f32_e32 v133, v133
	v_exp_f32_e32 v134, v134
	v_exp_f32_e32 v135, v135
	v_mfma_f32_32x32x16_bf16 v[50:65], v[218:221], v[246:249], v[50:65]
	v_exp_f32_e32 v136, v136
	v_exp_f32_e32 v137, v137
	v_add_f32_e32 v207, v207, v130
	v_add_f32_e32 v193, v193, v131
	v_add_f32_e32 v207, v207, v132
	v_add_f32_e32 v193, v193, v133
	ds_read_b64_tr_b16 v[246:247], v195 offset:9216
	ds_read_b64_tr_b16 v[248:249], v195 offset:11264
	s_waitcnt lgkmcnt(10)
	v_mfma_f32_32x32x16_bf16 v[66:81], v[154:157], v[198:201], v[66:81]
	v_add_f32_e32 v207, v207, v134
	v_add_f32_e32 v193, v193, v135
	v_add_f32_e32 v207, v207, v136
	v_add_f32_e32 v193, v193, v137
	v_cvt_pk_bf16_f32 v130, v130, v131
	v_cvt_pk_bf16_f32 v131, v132, v133
	v_mfma_f32_32x32x16_bf16 v[34:49], v[218:221], v[198:201], v[34:49]
	v_cvt_pk_bf16_f32 v132, v134, v135
	v_cvt_pk_bf16_f32 v133, v136, v137
	ds_read_b64_tr_b16 v[198:199], v195 offset:9728
	ds_read_b64_tr_b16 v[200:201], v195 offset:11776
	v_permlane32_swap_b32_e32 v130, v132
	v_permlane32_swap_b32_e32 v131, v133
	s_waitcnt lgkmcnt(10)
	v_mfma_f32_32x32x16_bf16 v[98:113], v[154:157], v[162:165], v[98:113]
	v_exp_f32_e32 v226, v226
	v_exp_f32_e32 v227, v227
	v_exp_f32_e32 v228, v228
	v_exp_f32_e32 v229, v229
	v_exp_f32_e32 v230, v230
	v_exp_f32_e32 v231, v231
	v_mfma_f32_32x32x16_bf16 v[18:33], v[218:221], v[162:165], v[18:33]
	v_exp_f32_e32 v232, v232
	v_exp_f32_e32 v233, v233
	v_add_f32_e32 v206, v206, v226
	v_add_f32_e32 v209, v209, v227
	v_add_f32_e32 v206, v206, v228
	v_add_f32_e32 v209, v209, v229
	ds_read_b64_tr_b16 v[162:163], v195 offset:12288
	ds_read_b64_tr_b16 v[164:165], v195 offset:14336
	s_waitcnt lgkmcnt(10)
	v_mfma_f32_32x32x16_bf16 v[114:129], v[154:157], v[166:169], v[114:129]
	v_add_f32_e32 v206, v206, v230
	v_add_f32_e32 v209, v209, v231
	v_add_f32_e32 v206, v206, v232
	v_add_f32_e32 v209, v209, v233
	v_cvt_pk_bf16_f32 v226, v226, v227
	v_cvt_pk_bf16_f32 v227, v228, v229
	v_mfma_f32_32x32x16_bf16 v[2:17], v[218:221], v[166:169], v[2:17]
	v_cvt_pk_bf16_f32 v228, v230, v231
	v_cvt_pk_bf16_f32 v229, v232, v233
	ds_read_b64_tr_b16 v[166:167], v195 offset:12800
	ds_read_b64_tr_b16 v[168:169], v195 offset:14848
	v_permlane32_swap_b32_e32 v226, v228
	v_permlane32_swap_b32_e32 v227, v229
	s_waitcnt lgkmcnt(10)
	v_mfma_f32_32x32x16_bf16 v[82:97], v[130:133], v[170:173], v[82:97]
	v_exp_f32_e32 v138, v138
	v_exp_f32_e32 v139, v139
	v_exp_f32_e32 v140, v140
	v_exp_f32_e32 v141, v141
	v_exp_f32_e32 v142, v142
	v_exp_f32_e32 v143, v143
	v_mfma_f32_32x32x16_bf16 v[50:65], v[226:229], v[170:173], v[50:65]
	v_exp_f32_e32 v144, v144
	v_exp_f32_e32 v145, v145
	v_add_f32_e32 v207, v207, v138
	v_add_f32_e32 v193, v193, v139
	v_add_f32_e32 v207, v207, v140
	v_add_f32_e32 v193, v193, v141
	ds_read_b64_tr_b16 v[170:171], v195 offset:13312
	ds_read_b64_tr_b16 v[172:173], v195 offset:15360
	s_waitcnt lgkmcnt(10)
	v_mfma_f32_32x32x16_bf16 v[66:81], v[130:133], v[242:245], v[66:81]
	v_add_f32_e32 v207, v207, v142
	v_add_f32_e32 v193, v193, v143
	v_add_f32_e32 v207, v207, v144
	v_add_f32_e32 v193, v193, v145
	v_cvt_pk_bf16_f32 v138, v138, v139
	v_cvt_pk_bf16_f32 v139, v140, v141
	v_mfma_f32_32x32x16_bf16 v[34:49], v[226:229], v[242:245], v[34:49]
	v_cvt_pk_bf16_f32 v140, v142, v143
	v_cvt_pk_bf16_f32 v141, v144, v145
	ds_read_b64_tr_b16 v[242:243], v195 offset:13824
	ds_read_b64_tr_b16 v[244:245], v195 offset:15872
	v_permlane32_swap_b32_e32 v138, v140
	v_permlane32_swap_b32_e32 v139, v141
	s_waitcnt lgkmcnt(10)
	v_mfma_f32_32x32x16_bf16 v[98:113], v[130:133], v[246:249], v[98:113]
	v_exp_f32_e32 v234, v234
	v_exp_f32_e32 v235, v235
	v_exp_f32_e32 v236, v236
	v_exp_f32_e32 v237, v237
	v_exp_f32_e32 v238, v238
	v_exp_f32_e32 v239, v239
	v_mfma_f32_32x32x16_bf16 v[18:33], v[226:229], v[246:249], v[18:33]
	v_exp_f32_e32 v240, v240
	v_exp_f32_e32 v241, v241
	v_add_f32_e32 v206, v206, v234
	v_add_f32_e32 v209, v209, v235
	v_add_f32_e32 v206, v206, v236
	v_add_f32_e32 v209, v209, v237
	s_waitcnt lgkmcnt(8)
	v_mfma_f32_32x32x16_bf16 v[114:129], v[130:133], v[198:201], v[114:129]
	v_add_f32_e32 v206, v206, v238
	v_add_f32_e32 v209, v209, v239
	v_add_f32_e32 v206, v206, v240
	v_add_f32_e32 v209, v209, v241
	v_cvt_pk_bf16_f32 v234, v234, v235
	v_cvt_pk_bf16_f32 v235, v236, v237
	v_mfma_f32_32x32x16_bf16 v[2:17], v[226:229], v[198:201], v[2:17]
	v_cvt_pk_bf16_f32 v236, v238, v239
	v_cvt_pk_bf16_f32 v237, v240, v241
	s_nop 1
	v_permlane32_swap_b32_e32 v234, v236
	v_permlane32_swap_b32_e32 v235, v237
	s_waitcnt lgkmcnt(6)
	v_mfma_f32_32x32x16_bf16 v[82:97], v[138:141], v[162:165], v[82:97]
	v_mfma_f32_32x32x16_bf16 v[50:65], v[234:237], v[162:165], v[50:65]
	s_waitcnt lgkmcnt(4)
	v_mfma_f32_32x32x16_bf16 v[66:81], v[138:141], v[166:169], v[66:81]
	v_mfma_f32_32x32x16_bf16 v[34:49], v[234:237], v[166:169], v[34:49]
	s_waitcnt lgkmcnt(2)
	v_mfma_f32_32x32x16_bf16 v[98:113], v[138:141], v[170:173], v[98:113]
	v_mfma_f32_32x32x16_bf16 v[18:33], v[234:237], v[170:173], v[18:33]
	s_waitcnt lgkmcnt(0)
	v_mfma_f32_32x32x16_bf16 v[114:129], v[138:141], v[242:245], v[114:129]
	v_mfma_f32_32x32x16_bf16 v[2:17], v[234:237], v[242:245], v[2:17]
	s_add_i32 s72, s72, 1
	s_add_i32 s71, s71, 64
	s_addk_i32 s70, 0x4000
	s_waitcnt vmcnt(0)
	s_barrier
	ds_read_b128 v[162:165], v180 offset:49152
	ds_read_b128 v[170:173], v178 offset:0
	ds_read_b128 v[166:169], v180 offset:57344
	ds_read_b128 v[242:245], v182 offset:49152
	ds_read_b128 v[214:217], v179 offset:0
	ds_read_b128 v[210:213], v182 offset:57344
	ds_read_b128 v[218:221], v184 offset:49152
	ds_read_b128 v[226:229], v181 offset:0
	ds_read_b128 v[222:225], v184 offset:57344
	ds_read_b128 v[230:233], v186 offset:49152
	ds_read_b128 v[238:241], v183 offset:0
	ds_read_b128 v[234:237], v186 offset:57344
	s_waitcnt lgkmcnt(10)
	v_mfma_f32_32x32x16_bf16 v[146:161], v[162:165], v[170:173], 0
	s_waitcnt lgkmcnt(9)
	v_mfma_f32_32x32x16_bf16 v[130:145], v[166:169], v[170:173], 0
	ds_read_b128 v[162:165], v188 offset:49152
	ds_read_b128 v[170:173], v251 offset:0
	ds_read_b128 v[166:169], v188 offset:57344
	s_cmpk_eq_i32 s72, 0x43
	s_cbranch_scc1 .Lfa_skip1
	s_cmp_lt_u32 s72, 3
	s_cselect_b32 s5, s66, s68
	s_add_i32 s5, s5, s71
	s_mul_hi_i32 s19, s5, 0x3200
	s_mulk_i32 s5, 0x3200
	s_add_u32 s18, s20, s5
	s_addc_u32 s19, s21, s19
	s_add_i32 s75, s27, 0x0
	s_add_i32 s5, s30, 0x0
	s_add_i32 m0, s75, 0x8000
	s_nop 0
	global_load_lds_dwordx4 v185, s[18:19]
	s_mov_b32 m0, s75
	s_nop 0
	global_load_lds_dwordx4 v187, s[18:19]
	s_add_i32 m0, s5, 0x8000
	s_nop 0
	global_load_lds_dwordx4 v189, s[18:19]
	s_mov_b32 m0, s5
	s_nop 0
	global_load_lds_dwordx4 v191, s[18:19]
.Lfa_skip1:
	s_waitcnt lgkmcnt(10)
	v_mfma_f32_32x32x16_bf16 v[146:161], v[242:245], v[214:217], v[146:161]
	s_waitcnt lgkmcnt(9)
	v_mfma_f32_32x32x16_bf16 v[130:145], v[210:213], v[214:217], v[130:145]
	ds_read_b128 v[242:245], v190 offset:49152
	ds_read_b128 v[198:201], v174 offset:0
	ds_read_b128 v[246:249], v190 offset:57344
	s_waitcnt lgkmcnt(10)
	v_mfma_f32_32x32x16_bf16 v[146:161], v[218:221], v[226:229], v[146:161]
	s_waitcnt lgkmcnt(9)
	v_mfma_f32_32x32x16_bf16 v[130:145], v[222:225], v[226:229], v[130:145]
	s_waitcnt lgkmcnt(7)
	v_mfma_f32_32x32x16_bf16 v[146:161], v[230:233], v[238:241], v[146:161]
	s_waitcnt lgkmcnt(6)
	v_mfma_f32_32x32x16_bf16 v[130:145], v[234:237], v[238:241], v[130:145]
	s_waitcnt lgkmcnt(4)
	v_mfma_f32_32x32x16_bf16 v[210:225], v[162:165], v[170:173], 0
	s_waitcnt lgkmcnt(3)
	v_mfma_f32_32x32x16_bf16 v[226:241], v[166:169], v[170:173], 0
	ds_read_b128 v[162:165], v192 offset:49152
	ds_read_b128 v[170:173], v175 offset:0
	ds_read_b128 v[166:169], v192 offset:57344
	s_waitcnt lgkmcnt(4)
	v_mfma_f32_32x32x16_bf16 v[210:225], v[242:245], v[198:201], v[210:225]
	s_nop 0
	v_exp_f32_e32 v146, v146
	v_exp_f32_e32 v147, v147
	v_exp_f32_e32 v148, v148
	v_exp_f32_e32 v149, v149
	v_exp_f32_e32 v150, v150
	v_exp_f32_e32 v151, v151
	s_waitcnt lgkmcnt(3)
	v_mfma_f32_32x32x16_bf16 v[226:241], v[246:249], v[198:201], v[226:241]
	ds_read_b128 v[242:245], v194 offset:49152
	ds_read_b128 v[198:201], v203 offset:0
	ds_read_b128 v[246:249], v194 offset:57344
	v_exp_f32_e32 v152, v152
	v_exp_f32_e32 v153, v153
	v_add_f32_e32 v207, v207, v146
	v_add_f32_e32 v193, v193, v147
	v_add_f32_e32 v207, v207, v148
	v_add_f32_e32 v193, v193, v149
	s_waitcnt lgkmcnt(4)
	v_mfma_f32_32x32x16_bf16 v[210:225], v[162:165], v[170:173], v[210:225]
	v_add_f32_e32 v207, v207, v150
	v_add_f32_e32 v193, v193, v151
	v_add_f32_e32 v207, v207, v152
	v_add_f32_e32 v193, v193, v153
	v_cvt_pk_bf16_f32 v146, v146, v147
	v_cvt_pk_bf16_f32 v147, v148, v149
	s_waitcnt lgkmcnt(3)
	v_mfma_f32_32x32x16_bf16 v[226:241], v[166:169], v[170:173], v[226:241]
	v_cvt_pk_bf16_f32 v148, v150, v151
	v_cvt_pk_bf16_f32 v149, v152, v153
	ds_read_b64_tr_b16 v[162:163], v195 offset:16384
	ds_read_b64_tr_b16 v[164:165], v195 offset:18432
	ds_read_b64_tr_b16 v[166:167], v195 offset:16896
	ds_read_b64_tr_b16 v[168:169], v195 offset:18944
	ds_read_b64_tr_b16 v[170:171], v195 offset:17408
	ds_read_b64_tr_b16 v[172:173], v195 offset:19456
	v_permlane32_swap_b32_e32 v146, v148
	v_permlane32_swap_b32_e32 v147, v149
	s_waitcnt lgkmcnt(7)
	v_mfma_f32_32x32x16_bf16 v[210:225], v[242:245], v[198:201], v[210:225]
	s_waitcnt lgkmcnt(6)
	v_mfma_f32_32x32x16_bf16 v[226:241], v[246:249], v[198:201], v[226:241]
	ds_read_b64_tr_b16 v[242:243], v195 offset:17920
	ds_read_b64_tr_b16 v[244:245], v195 offset:19968
	ds_read_b64_tr_b16 v[246:247], v195 offset:20480
	ds_read_b64_tr_b16 v[248:249], v195 offset:22528
	ds_read_b64_tr_b16 v[198:199], v195 offset:20992
	ds_read_b64_tr_b16 v[200:201], v195 offset:23040
	s_nop 3
	v_exp_f32_e32 v210, v210
	v_exp_f32_e32 v211, v211
	v_exp_f32_e32 v212, v212
	v_exp_f32_e32 v213, v213
	v_exp_f32_e32 v214, v214
	v_exp_f32_e32 v215, v215
	v_exp_f32_e32 v216, v216
	v_exp_f32_e32 v217, v217
	v_add_f32_e32 v206, v206, v210
	v_add_f32_e32 v209, v209, v211
	v_add_f32_e32 v206, v206, v212
	v_add_f32_e32 v209, v209, v213
	v_add_f32_e32 v206, v206, v214
	v_add_f32_e32 v209, v209, v215
	v_add_f32_e32 v206, v206, v216
	v_add_f32_e32 v209, v209, v217
	v_cvt_pk_bf16_f32 v210, v210, v211
	v_cvt_pk_bf16_f32 v211, v212, v213
	v_cvt_pk_bf16_f32 v212, v214, v215
	v_cvt_pk_bf16_f32 v213, v216, v217
	s_nop 1
	v_permlane32_swap_b32_e32 v210, v212
	v_permlane32_swap_b32_e32 v211, v213
	s_waitcnt lgkmcnt(10)
	v_mfma_f32_32x32x16_bf16 v[82:97], v[146:149], v[162:165], v[82:97]
	v_exp_f32_e32 v154, v154
	v_exp_f32_e32 v155, v155
	v_exp_f32_e32 v156, v156
	v_exp_f32_e32 v157, v157
	v_exp_f32_e32 v158, v158
	v_exp_f32_e32 v159, v159
	v_mfma_f32_32x32x16_bf16 v[50:65], v[210:213], v[162:165], v[50:65]
	v_exp_f32_e32 v160, v160
	v_exp_f32_e32 v161, v161
	v_add_f32_e32 v207, v207, v154
	v_add_f32_e32 v193, v193, v155
	v_add_f32_e32 v207, v207, v156
	v_add_f32_e32 v193, v193, v157
	ds_read_b64_tr_b16 v[162:163], v195 offset:21504
	ds_read_b64_tr_b16 v[164:165], v195 offset:23552
	s_waitcnt lgkmcnt(10)
	v_mfma_f32_32x32x16_bf16 v[66:81], v[146:149], v[166:169], v[66:81]
	v_add_f32_e32 v207, v207, v158
	v_add_f32_e32 v193, v193, v159
	v_add_f32_e32 v207, v207, v160
	v_add_f32_e32 v193, v193, v161
	v_cvt_pk_bf16_f32 v154, v154, v155
	v_cvt_pk_bf16_f32 v155, v156, v157
	v_mfma_f32_32x32x16_bf16 v[34:49], v[210:213], v[166:169], v[34:49]
	v_cvt_pk_bf16_f32 v156, v158, v159
	v_cvt_pk_bf16_f32 v157, v160, v161
	ds_read_b64_tr_b16 v[166:167], v195 offset:22016
	ds_read_b64_tr_b16 v[168:169], v195 offset:24064
	v_permlane32_swap_b32_e32 v154, v156
	v_permlane32_swap_b32_e32 v155, v157
	s_waitcnt lgkmcnt(10)
	v_mfma_f32_32x32x16_bf16 v[98:113], v[146:149], v[170:173], v[98:113]
	v_exp_f32_e32 v218, v218
	v_exp_f32_e32 v219, v219
	v_exp_f32_e32 v220, v220
	v_exp_f32_e32 v221, v221
	v_exp_f32_e32 v222, v222
	v_exp_f32_e32 v223, v223
	v_mfma_f32_32x32x16_bf16 v[18:33], v[210:213], v[170:173], v[18:33]
	v_exp_f32_e32 v224, v224
	v_exp_f32_e32 v225, v225
	v_add_f32_e32 v206, v206, v218
	v_add_f32_e32 v209, v209, v219
	v_add_f32_e32 v206, v206, v220
	v_add_f32_e32 v209, v209, v221
	ds_read_b64_tr_b16 v[170:171], v195 offset:24576
	ds_read_b64_tr_b16 v[172:173], v195 offset:26624
	s_waitcnt lgkmcnt(10)
	v_mfma_f32_32x32x16_bf16 v[114:129], v[146:149], v[242:245], v[114:129]
	v_add_f32_e32 v206, v206, v222
	v_add_f32_e32 v209, v209, v223
	v_add_f32_e32 v206, v206, v224
	v_add_f32_e32 v209, v209, v225
	v_cvt_pk_bf16_f32 v218, v218, v219
	v_cvt_pk_bf16_f32 v219, v220, v221
	v_mfma_f32_32x32x16_bf16 v[2:17], v[210:213], v[242:245], v[2:17]
	v_cvt_pk_bf16_f32 v220, v222, v223
	v_cvt_pk_bf16_f32 v221, v224, v225
	ds_read_b64_tr_b16 v[242:243], v195 offset:25088
	ds_read_b64_tr_b16 v[244:245], v195 offset:27136
	v_permlane32_swap_b32_e32 v218, v220
	v_permlane32_swap_b32_e32 v219, v221
	s_waitcnt lgkmcnt(10)
	v_mfma_f32_32x32x16_bf16 v[82:97], v[154:157], v[246:249], v[82:97]
	v_exp_f32_e32 v130, v130
	v_exp_f32_e32 v131, v131
	v_exp_f32_e32 v132, v132
	v_exp_f32_e32 v133, v133
	v_exp_f32_e32 v134, v134
	v_exp_f32_e32 v135, v135
	v_mfma_f32_32x32x16_bf16 v[50:65], v[218:221], v[246:249], v[50:65]
	v_exp_f32_e32 v136, v136
	v_exp_f32_e32 v137, v137
	v_add_f32_e32 v207, v207, v130
	v_add_f32_e32 v193, v193, v131
	v_add_f32_e32 v207, v207, v132
	v_add_f32_e32 v193, v193, v133
	ds_read_b64_tr_b16 v[246:247], v195 offset:25600
	ds_read_b64_tr_b16 v[248:249], v195 offset:27648
	s_waitcnt lgkmcnt(10)
	v_mfma_f32_32x32x16_bf16 v[66:81], v[154:157], v[198:201], v[66:81]
	v_add_f32_e32 v207, v207, v134
	v_add_f32_e32 v193, v193, v135
	v_add_f32_e32 v207, v207, v136
	v_add_f32_e32 v193, v193, v137
	v_cvt_pk_bf16_f32 v130, v130, v131
	v_cvt_pk_bf16_f32 v131, v132, v133
	v_mfma_f32_32x32x16_bf16 v[34:49], v[218:221], v[198:201], v[34:49]
	v_cvt_pk_bf16_f32 v132, v134, v135
	v_cvt_pk_bf16_f32 v133, v136, v137
	ds_read_b64_tr_b16 v[198:199], v195 offset:26112
	ds_read_b64_tr_b16 v[200:201], v195 offset:28160
	v_permlane32_swap_b32_e32 v130, v132
	v_permlane32_swap_b32_e32 v131, v133
	s_waitcnt lgkmcnt(10)
	v_mfma_f32_32x32x16_bf16 v[98:113], v[154:157], v[162:165], v[98:113]
	v_exp_f32_e32 v226, v226
	v_exp_f32_e32 v227, v227
	v_exp_f32_e32 v228, v228
	v_exp_f32_e32 v229, v229
	v_exp_f32_e32 v230, v230
	v_exp_f32_e32 v231, v231
	v_mfma_f32_32x32x16_bf16 v[18:33], v[218:221], v[162:165], v[18:33]
	v_exp_f32_e32 v232, v232
	v_exp_f32_e32 v233, v233
	v_add_f32_e32 v206, v206, v226
	v_add_f32_e32 v209, v209, v227
	v_add_f32_e32 v206, v206, v228
	v_add_f32_e32 v209, v209, v229
	ds_read_b64_tr_b16 v[162:163], v195 offset:28672
	ds_read_b64_tr_b16 v[164:165], v195 offset:30720
	s_waitcnt lgkmcnt(10)
	v_mfma_f32_32x32x16_bf16 v[114:129], v[154:157], v[166:169], v[114:129]
	v_add_f32_e32 v206, v206, v230
	v_add_f32_e32 v209, v209, v231
	v_add_f32_e32 v206, v206, v232
	v_add_f32_e32 v209, v209, v233
	v_cvt_pk_bf16_f32 v226, v226, v227
	v_cvt_pk_bf16_f32 v227, v228, v229
	v_mfma_f32_32x32x16_bf16 v[2:17], v[218:221], v[166:169], v[2:17]
	v_cvt_pk_bf16_f32 v228, v230, v231
	v_cvt_pk_bf16_f32 v229, v232, v233
	ds_read_b64_tr_b16 v[166:167], v195 offset:29184
	ds_read_b64_tr_b16 v[168:169], v195 offset:31232
	v_permlane32_swap_b32_e32 v226, v228
	v_permlane32_swap_b32_e32 v227, v229
	s_waitcnt lgkmcnt(10)
	v_mfma_f32_32x32x16_bf16 v[82:97], v[130:133], v[170:173], v[82:97]
	v_exp_f32_e32 v138, v138
	v_exp_f32_e32 v139, v139
	v_exp_f32_e32 v140, v140
	v_exp_f32_e32 v141, v141
	v_exp_f32_e32 v142, v142
	v_exp_f32_e32 v143, v143
	v_mfma_f32_32x32x16_bf16 v[50:65], v[226:229], v[170:173], v[50:65]
	v_exp_f32_e32 v144, v144
	v_exp_f32_e32 v145, v145
	v_add_f32_e32 v207, v207, v138
	v_add_f32_e32 v193, v193, v139
	v_add_f32_e32 v207, v207, v140
	v_add_f32_e32 v193, v193, v141
	ds_read_b64_tr_b16 v[170:171], v195 offset:29696
	ds_read_b64_tr_b16 v[172:173], v195 offset:31744
	s_waitcnt lgkmcnt(10)
	v_mfma_f32_32x32x16_bf16 v[66:81], v[130:133], v[242:245], v[66:81]
	v_add_f32_e32 v207, v207, v142
	v_add_f32_e32 v193, v193, v143
	v_add_f32_e32 v207, v207, v144
	v_add_f32_e32 v193, v193, v145
	v_cvt_pk_bf16_f32 v138, v138, v139
	v_cvt_pk_bf16_f32 v139, v140, v141
	v_mfma_f32_32x32x16_bf16 v[34:49], v[226:229], v[242:245], v[34:49]
	v_cvt_pk_bf16_f32 v140, v142, v143
	v_cvt_pk_bf16_f32 v141, v144, v145
	ds_read_b64_tr_b16 v[242:243], v195 offset:30208
	ds_read_b64_tr_b16 v[244:245], v195 offset:32256
	v_permlane32_swap_b32_e32 v138, v140
	v_permlane32_swap_b32_e32 v139, v141
	s_waitcnt lgkmcnt(10)
	v_mfma_f32_32x32x16_bf16 v[98:113], v[130:133], v[246:249], v[98:113]
	v_exp_f32_e32 v234, v234
	v_exp_f32_e32 v235, v235
	v_exp_f32_e32 v236, v236
	v_exp_f32_e32 v237, v237
	v_exp_f32_e32 v238, v238
	v_exp_f32_e32 v239, v239
	v_mfma_f32_32x32x16_bf16 v[18:33], v[226:229], v[246:249], v[18:33]
	v_exp_f32_e32 v240, v240
	v_exp_f32_e32 v241, v241
	v_add_f32_e32 v206, v206, v234
	v_add_f32_e32 v209, v209, v235
	v_add_f32_e32 v206, v206, v236
	v_add_f32_e32 v209, v209, v237
	s_waitcnt lgkmcnt(8)
	v_mfma_f32_32x32x16_bf16 v[114:129], v[130:133], v[198:201], v[114:129]
	v_add_f32_e32 v206, v206, v238
	v_add_f32_e32 v209, v209, v239
	v_add_f32_e32 v206, v206, v240
	v_add_f32_e32 v209, v209, v241
	v_cvt_pk_bf16_f32 v234, v234, v235
	v_cvt_pk_bf16_f32 v235, v236, v237
	v_mfma_f32_32x32x16_bf16 v[2:17], v[226:229], v[198:201], v[2:17]
	v_cvt_pk_bf16_f32 v236, v238, v239
	v_cvt_pk_bf16_f32 v237, v240, v241
	s_nop 1
	v_permlane32_swap_b32_e32 v234, v236
	v_permlane32_swap_b32_e32 v235, v237
	s_waitcnt lgkmcnt(6)
	v_mfma_f32_32x32x16_bf16 v[82:97], v[138:141], v[162:165], v[82:97]
	v_mfma_f32_32x32x16_bf16 v[50:65], v[234:237], v[162:165], v[50:65]
	s_waitcnt lgkmcnt(4)
	v_mfma_f32_32x32x16_bf16 v[66:81], v[138:141], v[166:169], v[66:81]
	v_mfma_f32_32x32x16_bf16 v[34:49], v[234:237], v[166:169], v[34:49]
	s_waitcnt lgkmcnt(2)
	v_mfma_f32_32x32x16_bf16 v[98:113], v[138:141], v[170:173], v[98:113]
	v_mfma_f32_32x32x16_bf16 v[18:33], v[234:237], v[170:173], v[18:33]
	s_waitcnt lgkmcnt(0)
	v_mfma_f32_32x32x16_bf16 v[114:129], v[138:141], v[242:245], v[114:129]
	v_mfma_f32_32x32x16_bf16 v[2:17], v[234:237], v[242:245], v[2:17]
	s_add_i32 s72, s72, 1
	s_add_i32 s71, s71, 64
	s_addk_i32 s70, 0x4000
	s_cmpk_eq_i32 s72, 0x44
	s_waitcnt vmcnt(0)
	s_barrier
	s_cbranch_scc0 .Lfa_loop
	v_add_f32_e32 v207, v207, v193
	v_add_f32_e32 v206, v206, v209
	s_mul_i32 s4, s79, 0x700
	s_add_i32 s4, s4, 0x20800
	v_lshl_add_u32 v250, v196, 2, s4
	ds_read_b32 v162, v250 offset:0
	ds_read_b32 v164, v250 offset:256
	ds_read_b32 v166, v250 offset:512
	ds_read_b32 v168, v250 offset:768
	ds_read_b32 v170, v250 offset:1024
	ds_read_b32 v172, v250 offset:1280
	ds_read_b32 v174, v250 offset:1536
	v_mov_b32_e32 v163, 0
	v_mov_b32_e32 v165, 0
	v_mov_b32_e32 v167, 0
	v_mov_b32_e32 v169, 0
	v_mov_b32_e32 v171, 0
	v_mov_b32_e32 v173, 0
	v_mov_b32_e32 v175, 0
	v_lshlrev_b32_e32 v178, 8, v176
	v_mov_b32_e32 v198, 0x2800
	v_mov_b32_e32 v199, 0x8000
	v_mov_b32_e32 v200, 0x260
	v_mov_b32_e32 v201, 0xc2700000
	v_sub_u32_e32 v179, v180, v178
	v_sub_u32_e32 v181, v182, v178
	v_sub_u32_e32 v183, v184, v178
	v_sub_u32_e32 v185, v186, v178
	v_sub_u32_e32 v187, v188, v178
	v_sub_u32_e32 v189, v190, v178
	v_sub_u32_e32 v191, v192, v178
	v_sub_u32_e32 v193, v194, v178
	v_mov_b32_e32 v203, 0x358637bd
	s_waitcnt lgkmcnt(0)
	s_branch .LBB0_651
.LBB0_640:
	v_mov_b32_e32 v130, v208
	s_nop 0
	v_readfirstlane_b32 s4, v130
	s_setprio 1
	s_and_b32 s74, s70, 0x4000
	s_add_i32 s73, s74, 0
	v_add_u32_e32 v130, s73, v180
	ds_read_b128 v[130:133], v130 offset:32768
	v_add_u32_e32 v134, s24, v180
	ds_read_b128 v[134:137], v134
	v_add3_u32 v138, s73, v179, v178
	v_add_u32_e32 v209, s24, v182
	v_add_u32_e32 v142, s73, v182
	ds_read_b128 v[138:141], v138 offset:40960
	ds_read_b128 v[210:213], v142 offset:32768
	ds_read_b128 v[214:217], v209
	v_add3_u32 v209, s73, v181, v178
	s_waitcnt lgkmcnt(3)
	v_mfma_f32_32x32x16_bf16 v[146:161], v[130:133], v[134:137], 0
	s_waitcnt lgkmcnt(0)
	v_mfma_f32_32x32x16_bf16 v[146:161], v[210:213], v[214:217], v[146:161]
	ds_read_b128 v[210:213], v209 offset:40960
	v_add_u32_e32 v209, s73, v184
	v_mfma_f32_32x32x16_bf16 v[130:145], v[138:141], v[134:137], 0
	s_waitcnt lgkmcnt(0)
	v_mfma_f32_32x32x16_bf16 v[130:145], v[210:213], v[214:217], v[130:145]
	ds_read_b128 v[210:213], v209 offset:32768
	v_add_u32_e32 v209, s24, v184
	ds_read_b128 v[214:217], v209
	v_add3_u32 v209, s73, v183, v178
	ds_read_b128 v[218:221], v209 offset:40960
	v_add_u32_e32 v209, s73, v186
	ds_read_b128 v[222:225], v209 offset:32768
	v_add_u32_e32 v209, s24, v186
	s_waitcnt lgkmcnt(2)
	v_mfma_f32_32x32x16_bf16 v[146:161], v[210:213], v[214:217], v[146:161]
	ds_read_b128 v[210:213], v209
	v_add3_u32 v209, s73, v185, v178
	s_waitcnt lgkmcnt(2)
	v_mfma_f32_32x32x16_bf16 v[130:145], v[218:221], v[214:217], v[130:145]
	ds_read_b128 v[214:217], v209 offset:40960
	s_waitcnt lgkmcnt(1)
	v_mfma_f32_32x32x16_bf16 v[146:161], v[222:225], v[210:213], v[146:161]
	s_waitcnt lgkmcnt(0)
	v_mfma_f32_32x32x16_bf16 v[130:145], v[214:217], v[210:213], v[130:145]
	s_setprio 0
	s_cmpk_eq_i32 s72, 0x43
	s_cbranch_scc1 .LBB0_642
	v_mov_b32_e32 v209, v196
	s_cmp_lt_u32 s72, 3
	s_cselect_b32 s5, s66, s68
	v_ashrrev_i32_e32 v210, 4, v209
	v_and_b32_e32 v211, 15, v209
	v_add_u32_e32 v215, s25, v210
	s_add_i32 s5, s5, s71
	v_bitop3_b32 v216, v215, v211, 15 bitop3:0x6c
	v_mul_lo_u32 v215, v215, s44
	s_mul_hi_i32 s19, s5, 0x3200
	s_mulk_i32 s5, 0x3200
	v_ashrrev_i32_e32 v212, 5, v209
	v_add_u32_e32 v215, s67, v215
	v_lshlrev_b32_e32 v216, 4, v216
	s_add_u32 s18, s20, s5
	v_lshl_or_b32 v215, v215, 1, v216
	v_add_u32_e32 v216, s26, v212
	s_addc_u32 s19, s21, s19
	v_bfe_u32 v213, v209, 2, 2
	v_lshrrev_b32_e32 v214, 1, v209
	s_xor_b32 s5, s74, 0x4000
	v_lshlrev_b32_e32 v217, 1, v216
	v_and_or_b32 v213, v214, 8, v213
	v_lshlrev_b32_e32 v214, 3, v209
	s_add_i32 s5, s5, 0
	v_and_b32_e32 v217, 0xfffff0, v217
	v_and_b32_e32 v216, 4, v216
	v_and_b32_e32 v214, 24, v214
	v_or3_b32 v216, v216, v217, v213
	v_and_b32_e32 v209, 0x60, v209
	s_add_i32 s75, s5, s27
	v_mul_u32_u24_e32 v216, 0x1900, v216
	v_or3_b32 v209, s69, v209, v214
	s_add_i32 m0, s75, 0x8000
	v_add_lshl_u32 v209, v209, v216, 1
	global_load_lds_dwordx4 v215, s[18:19]
	s_mov_b32 m0, s75
	s_add_i32 s5, s5, s30
	global_load_lds_dwordx4 v209, s[18:19]
	v_add_u32_e32 v209, s28, v210
	v_mul_lo_u32 v210, v209, s44
	v_bitop3_b32 v209, v209, v211, 15 bitop3:0x6c
	v_add_u32_e32 v210, s67, v210
	v_lshlrev_b32_e32 v209, 4, v209
	v_lshl_or_b32 v209, v210, 1, v209
	v_add_u32_e32 v210, s29, v212
	v_lshlrev_b32_e32 v211, 1, v210
	v_and_b32_e32 v211, 0xfffff0, v211
	v_and_b32_e32 v212, 4, v210
	v_lshlrev_b32_e32 v210, 5, v210
	v_or3_b32 v211, v212, v211, v213
	v_and_b32_e32 v210, 0x60, v210
	v_mul_u32_u24_e32 v211, 0x1900, v211
	v_or3_b32 v210, s69, v210, v214
	s_add_i32 m0, s5, 0x8000
	v_add_lshl_u32 v210, v210, v211, 1
	global_load_lds_dwordx4 v209, s[18:19]
	s_mov_b32 m0, s5
	s_nop 0
	global_load_lds_dwordx4 v210, s[18:19]

.LBB0_715:
	ds_read_b128 v[154:157], v150
	ds_read_b128 v[158:161], v150 offset:1024
	ds_read_b128 v[162:165], v150 offset:2048
	ds_read_b128 v[166:169], v150 offset:3072
	s_add_u32 s30, s28, 0xfff80080
	s_addc_u32 s31, s29, -1
	s_cmp_eq_u32 s74, 28
	s_cselect_b32 s35, s21, s31
	s_cselect_b32 s34, s70, s30
	s_cselect_b32 s31, s19, s73
	s_cselect_b32 s30, s71, s72
	v_lshl_add_u64 v[146:147], s[28:29], 0, v[138:139]
	s_add_i32 m0, s27, 0xc000
	ds_read_b128 v[170:173], v151
	ds_read_b128 v[174:177], v151 offset:1024
	ds_read_b128 v[178:181], v151 offset:2048
	ds_read_b128 v[182:185], v151 offset:3072
	ds_read_b128 v[186:189], v151 offset:4096
	ds_read_b128 v[190:193], v151 offset:5120
	ds_read_b128 v[198:201], v151 offset:6144
	ds_read_b128 v[202:205], v151 offset:7168
	global_load_lds_dwordx4 v[146:147], off
	v_lshl_add_u64 v[146:147], s[28:29], 0, v[140:141]
	s_add_i32 m0, s27, 0xe000
	s_nop 0
	global_load_lds_dwordx4 v[146:147], off
	s_waitcnt lgkmcnt(8)
	s_barrier
	s_waitcnt lgkmcnt(0)
	s_waitcnt lgkmcnt(0)
	v_mfma_f32_16x16x32_bf16 v[126:129], v[154:157], v[170:173], v[126:129]
	v_mfma_f32_16x16x32_bf16 v[122:125], v[162:165], v[170:173], v[122:125]
	v_mfma_f32_16x16x32_bf16 v[114:117], v[154:157], v[178:181], v[114:117]
	v_mfma_f32_16x16x32_bf16 v[106:109], v[162:165], v[178:181], v[106:109]
	v_mfma_f32_16x16x32_bf16 v[98:101], v[154:157], v[186:189], v[98:101]
	v_mfma_f32_16x16x32_bf16 v[90:93], v[162:165], v[186:189], v[90:93]
	v_mfma_f32_16x16x32_bf16 v[82:85], v[154:157], v[198:201], v[82:85]
	v_mfma_f32_16x16x32_bf16 v[74:77], v[162:165], v[198:201], v[74:77]
	v_mfma_f32_16x16x32_bf16 v[126:129], v[158:161], v[174:177], v[126:129]
	v_mfma_f32_16x16x32_bf16 v[122:125], v[166:169], v[174:177], v[122:125]
	v_mfma_f32_16x16x32_bf16 v[114:117], v[158:161], v[182:185], v[114:117]
	v_mfma_f32_16x16x32_bf16 v[106:109], v[166:169], v[182:185], v[106:109]
	v_mfma_f32_16x16x32_bf16 v[98:101], v[158:161], v[190:193], v[98:101]
	v_mfma_f32_16x16x32_bf16 v[90:93], v[166:169], v[190:193], v[90:93]
	v_mfma_f32_16x16x32_bf16 v[82:85], v[158:161], v[202:205], v[82:85]
	v_mfma_f32_16x16x32_bf16 v[74:77], v[166:169], v[202:205], v[74:77]
	s_barrier
	s_add_i32 s75, s55, s40
	v_lshl_add_u64 v[146:147], s[30:31], 0, v[132:133]
	s_mov_b32 m0, s75
	ds_read_b128 v[206:209], v152
	ds_read_b128 v[210:213], v152 offset:1024
	ds_read_b128 v[214:217], v152 offset:2048
	ds_read_b128 v[218:221], v152 offset:3072
	global_load_lds_dwordx4 v[146:147], off
	v_lshl_add_u64 v[194:195], s[30:31], 0, v[136:137]
	s_add_i32 m0, s75, 0x2000
	s_nop 0
	global_load_lds_dwordx4 v[194:195], off
	s_barrier
	s_waitcnt lgkmcnt(0)
	s_waitcnt lgkmcnt(0)
	v_mfma_f32_16x16x32_bf16 v[118:121], v[206:209], v[170:173], v[118:121]
	v_mfma_f32_16x16x32_bf16 v[110:113], v[214:217], v[170:173], v[110:113]
	v_mfma_f32_16x16x32_bf16 v[102:105], v[206:209], v[178:181], v[102:105]
	v_mfma_f32_16x16x32_bf16 v[94:97], v[214:217], v[178:181], v[94:97]
	v_mfma_f32_16x16x32_bf16 v[86:89], v[206:209], v[186:189], v[86:89]
	v_mfma_f32_16x16x32_bf16 v[78:81], v[214:217], v[186:189], v[78:81]
	v_mfma_f32_16x16x32_bf16 v[70:73], v[206:209], v[198:201], v[70:73]
	v_mfma_f32_16x16x32_bf16 v[66:69], v[214:217], v[198:201], v[66:69]
	v_mfma_f32_16x16x32_bf16 v[118:121], v[210:213], v[174:177], v[118:121]
	v_mfma_f32_16x16x32_bf16 v[110:113], v[218:221], v[174:177], v[110:113]
	v_mfma_f32_16x16x32_bf16 v[102:105], v[210:213], v[182:185], v[102:105]
	v_mfma_f32_16x16x32_bf16 v[94:97], v[218:221], v[182:185], v[94:97]
	v_mfma_f32_16x16x32_bf16 v[86:89], v[210:213], v[190:193], v[86:89]
	v_mfma_f32_16x16x32_bf16 v[78:81], v[218:221], v[190:193], v[78:81]
	v_mfma_f32_16x16x32_bf16 v[70:73], v[210:213], v[202:205], v[70:73]
	v_mfma_f32_16x16x32_bf16 v[66:69], v[218:221], v[202:205], v[66:69]
	s_mov_b32 m0, s27
	v_lshl_add_u64 v[222:223], s[34:35], 0, v[130:131]
	s_barrier
	ds_read_b128 v[170:173], v151 offset:16384
	ds_read_b128 v[174:177], v151 offset:17408
	ds_read_b128 v[178:181], v151 offset:18432
	ds_read_b128 v[182:185], v151 offset:19456
	ds_read_b128 v[186:189], v151 offset:20480
	ds_read_b128 v[190:193], v151 offset:21504
	ds_read_b128 v[198:201], v151 offset:22528
	ds_read_b128 v[202:205], v151 offset:23552
	global_load_lds_dwordx4 v[222:223], off
	v_lshl_add_u64 v[224:225], s[34:35], 0, v[134:135]
	s_mov_b32 m0, s42
	s_nop 0
	global_load_lds_dwordx4 v[224:225], off
	s_barrier
	s_waitcnt lgkmcnt(0)
	s_waitcnt lgkmcnt(0)
	v_mfma_f32_16x16x32_bf16 v[62:65], v[154:157], v[170:173], v[62:65]
	v_mfma_f32_16x16x32_bf16 v[58:61], v[162:165], v[170:173], v[58:61]
	v_mfma_f32_16x16x32_bf16 v[54:57], v[154:157], v[178:181], v[54:57]
	v_mfma_f32_16x16x32_bf16 v[46:49], v[162:165], v[178:181], v[46:49]
	v_mfma_f32_16x16x32_bf16 v[38:41], v[154:157], v[186:189], v[38:41]
	v_mfma_f32_16x16x32_bf16 v[30:33], v[162:165], v[186:189], v[30:33]
	v_mfma_f32_16x16x32_bf16 v[22:25], v[154:157], v[198:201], v[22:25]
	v_mfma_f32_16x16x32_bf16 v[14:17], v[162:165], v[198:201], v[14:17]
	v_mfma_f32_16x16x32_bf16 v[62:65], v[158:161], v[174:177], v[62:65]
	v_mfma_f32_16x16x32_bf16 v[58:61], v[166:169], v[174:177], v[58:61]
	v_mfma_f32_16x16x32_bf16 v[54:57], v[158:161], v[182:185], v[54:57]
	v_mfma_f32_16x16x32_bf16 v[46:49], v[166:169], v[182:185], v[46:49]
	v_mfma_f32_16x16x32_bf16 v[38:41], v[158:161], v[190:193], v[38:41]
	v_mfma_f32_16x16x32_bf16 v[30:33], v[166:169], v[190:193], v[30:33]
	v_mfma_f32_16x16x32_bf16 v[22:25], v[158:161], v[202:205], v[22:25]
	v_mfma_f32_16x16x32_bf16 v[14:17], v[166:169], v[202:205], v[14:17]
	s_barrier
	s_add_u32 s76, s30, 0x80000
	s_addc_u32 s77, s31, 0
	s_add_i32 s75, s64, s40
	v_lshl_add_u64 v[154:155], s[76:77], 0, v[132:133]
	s_mov_b32 m0, s75
	s_nop 0
	global_load_lds_dwordx4 v[154:155], off
	v_lshl_add_u64 v[154:155], s[76:77], 0, v[136:137]
	s_add_i32 m0, s75, 0x2000
	s_nop 0
	global_load_lds_dwordx4 v[154:155], off
	s_waitcnt vmcnt(6)
	s_barrier
	v_mfma_f32_16x16x32_bf16 v[50:53], v[206:209], v[170:173], v[50:53]
	v_mfma_f32_16x16x32_bf16 v[42:45], v[214:217], v[170:173], v[42:45]
	v_mfma_f32_16x16x32_bf16 v[34:37], v[206:209], v[178:181], v[34:37]
	v_mfma_f32_16x16x32_bf16 v[26:29], v[214:217], v[178:181], v[26:29]
	v_mfma_f32_16x16x32_bf16 v[18:21], v[206:209], v[186:189], v[18:21]
	v_mfma_f32_16x16x32_bf16 v[10:13], v[214:217], v[186:189], v[10:13]
	v_mfma_f32_16x16x32_bf16 v[6:9], v[206:209], v[198:201], v[6:9]
	v_mfma_f32_16x16x32_bf16 v[2:5], v[214:217], v[198:201], v[2:5]
	v_mfma_f32_16x16x32_bf16 v[50:53], v[210:213], v[174:177], v[50:53]
	v_mfma_f32_16x16x32_bf16 v[42:45], v[218:221], v[174:177], v[42:45]
	v_mfma_f32_16x16x32_bf16 v[34:37], v[210:213], v[182:185], v[34:37]
	v_mfma_f32_16x16x32_bf16 v[26:29], v[218:221], v[182:185], v[26:29]
	v_mfma_f32_16x16x32_bf16 v[18:21], v[210:213], v[190:193], v[18:21]
	v_mfma_f32_16x16x32_bf16 v[10:13], v[218:221], v[190:193], v[10:13]
	v_mfma_f32_16x16x32_bf16 v[6:9], v[210:213], v[202:205], v[6:9]
	v_mfma_f32_16x16x32_bf16 v[2:5], v[218:221], v[202:205], v[2:5]
	s_add_i32 s75, 0, 0x18000
	v_add_u32_e32 v153, s75, v148
	s_barrier
	ds_read_b128 v[154:157], v153
	ds_read_b128 v[158:161], v153 offset:1024
	ds_read_b128 v[162:165], v153 offset:2048
	ds_read_b128 v[166:169], v153 offset:3072
	s_add_u32 s34, s34, 0x80000
	s_addc_u32 s35, s35, 0
	s_mov_b32 m0, s43
	v_lshl_add_u64 v[206:207], s[34:35], 0, v[130:131]
	ds_read_b128 v[170:173], v151 offset:32768
	ds_read_b128 v[174:177], v151 offset:33792
	ds_read_b128 v[178:181], v151 offset:34816
	ds_read_b128 v[182:185], v151 offset:35840
	ds_read_b128 v[186:189], v151 offset:36864
	ds_read_b128 v[190:193], v151 offset:37888
	ds_read_b128 v[198:201], v151 offset:38912
	ds_read_b128 v[202:205], v151 offset:39936
	global_load_lds_dwordx4 v[206:207], off
	v_lshl_add_u64 v[206:207], s[34:35], 0, v[134:135]
	s_mov_b32 m0, s44
	s_nop 0
	global_load_lds_dwordx4 v[206:207], off
	s_waitcnt lgkmcnt(8)
	s_barrier
	s_waitcnt lgkmcnt(0)
	s_waitcnt lgkmcnt(0)
	v_mfma_f32_16x16x32_bf16 v[126:129], v[154:157], v[170:173], v[126:129]
	v_mfma_f32_16x16x32_bf16 v[122:125], v[162:165], v[170:173], v[122:125]
	v_mfma_f32_16x16x32_bf16 v[114:117], v[154:157], v[178:181], v[114:117]
	v_mfma_f32_16x16x32_bf16 v[106:109], v[162:165], v[178:181], v[106:109]
	v_mfma_f32_16x16x32_bf16 v[98:101], v[154:157], v[186:189], v[98:101]
	v_mfma_f32_16x16x32_bf16 v[90:93], v[162:165], v[186:189], v[90:93]
	v_mfma_f32_16x16x32_bf16 v[82:85], v[154:157], v[198:201], v[82:85]
	v_mfma_f32_16x16x32_bf16 v[74:77], v[162:165], v[198:201], v[74:77]
	v_mfma_f32_16x16x32_bf16 v[126:129], v[158:161], v[174:177], v[126:129]
	v_mfma_f32_16x16x32_bf16 v[122:125], v[166:169], v[174:177], v[122:125]
	v_mfma_f32_16x16x32_bf16 v[114:117], v[158:161], v[182:185], v[114:117]
	v_mfma_f32_16x16x32_bf16 v[106:109], v[166:169], v[182:185], v[106:109]
	v_mfma_f32_16x16x32_bf16 v[98:101], v[158:161], v[190:193], v[98:101]
	v_mfma_f32_16x16x32_bf16 v[90:93], v[166:169], v[190:193], v[90:93]
	v_mfma_f32_16x16x32_bf16 v[82:85], v[158:161], v[202:205], v[82:85]
	v_mfma_f32_16x16x32_bf16 v[74:77], v[166:169], v[202:205], v[74:77]
	s_barrier
	s_add_i32 s34, 0, 0x1c000
	s_add_i32 s35, s75, s40
	v_add_u32_e32 v153, s34, v148
	v_lshl_add_u64 v[146:147], v[146:147], 0, s[8:9]
	s_mov_b32 m0, s35
	ds_read_b128 v[206:209], v153
	ds_read_b128 v[210:213], v153 offset:1024
	ds_read_b128 v[214:217], v153 offset:2048
	ds_read_b128 v[218:221], v153 offset:3072
	global_load_lds_dwordx4 v[146:147], off
	v_lshl_add_u64 v[146:147], v[194:195], 0, s[8:9]
	s_add_i32 m0, s35, 0x2000
	s_nop 0
	global_load_lds_dwordx4 v[146:147], off
	s_barrier
	s_waitcnt lgkmcnt(0)
	s_waitcnt lgkmcnt(0)
	v_mfma_f32_16x16x32_bf16 v[118:121], v[206:209], v[170:173], v[118:121]
	v_mfma_f32_16x16x32_bf16 v[110:113], v[214:217], v[170:173], v[110:113]
	v_mfma_f32_16x16x32_bf16 v[102:105], v[206:209], v[178:181], v[102:105]
	v_mfma_f32_16x16x32_bf16 v[94:97], v[214:217], v[178:181], v[94:97]
	v_mfma_f32_16x16x32_bf16 v[86:89], v[206:209], v[186:189], v[86:89]
	v_mfma_f32_16x16x32_bf16 v[78:81], v[214:217], v[186:189], v[78:81]
	v_mfma_f32_16x16x32_bf16 v[70:73], v[206:209], v[198:201], v[70:73]
	v_mfma_f32_16x16x32_bf16 v[66:69], v[214:217], v[198:201], v[66:69]
	v_mfma_f32_16x16x32_bf16 v[118:121], v[210:213], v[174:177], v[118:121]
	v_mfma_f32_16x16x32_bf16 v[110:113], v[218:221], v[174:177], v[110:113]
	v_mfma_f32_16x16x32_bf16 v[102:105], v[210:213], v[182:185], v[102:105]
	v_mfma_f32_16x16x32_bf16 v[94:97], v[218:221], v[182:185], v[94:97]
	v_mfma_f32_16x16x32_bf16 v[86:89], v[210:213], v[190:193], v[86:89]
	v_mfma_f32_16x16x32_bf16 v[78:81], v[218:221], v[190:193], v[78:81]
	v_mfma_f32_16x16x32_bf16 v[70:73], v[210:213], v[202:205], v[70:73]
	v_mfma_f32_16x16x32_bf16 v[66:69], v[218:221], v[202:205], v[66:69]
	s_mov_b32 m0, s53
	v_lshl_add_u64 v[146:147], v[222:223], 0, s[8:9]
	s_barrier
	ds_read_b128 v[170:173], v151 offset:49152
	ds_read_b128 v[174:177], v151 offset:50176
	ds_read_b128 v[178:181], v151 offset:51200
	ds_read_b128 v[182:185], v151 offset:52224
	ds_read_b128 v[186:189], v151 offset:53248
	ds_read_b128 v[190:193], v151 offset:54272
	ds_read_b128 v[198:201], v151 offset:55296
	ds_read_b128 v[202:205], v151 offset:56320
	global_load_lds_dwordx4 v[146:147], off
	v_lshl_add_u64 v[146:147], v[224:225], 0, s[8:9]
	s_mov_b32 m0, s54
	s_nop 0
	global_load_lds_dwordx4 v[146:147], off
	s_barrier
	s_waitcnt lgkmcnt(0)
	s_waitcnt lgkmcnt(0)
	v_mfma_f32_16x16x32_bf16 v[62:65], v[154:157], v[170:173], v[62:65]
	v_mfma_f32_16x16x32_bf16 v[58:61], v[162:165], v[170:173], v[58:61]
	v_mfma_f32_16x16x32_bf16 v[54:57], v[154:157], v[178:181], v[54:57]
	v_mfma_f32_16x16x32_bf16 v[46:49], v[162:165], v[178:181], v[46:49]
	v_mfma_f32_16x16x32_bf16 v[38:41], v[154:157], v[186:189], v[38:41]
	v_mfma_f32_16x16x32_bf16 v[30:33], v[162:165], v[186:189], v[30:33]
	v_mfma_f32_16x16x32_bf16 v[22:25], v[154:157], v[198:201], v[22:25]
	v_mfma_f32_16x16x32_bf16 v[14:17], v[162:165], v[198:201], v[14:17]
	v_mfma_f32_16x16x32_bf16 v[62:65], v[158:161], v[174:177], v[62:65]
	v_mfma_f32_16x16x32_bf16 v[58:61], v[166:169], v[174:177], v[58:61]
	v_mfma_f32_16x16x32_bf16 v[54:57], v[158:161], v[182:185], v[54:57]
	v_mfma_f32_16x16x32_bf16 v[46:49], v[166:169], v[182:185], v[46:49]
	v_mfma_f32_16x16x32_bf16 v[38:41], v[158:161], v[190:193], v[38:41]
	v_mfma_f32_16x16x32_bf16 v[30:33], v[166:169], v[190:193], v[30:33]
	v_mfma_f32_16x16x32_bf16 v[22:25], v[158:161], v[202:205], v[22:25]
	v_mfma_f32_16x16x32_bf16 v[14:17], v[166:169], v[202:205], v[14:17]
	s_barrier
	s_add_u32 s30, s30, 0x80080
	s_addc_u32 s31, s31, 0
	s_add_i32 s34, s34, s40
	v_lshl_add_u64 v[146:147], s[30:31], 0, v[132:133]
	s_mov_b32 m0, s34
	s_nop 0
	global_load_lds_dwordx4 v[146:147], off
	v_lshl_add_u64 v[146:147], s[30:31], 0, v[136:137]
	s_add_i32 m0, s34, 0x2000
	s_nop 0
	global_load_lds_dwordx4 v[146:147], off
	s_waitcnt vmcnt(6)
	s_barrier
	v_mfma_f32_16x16x32_bf16 v[50:53], v[206:209], v[170:173], v[50:53]
	v_mfma_f32_16x16x32_bf16 v[42:45], v[214:217], v[170:173], v[42:45]
	v_mfma_f32_16x16x32_bf16 v[34:37], v[206:209], v[178:181], v[34:37]
	v_mfma_f32_16x16x32_bf16 v[26:29], v[214:217], v[178:181], v[26:29]
	v_mfma_f32_16x16x32_bf16 v[18:21], v[206:209], v[186:189], v[18:21]
	v_mfma_f32_16x16x32_bf16 v[10:13], v[214:217], v[186:189], v[10:13]
	v_mfma_f32_16x16x32_bf16 v[6:9], v[206:209], v[198:201], v[6:9]
	v_mfma_f32_16x16x32_bf16 v[2:5], v[214:217], v[198:201], v[2:5]
	v_mfma_f32_16x16x32_bf16 v[50:53], v[210:213], v[174:177], v[50:53]
	v_mfma_f32_16x16x32_bf16 v[42:45], v[218:221], v[174:177], v[42:45]
	v_mfma_f32_16x16x32_bf16 v[34:37], v[210:213], v[182:185], v[34:37]
	v_mfma_f32_16x16x32_bf16 v[26:29], v[218:221], v[182:185], v[26:29]
	v_mfma_f32_16x16x32_bf16 v[18:21], v[210:213], v[190:193], v[18:21]
	v_mfma_f32_16x16x32_bf16 v[10:13], v[218:221], v[190:193], v[10:13]
	v_mfma_f32_16x16x32_bf16 v[6:9], v[210:213], v[202:205], v[6:9]
	v_mfma_f32_16x16x32_bf16 v[2:5], v[218:221], v[202:205], v[2:5]
	s_add_i32 s74, s74, 2
	s_add_u32 s28, s28, 0x100
	s_addc_u32 s29, s29, 0
	s_add_u32 s72, s72, 0x100
	s_addc_u32 s73, s73, 0
	s_cmp_gt_u32 s74, 29
	s_barrier
	s_cbranch_scc0 .LBB0_715
	v_lshl_add_u32 v154, s26, 8, v1
	v_lshl_or_b32 v146, s69, 8, v149
	v_ashrrev_i32_e32 v155, 31, v154
	v_ashrrev_i32_e32 v147, 31, v146
	v_lshlrev_b64 v[156:157], 12, v[154:155]
	v_lshl_add_u64 v[156:157], s[6:7], 0, v[156:157]
	v_lshlrev_b64 v[158:159], 1, v[146:147]
	v_lshl_add_u64 v[146:147], v[156:157], 0, v[158:159]
	v_cvt_pk_bf16_f32 v126, v126, v127
	v_cvt_pk_bf16_f32 v127, v128, v129
	v_cvt_pk_bf16_f32 v128, v122, v123
	v_cvt_pk_bf16_f32 v129, v124, v125
	global_store_dwordx4 v[146:147], v[126:129], off
	v_cvt_pk_bf16_f32 v118, v118, v119
	v_cvt_pk_bf16_f32 v119, v120, v121
	v_cvt_pk_bf16_f32 v120, v110, v111
	v_or_b32_e32 v110, 16, v154
	v_ashrrev_i32_e32 v111, 31, v110
	v_lshlrev_b64 v[110:111], 12, v[110:111]
	v_lshl_add_u64 v[110:111], s[6:7], 0, v[110:111]
	v_cvt_pk_bf16_f32 v121, v112, v113
	global_store_dwordx4 v[146:147], v[118:121], off offset:256
	s_mov_b32 s69, s18
	s_mov_b32 s26, s20
	v_lshl_add_u64 v[118:119], v[110:111], 0, v[158:159]
	v_cvt_pk_bf16_f32 v110, v114, v115
	v_cvt_pk_bf16_f32 v111, v116, v117
	v_cvt_pk_bf16_f32 v112, v106, v107
	v_cvt_pk_bf16_f32 v113, v108, v109
	global_store_dwordx4 v[118:119], v[110:113], off
	v_cvt_pk_bf16_f32 v102, v102, v103
	v_cvt_pk_bf16_f32 v103, v104, v105
	v_cvt_pk_bf16_f32 v104, v94, v95
	v_or_b32_e32 v94, 32, v154
	v_ashrrev_i32_e32 v95, 31, v94
	v_lshlrev_b64 v[94:95], 12, v[94:95]
	v_lshl_add_u64 v[94:95], s[6:7], 0, v[94:95]
	v_cvt_pk_bf16_f32 v105, v96, v97
	global_store_dwordx4 v[118:119], v[102:105], off offset:256
	s_mov_b64 s[30:31], s[24:25]
	s_mov_b64 s[28:29], s[22:23]
	v_lshl_add_u64 v[102:103], v[94:95], 0, v[158:159]
	v_cvt_pk_bf16_f32 v94, v98, v99
	v_cvt_pk_bf16_f32 v95, v100, v101
	v_cvt_pk_bf16_f32 v96, v90, v91
	v_cvt_pk_bf16_f32 v97, v92, v93
	global_store_dwordx4 v[102:103], v[94:97], off
	v_cvt_pk_bf16_f32 v86, v86, v87
	v_cvt_pk_bf16_f32 v87, v88, v89
	v_cvt_pk_bf16_f32 v88, v78, v79
	v_or_b32_e32 v78, 48, v154
	v_ashrrev_i32_e32 v79, 31, v78
	v_lshlrev_b64 v[78:79], 12, v[78:79]
	v_lshl_add_u64 v[78:79], s[6:7], 0, v[78:79]
	v_cvt_pk_bf16_f32 v89, v80, v81
	global_store_dwordx4 v[102:103], v[86:89], off offset:256
	s_nop 1
	v_lshl_add_u64 v[86:87], v[78:79], 0, v[158:159]
	v_cvt_pk_bf16_f32 v78, v82, v83
	v_cvt_pk_bf16_f32 v79, v84, v85
	v_cvt_pk_bf16_f32 v80, v74, v75
	v_cvt_pk_bf16_f32 v81, v76, v77
	global_store_dwordx4 v[86:87], v[78:81], off
	v_cvt_pk_bf16_f32 v70, v70, v71
	v_cvt_pk_bf16_f32 v71, v72, v73
	v_cvt_pk_bf16_f32 v72, v66, v67
	v_cvt_pk_bf16_f32 v73, v68, v69
	global_store_dwordx4 v[86:87], v[70:73], off offset:256
	v_cvt_pk_bf16_f32 v62, v62, v63
	v_cvt_pk_bf16_f32 v63, v64, v65
	v_cvt_pk_bf16_f32 v64, v58, v59
	v_add_co_u32_e32 v58, vcc, s65, v146
	v_lshl_add_u64 v[66:67], v[146:147], 0, s[4:5]
	s_nop 0
	v_addc_co_u32_e32 v59, vcc, 0, v147, vcc
	v_cvt_pk_bf16_f32 v65, v60, v61
	global_store_dwordx4 v[58:59], v[62:65], off
	v_cvt_pk_bf16_f32 v50, v50, v51
	v_cvt_pk_bf16_f32 v51, v52, v53
	v_cvt_pk_bf16_f32 v52, v42, v43
	v_cvt_pk_bf16_f32 v53, v44, v45
	global_store_dwordx4 v[66:67], v[50:53], off offset:256
	v_cvt_pk_bf16_f32 v42, v54, v55
	v_cvt_pk_bf16_f32 v43, v56, v57
	v_cvt_pk_bf16_f32 v44, v46, v47
	v_add_co_u32_e32 v46, vcc, s66, v146
	s_nop 0
	v_lshl_add_u64 v[50:51], v[146:147], 0, s[10:11]
	v_addc_co_u32_e32 v47, vcc, 0, v147, vcc
	v_cvt_pk_bf16_f32 v45, v48, v49
	global_store_dwordx4 v[46:47], v[42:45], off
	v_cvt_pk_bf16_f32 v34, v34, v35
	v_cvt_pk_bf16_f32 v35, v36, v37
	v_cvt_pk_bf16_f32 v36, v26, v27
	v_cvt_pk_bf16_f32 v37, v28, v29
	global_store_dwordx4 v[50:51], v[34:37], off offset:256
	v_cvt_pk_bf16_f32 v26, v38, v39
	v_cvt_pk_bf16_f32 v27, v40, v41
	v_cvt_pk_bf16_f32 v28, v30, v31
	v_add_co_u32_e32 v30, vcc, s67, v146
	s_nop 0
	v_lshl_add_u64 v[34:35], v[146:147], 0, s[14:15]
	v_addc_co_u32_e32 v31, vcc, 0, v147, vcc
	v_cvt_pk_bf16_f32 v29, v32, v33
	global_store_dwordx4 v[30:31], v[26:29], off
	v_cvt_pk_bf16_f32 v18, v18, v19
	v_cvt_pk_bf16_f32 v19, v20, v21
	v_cvt_pk_bf16_f32 v20, v10, v11
	v_cvt_pk_bf16_f32 v21, v12, v13
	global_store_dwordx4 v[34:35], v[18:21], off offset:256
	v_cvt_pk_bf16_f32 v10, v22, v23
	v_cvt_pk_bf16_f32 v11, v24, v25
	v_cvt_pk_bf16_f32 v12, v14, v15
	v_add_co_u32_e32 v14, vcc, s68, v146
	s_nop 0
	v_lshl_add_u64 v[18:19], v[146:147], 0, s[16:17]
	v_addc_co_u32_e32 v15, vcc, 0, v147, vcc
	s_and_b64 vcc, exec, s[0:1]
	v_cvt_pk_bf16_f32 v13, v16, v17
	global_store_dwordx4 v[14:15], v[10:13], off
	v_cvt_pk_bf16_f32 v6, v6, v7
	v_cvt_pk_bf16_f32 v7, v8, v9
	v_cvt_pk_bf16_f32 v8, v2, v3
	v_cvt_pk_bf16_f32 v9, v4, v5
	global_store_dwordx4 v[18:19], v[6:9], off offset:256
	s_cbranch_vccz .LBB0_708
	s_waitcnt vmcnt(0)
	s_cmpk_gt_u32 s33, 0xff
	s_cbranch_scc1 .LBB0_719
	s_barrier

.LBB0_1060:
	v_add_u32_e32 v14, s39, v201
	s_add_u32 s4, s26, 0x100
	ds_read_b128 v[2:5], v14
	ds_read_b128 v[6:9], v14 offset:1024
	ds_read_b128 v[10:13], v14 offset:2048
	ds_read_b128 v[14:17], v14 offset:3072
	s_addc_u32 s5, s27, 0
	s_add_u32 s54, s50, s26
	s_addc_u32 s55, s51, s27
	s_cmp_eq_u32 s52, 12
	s_cselect_b64 vcc, -1, 0
	s_and_b64 s[24:25], vcc, exec
	s_cselect_b32 s53, 0, s4
	s_cselect_b32 s25, s21, s55
	s_cselect_b32 s24, s49, s54
	v_lshl_add_u64 v[18:19], v[186:187], 0, s[26:27]
	s_add_i32 m0, s33, 0xc000
	ds_read_b128 v[210:213], v203
	ds_read_b128 v[214:217], v203 offset:1024
	ds_read_b128 v[218:221], v203 offset:2048
	ds_read_b128 v[222:225], v203 offset:3072
	ds_read_b128 v[226:229], v203 offset:4096
	ds_read_b128 v[230:233], v203 offset:5120
	ds_read_b128 v[234:237], v203 offset:6144
	ds_read_b128 v[238:241], v203 offset:7168
	global_load_lds_dwordx4 v[18:19], off
	v_lshl_add_u64 v[18:19], v[184:185], 0, s[26:27]
	s_add_i32 m0, s33, 0xe000
	s_nop 0
	global_load_lds_dwordx4 v[18:19], off
	s_waitcnt lgkmcnt(8)
	s_barrier
	s_waitcnt lgkmcnt(0)
	s_waitcnt lgkmcnt(0)
	v_mfma_f32_16x16x128_f8f6f4 v[158:161], v[2:9], v[210:217], v[158:161]
	v_mfma_f32_16x16x128_f8f6f4 v[150:153], v[10:17], v[210:217], v[150:153]
	v_mfma_f32_16x16x128_f8f6f4 v[142:145], v[2:9], v[218:225], v[142:145]
	v_mfma_f32_16x16x128_f8f6f4 v[134:137], v[10:17], v[218:225], v[134:137]
	v_mfma_f32_16x16x128_f8f6f4 v[126:129], v[2:9], v[226:233], v[126:129]
	v_mfma_f32_16x16x128_f8f6f4 v[118:121], v[10:17], v[226:233], v[118:121]
	v_mfma_f32_16x16x128_f8f6f4 v[110:113], v[2:9], v[234:241], v[110:113]
	v_mfma_f32_16x16x128_f8f6f4 v[102:105], v[10:17], v[234:241], v[102:105]
	s_barrier
	s_add_i32 s26, s39, s23
	v_add_u32_e32 v30, s40, v201
	v_lshl_add_u64 v[188:189], s[24:25], 0, v[164:165]
	s_mov_b32 m0, s26
	ds_read_b128 v[18:21], v30
	ds_read_b128 v[22:25], v30 offset:1024
	ds_read_b128 v[26:29], v30 offset:2048
	ds_read_b128 v[30:33], v30 offset:3072
	global_load_lds_dwordx4 v[188:189], off
	v_lshl_add_u64 v[190:191], s[24:25], 0, v[166:167]
	s_add_i32 m0, s26, 0x2000
	s_nop 0
	global_load_lds_dwordx4 v[190:191], off
	s_barrier
	s_waitcnt lgkmcnt(0)
	s_waitcnt lgkmcnt(0)
	v_mfma_f32_16x16x128_f8f6f4 v[154:157], v[18:25], v[210:217], v[154:157]
	v_mfma_f32_16x16x128_f8f6f4 v[146:149], v[26:33], v[210:217], v[146:149]
	v_mfma_f32_16x16x128_f8f6f4 v[138:141], v[18:25], v[218:225], v[138:141]
	v_mfma_f32_16x16x128_f8f6f4 v[130:133], v[26:33], v[218:225], v[130:133]
	v_mfma_f32_16x16x128_f8f6f4 v[122:125], v[18:25], v[226:233], v[122:125]
	v_mfma_f32_16x16x128_f8f6f4 v[114:117], v[26:33], v[226:233], v[114:117]
	v_mfma_f32_16x16x128_f8f6f4 v[106:109], v[18:25], v[234:241], v[106:109]
	v_mfma_f32_16x16x128_f8f6f4 v[98:101], v[26:33], v[234:241], v[98:101]
	s_add_u32 s26, s10, s53
	s_mov_b32 m0, s33
	s_addc_u32 s27, s11, 0
	v_cndmask_b32_e32 v162, v208, v206, vcc
	s_barrier
	ds_read_b128 v[210:213], v203 offset:16384
	ds_read_b128 v[214:217], v203 offset:17408
	ds_read_b128 v[218:221], v203 offset:18432
	ds_read_b128 v[222:225], v203 offset:19456
	ds_read_b128 v[226:229], v203 offset:20480
	ds_read_b128 v[230:233], v203 offset:21504
	ds_read_b128 v[234:237], v203 offset:22528
	ds_read_b128 v[238:241], v203 offset:23552
	v_cndmask_b32_e32 v192, v178, v207, vcc
	global_load_lds_dwordx4 v162, s[26:27]
	s_mov_b32 m0, s34
	v_mov_b32_e32 v193, v163
	global_load_lds_dwordx4 v192, s[26:27]
	s_barrier
	s_waitcnt lgkmcnt(0)
	v_lshl_add_u64 v[194:195], s[26:27], 0, v[162:163]
	v_lshl_add_u64 v[192:193], s[26:27], 0, v[192:193]
	s_waitcnt lgkmcnt(0)
	v_mfma_f32_16x16x128_f8f6f4 v[94:97], v[2:9], v[210:217], v[94:97]
	v_mfma_f32_16x16x128_f8f6f4 v[86:89], v[10:17], v[210:217], v[86:89]
	v_mfma_f32_16x16x128_f8f6f4 v[78:81], v[2:9], v[218:225], v[78:81]
	v_mfma_f32_16x16x128_f8f6f4 v[70:73], v[10:17], v[218:225], v[70:73]
	v_mfma_f32_16x16x128_f8f6f4 v[62:65], v[2:9], v[226:233], v[62:65]
	v_mfma_f32_16x16x128_f8f6f4 v[54:57], v[10:17], v[226:233], v[54:57]
	v_mfma_f32_16x16x128_f8f6f4 v[46:49], v[2:9], v[234:241], v[46:49]
	v_mfma_f32_16x16x128_f8f6f4 v[38:41], v[10:17], v[234:241], v[38:41]
	s_barrier
	s_add_u32 s54, s24, 0x40000
	s_addc_u32 s55, s25, 0
	s_add_i32 s53, s40, s23
	v_lshl_add_u64 v[2:3], s[54:55], 0, v[164:165]
	s_mov_b32 m0, s53
	s_nop 0
	global_load_lds_dwordx4 v[2:3], off
	v_lshl_add_u64 v[2:3], s[54:55], 0, v[166:167]
	s_add_i32 m0, s53, 0x2000
	s_nop 0
	global_load_lds_dwordx4 v[2:3], off
	s_waitcnt vmcnt(6)
	s_barrier
	v_mfma_f32_16x16x128_f8f6f4 v[90:93], v[18:25], v[210:217], v[90:93]
	v_mfma_f32_16x16x128_f8f6f4 v[82:85], v[26:33], v[210:217], v[82:85]
	v_mfma_f32_16x16x128_f8f6f4 v[74:77], v[18:25], v[218:225], v[74:77]
	v_mfma_f32_16x16x128_f8f6f4 v[66:69], v[26:33], v[218:225], v[66:69]
	v_mfma_f32_16x16x128_f8f6f4 v[58:61], v[18:25], v[226:233], v[58:61]
	v_mfma_f32_16x16x128_f8f6f4 v[50:53], v[26:33], v[226:233], v[50:53]
	v_mfma_f32_16x16x128_f8f6f4 v[42:45], v[18:25], v[234:241], v[42:45]
	v_mfma_f32_16x16x128_f8f6f4 v[34:37], v[26:33], v[234:241], v[34:37]
	s_add_i32 s53, 0, 0x18000
	v_add_u32_e32 v14, s53, v201
	s_barrier
	ds_read_b128 v[2:5], v14
	ds_read_b128 v[6:9], v14 offset:1024
	ds_read_b128 v[10:13], v14 offset:2048
	ds_read_b128 v[14:17], v14 offset:3072
	v_cndmask_b32_e32 v172, v180, v174, vcc
	s_mov_b32 m0, s35
	v_cndmask_b32_e32 v226, v182, v176, vcc
	v_mov_b32_e32 v227, v173
	v_lshl_add_u64 v[228:229], s[26:27], 0, v[172:173]
	ds_read_b128 v[18:21], v203 offset:32768
	ds_read_b128 v[22:25], v203 offset:33792
	ds_read_b128 v[26:29], v203 offset:34816
	ds_read_b128 v[30:33], v203 offset:35840
	ds_read_b128 v[210:213], v203 offset:36864
	ds_read_b128 v[214:217], v203 offset:37888
	ds_read_b128 v[218:221], v203 offset:38912
	ds_read_b128 v[222:225], v203 offset:39936
	global_load_lds_dwordx4 v[228:229], off
	v_lshl_add_u64 v[226:227], s[26:27], 0, v[226:227]
	s_mov_b32 m0, s36
	s_nop 0
	global_load_lds_dwordx4 v[226:227], off
	s_waitcnt lgkmcnt(8)
	s_barrier
	s_waitcnt lgkmcnt(0)
	s_waitcnt lgkmcnt(0)
	v_mfma_f32_16x16x128_f8f6f4 v[158:161], v[2:9], v[18:25], v[158:161]
	v_mfma_f32_16x16x128_f8f6f4 v[150:153], v[10:17], v[18:25], v[150:153]
	v_mfma_f32_16x16x128_f8f6f4 v[142:145], v[2:9], v[26:33], v[142:145]
	v_mfma_f32_16x16x128_f8f6f4 v[134:137], v[10:17], v[26:33], v[134:137]
	v_mfma_f32_16x16x128_f8f6f4 v[126:129], v[2:9], v[210:217], v[126:129]
	v_mfma_f32_16x16x128_f8f6f4 v[118:121], v[10:17], v[210:217], v[118:121]
	v_mfma_f32_16x16x128_f8f6f4 v[110:113], v[2:9], v[218:225], v[110:113]
	v_mfma_f32_16x16x128_f8f6f4 v[102:105], v[10:17], v[218:225], v[102:105]
	s_barrier
	s_add_i32 s26, 0, 0x1c000
	s_add_i32 s27, s53, s23
	v_add_u32_e32 v162, s26, v201
	v_lshl_add_u64 v[188:189], v[188:189], 0, s[16:17]
	s_mov_b32 m0, s27
	ds_read_b128 v[226:229], v162
	ds_read_b128 v[230:233], v162 offset:1024
	ds_read_b128 v[234:237], v162 offset:2048
	ds_read_b128 v[238:241], v162 offset:3072
	global_load_lds_dwordx4 v[188:189], off
	v_lshl_add_u64 v[188:189], v[190:191], 0, s[16:17]
	s_add_i32 m0, s27, 0x2000
	s_nop 0
	global_load_lds_dwordx4 v[188:189], off
	s_barrier
	s_waitcnt lgkmcnt(0)
	s_waitcnt lgkmcnt(0)
	v_mfma_f32_16x16x128_f8f6f4 v[154:157], v[226:233], v[18:25], v[154:157]
	v_mfma_f32_16x16x128_f8f6f4 v[146:149], v[234:241], v[18:25], v[146:149]
	v_mfma_f32_16x16x128_f8f6f4 v[138:141], v[226:233], v[26:33], v[138:141]
	v_mfma_f32_16x16x128_f8f6f4 v[130:133], v[234:241], v[26:33], v[130:133]
	v_mfma_f32_16x16x128_f8f6f4 v[122:125], v[226:233], v[210:217], v[122:125]
	v_mfma_f32_16x16x128_f8f6f4 v[114:117], v[234:241], v[210:217], v[114:117]
	v_mfma_f32_16x16x128_f8f6f4 v[106:109], v[226:233], v[218:225], v[106:109]
	v_mfma_f32_16x16x128_f8f6f4 v[98:101], v[234:241], v[218:225], v[98:101]
	s_mov_b32 m0, s37
	v_lshl_add_u64 v[188:189], v[194:195], 0, s[16:17]
	s_barrier
	ds_read_b128 v[18:21], v203 offset:49152
	ds_read_b128 v[22:25], v203 offset:50176
	ds_read_b128 v[26:29], v203 offset:51200
	ds_read_b128 v[30:33], v203 offset:52224
	ds_read_b128 v[210:213], v203 offset:53248
	ds_read_b128 v[214:217], v203 offset:54272
	ds_read_b128 v[218:221], v203 offset:55296
	ds_read_b128 v[222:225], v203 offset:56320
	global_load_lds_dwordx4 v[188:189], off
	v_lshl_add_u64 v[188:189], v[192:193], 0, s[16:17]
	s_mov_b32 m0, s38
	s_nop 0
	global_load_lds_dwordx4 v[188:189], off
	s_barrier
	s_waitcnt lgkmcnt(0)
	s_waitcnt lgkmcnt(0)
	v_mfma_f32_16x16x128_f8f6f4 v[94:97], v[2:9], v[18:25], v[94:97]
	v_mfma_f32_16x16x128_f8f6f4 v[86:89], v[10:17], v[18:25], v[86:89]
	v_mfma_f32_16x16x128_f8f6f4 v[78:81], v[2:9], v[26:33], v[78:81]
	v_mfma_f32_16x16x128_f8f6f4 v[70:73], v[10:17], v[26:33], v[70:73]
	v_mfma_f32_16x16x128_f8f6f4 v[62:65], v[2:9], v[210:217], v[62:65]
	v_mfma_f32_16x16x128_f8f6f4 v[54:57], v[10:17], v[210:217], v[54:57]
	v_mfma_f32_16x16x128_f8f6f4 v[46:49], v[2:9], v[218:225], v[46:49]
	v_mfma_f32_16x16x128_f8f6f4 v[38:41], v[10:17], v[218:225], v[38:41]
	s_barrier
	s_add_u32 s24, s24, 0x40080
	s_addc_u32 s25, s25, 0
	s_add_i32 s26, s26, s23
	v_lshl_add_u64 v[2:3], s[24:25], 0, v[164:165]
	s_mov_b32 m0, s26
	s_nop 0
	global_load_lds_dwordx4 v[2:3], off
	v_lshl_add_u64 v[2:3], s[24:25], 0, v[166:167]
	s_add_i32 m0, s26, 0x2000
	s_nop 0
	global_load_lds_dwordx4 v[2:3], off
	s_waitcnt vmcnt(6)
	s_barrier
	v_mfma_f32_16x16x128_f8f6f4 v[90:93], v[226:233], v[18:25], v[90:93]
	v_mfma_f32_16x16x128_f8f6f4 v[82:85], v[234:241], v[18:25], v[82:85]
	v_mfma_f32_16x16x128_f8f6f4 v[74:77], v[226:233], v[26:33], v[74:77]
	v_mfma_f32_16x16x128_f8f6f4 v[66:69], v[234:241], v[26:33], v[66:69]
	v_mfma_f32_16x16x128_f8f6f4 v[58:61], v[226:233], v[210:217], v[58:61]
	v_mfma_f32_16x16x128_f8f6f4 v[50:53], v[234:241], v[210:217], v[50:53]
	v_mfma_f32_16x16x128_f8f6f4 v[42:45], v[226:233], v[218:225], v[42:45]
	v_mfma_f32_16x16x128_f8f6f4 v[34:37], v[234:241], v[218:225], v[34:37]
	s_add_i32 s52, s52, 2
	s_cmp_gt_u32 s52, 13
	s_mov_b64 s[26:27], s[4:5]
	s_barrier
	s_cbranch_scc0 .LBB0_1060
	v_mov_b32_e32 v2, v158
	v_mov_b32_e32 v3, v154
	v_pk_mul_f32 v[2:3], v[2:3], s[18:19] op_sel_hi:[1,0]
	v_mov_b32_e32 v154, v159
	v_mul_f32_e32 v5, 0xbfb8aa3b, v2
	v_pk_mul_f32 v[6:7], v[154:155], s[18:19] op_sel_hi:[1,0]
	v_exp_f32_e32 v8, v5
	v_mul_f32_e32 v5, 0xbfb8aa3b, v6
	v_exp_f32_e32 v9, v5
	v_mul_f32_e32 v2, v2, v3
	v_add_f32_e32 v8, 1.0, v8
	v_rcp_f32_e32 v8, v8
	v_add_f32_e32 v9, 1.0, v9
	v_rcp_f32_e32 v9, v9
	v_mov_b32_e32 v3, v156
	v_mul_f32_e32 v8, v8, v2
	v_mul_f32_e32 v2, v6, v7
	v_mul_f32_e32 v9, v9, v2
	v_mov_b32_e32 v2, v160
	v_pk_mul_f32 v[2:3], v[2:3], s[18:19] op_sel_hi:[1,0]
	v_mov_b32_e32 v156, v161
	v_mul_f32_e32 v6, 0xbfb8aa3b, v2
	v_exp_f32_e32 v10, v6
	v_pk_mul_f32 v[6:7], v[156:157], s[18:19] op_sel_hi:[1,0]
	v_mul_f32_e32 v12, v2, v3
	v_mul_f32_e32 v11, 0xbfb8aa3b, v6
	v_exp_f32_e32 v11, v11
	v_add_f32_e32 v2, 1.0, v10
	v_rcp_f32_e32 v10, v2
	v_mov_b32_e32 v3, v146
	v_add_f32_e32 v2, 1.0, v11
	v_rcp_f32_e32 v11, v2
	v_mov_b32_e32 v2, v150
	v_pk_mul_f32 v[2:3], v[2:3], s[18:19] op_sel_hi:[1,0]
	v_mul_f32_e32 v6, v6, v7
	v_mul_f32_e32 v13, 0xbfb8aa3b, v2
	v_exp_f32_e32 v13, v13
	v_mul_f32_e32 v11, v11, v6
	v_mov_b32_e32 v146, v151
	v_mul_f32_e32 v10, v10, v12
	v_add_f32_e32 v6, 1.0, v13
	v_rcp_f32_e32 v12, v6
	v_pk_mul_f32 v[6:7], v[146:147], s[18:19] op_sel_hi:[1,0]
	v_mul_f32_e32 v2, v2, v3
	v_mul_f32_e32 v13, 0xbfb8aa3b, v6
	v_exp_f32_e32 v13, v13
	v_mul_f32_e32 v12, v12, v2
	v_mov_b32_e32 v3, v148
	v_mul_f32_e32 v14, v6, v7
	v_add_f32_e32 v2, 1.0, v13
	v_rcp_f32_e32 v13, v2
	v_mov_b32_e32 v2, v152
	v_pk_mul_f32 v[2:3], v[2:3], s[18:19] op_sel_hi:[1,0]
	v_mov_b32_e32 v148, v153
	v_mul_f32_e32 v6, 0xbfb8aa3b, v2
	v_exp_f32_e32 v15, v6
	v_pk_mul_f32 v[6:7], v[148:149], s[18:19] op_sel_hi:[1,0]
	v_mul_f32_e32 v13, v13, v14
	v_mul_f32_e32 v16, 0xbfb8aa3b, v6
	v_exp_f32_e32 v16, v16
	v_add_f32_e32 v14, 1.0, v15
	v_rcp_f32_e32 v14, v14
	v_mul_f32_e32 v2, v2, v3
	v_add_f32_e32 v15, 1.0, v16
	v_rcp_f32_e32 v15, v15
	v_mul_f32_e32 v3, v6, v7
	v_mul_f32_e32 v6, 4.0, v8
	v_mul_f32_e32 v7, 4.0, v9
	v_mul_f32_e32 v8, 4.0, v10
	v_mul_f32_e32 v9, 4.0, v11
	v_mul_f32_e32 v10, 4.0, v12
	v_mul_f32_e32 v11, 4.0, v13
	v_med3_f32 v12, v6, s41, v205
	v_med3_f32 v7, v7, s41, v205
	v_mov_b32_e32 v6, v163
	v_cvt_pk_fp8_f32 v6, v12, v7
	v_med3_f32 v10, v10, s41, v205
	v_med3_f32 v11, v11, s41, v205
	v_mov_b32_e32 v7, v163
	v_cvt_pk_fp8_f32 v7, v10, v11
	v_mul_f32_e32 v2, v14, v2
	v_mul_f32_e32 v3, v15, v3
	v_mul_f32_e32 v2, 4.0, v2
	v_mul_f32_e32 v3, 4.0, v3
	v_lshl_add_u32 v4, s48, 8, v179
	v_med3_f32 v8, v8, s41, v205
	v_med3_f32 v9, v9, s41, v205
	v_med3_f32 v2, v2, s41, v205
	v_med3_f32 v3, v3, s41, v205
	s_lshl_b32 s4, s22, 7
	v_ashrrev_i32_e32 v5, 31, v4
	v_cvt_pk_fp8_f32 v6, v8, v9 op_sel:[0,0,1]
	v_cvt_pk_fp8_f32 v7, v2, v3 op_sel:[0,0,1]
	s_and_b32 s4, s4, 0x780
	v_lshlrev_b64 v[2:3], 11, v[4:5]
	v_mov_b32_e32 v8, v142
	v_mov_b32_e32 v9, v138
	v_or_b32_e32 v162, s4, v202
	v_lshl_add_u64 v[2:3], s[12:13], 0, v[2:3]
	v_pk_mul_f32 v[8:9], v[8:9], s[18:19] op_sel_hi:[1,0]
	v_mov_b32_e32 v138, v143
	v_lshl_add_u64 v[2:3], v[2:3], 0, v[162:163]
	v_mul_f32_e32 v5, 0xbfb8aa3b, v8
	v_pk_mul_f32 v[10:11], v[138:139], s[18:19] op_sel_hi:[1,0]
	s_nop 15
	s_nop 15
	global_store_dwordx2 v[2:3], v[6:7], off
	v_exp_f32_e32 v5, v5
	v_mul_f32_e32 v7, 0xbfb8aa3b, v10
	v_exp_f32_e32 v12, v7
	v_mul_f32_e32 v8, v8, v9
	v_add_f32_e32 v5, 1.0, v5
	v_rcp_f32_e32 v5, v5
	v_add_f32_e32 v12, 1.0, v12
	v_rcp_f32_e32 v12, v12
	v_mov_b32_e32 v9, v140
	v_mul_f32_e32 v5, v5, v8
	v_mul_f32_e32 v8, v10, v11
	v_mul_f32_e32 v12, v12, v8
	v_mov_b32_e32 v8, v144
	v_pk_mul_f32 v[8:9], v[8:9], s[18:19] op_sel_hi:[1,0]
	v_mov_b32_e32 v140, v145
	v_mul_f32_e32 v10, 0xbfb8aa3b, v8
	v_exp_f32_e32 v13, v10
	v_pk_mul_f32 v[10:11], v[140:141], s[18:19] op_sel_hi:[1,0]
	v_mul_f32_e32 v15, v8, v9
	v_mul_f32_e32 v14, 0xbfb8aa3b, v10
	v_exp_f32_e32 v14, v14
	v_add_f32_e32 v8, 1.0, v13
	v_rcp_f32_e32 v13, v8
	v_mov_b32_e32 v9, v130
	v_add_f32_e32 v8, 1.0, v14
	v_rcp_f32_e32 v14, v8
	v_mov_b32_e32 v8, v134
	v_pk_mul_f32 v[8:9], v[8:9], s[18:19] op_sel_hi:[1,0]
	v_mul_f32_e32 v10, v10, v11
	v_mul_f32_e32 v16, 0xbfb8aa3b, v8
	v_exp_f32_e32 v16, v16
	v_mul_f32_e32 v14, v14, v10
	v_mov_b32_e32 v130, v135
	v_mul_f32_e32 v13, v13, v15
	v_add_f32_e32 v10, 1.0, v16
	v_rcp_f32_e32 v15, v10
	v_pk_mul_f32 v[10:11], v[130:131], s[18:19] op_sel_hi:[1,0]
	v_mul_f32_e32 v8, v8, v9
	v_mul_f32_e32 v16, 0xbfb8aa3b, v10
	v_exp_f32_e32 v16, v16
	v_mul_f32_e32 v15, v15, v8
	v_mov_b32_e32 v9, v132
	v_mul_f32_e32 v17, v10, v11
	v_add_f32_e32 v8, 1.0, v16
	v_rcp_f32_e32 v16, v8
	v_mov_b32_e32 v8, v136
	v_pk_mul_f32 v[8:9], v[8:9], s[18:19] op_sel_hi:[1,0]
	v_mov_b32_e32 v132, v137
	v_mul_f32_e32 v10, 0xbfb8aa3b, v8
	v_exp_f32_e32 v18, v10
	v_pk_mul_f32 v[10:11], v[132:133], s[18:19] op_sel_hi:[1,0]
	v_mul_f32_e32 v16, v16, v17
	v_mul_f32_e32 v19, 0xbfb8aa3b, v10
	v_exp_f32_e32 v19, v19
	v_add_f32_e32 v17, 1.0, v18
	v_rcp_f32_e32 v17, v17
	v_mul_f32_e32 v8, v8, v9
	v_add_f32_e32 v18, 1.0, v19
	v_rcp_f32_e32 v18, v18
	v_mul_f32_e32 v9, v10, v11
	v_mul_f32_e32 v8, v17, v8
	v_mul_f32_e32 v5, 4.0, v5
	v_mul_f32_e32 v9, v18, v9
	v_mul_f32_e32 v10, 4.0, v12
	v_mul_f32_e32 v11, 4.0, v13
	v_mul_f32_e32 v12, 4.0, v14
	v_mul_f32_e32 v13, 4.0, v15
	v_mul_f32_e32 v14, 4.0, v16
	v_mul_f32_e32 v15, 4.0, v8
	v_mul_f32_e32 v16, 4.0, v9
	v_med3_f32 v5, v5, s41, v205
	v_med3_f32 v9, v10, s41, v205
	v_mov_b32_e32 v8, v163
	v_cvt_pk_fp8_f32 v8, v5, v9
	v_med3_f32 v5, v11, s41, v205
	v_med3_f32 v10, v12, s41, v205
	v_med3_f32 v11, v13, s41, v205
	v_med3_f32 v12, v14, s41, v205
	v_mov_b32_e32 v9, v163
	v_cvt_pk_fp8_f32 v9, v11, v12
	v_or_b32_e32 v6, 16, v4
	v_cvt_pk_fp8_f32 v8, v5, v10 op_sel:[0,0,1]
	v_med3_f32 v5, v15, s41, v205
	v_med3_f32 v10, v16, s41, v205
	v_ashrrev_i32_e32 v7, 31, v6
	v_cvt_pk_fp8_f32 v9, v5, v10 op_sel:[0,0,1]
	v_lshlrev_b64 v[6:7], 11, v[6:7]
	v_lshl_add_u64 v[6:7], s[12:13], 0, v[6:7]
	v_lshl_add_u64 v[6:7], v[6:7], 0, v[162:163]
	global_store_dwordx2 v[6:7], v[8:9], off
	v_mov_b32_e32 v8, v126
	v_mov_b32_e32 v9, v122
	v_pk_mul_f32 v[8:9], v[8:9], s[18:19] op_sel_hi:[1,0]
	v_mov_b32_e32 v122, v127
	v_mul_f32_e32 v5, 0xbfb8aa3b, v8
	v_pk_mul_f32 v[10:11], v[122:123], s[18:19] op_sel_hi:[1,0]
	v_exp_f32_e32 v5, v5
	v_mul_f32_e32 v7, 0xbfb8aa3b, v10
	v_exp_f32_e32 v12, v7
	v_mul_f32_e32 v8, v8, v9
	v_add_f32_e32 v5, 1.0, v5
	v_rcp_f32_e32 v5, v5
	v_add_f32_e32 v12, 1.0, v12
	v_rcp_f32_e32 v12, v12
	v_mov_b32_e32 v9, v124
	v_mul_f32_e32 v5, v5, v8
	v_mul_f32_e32 v8, v10, v11
	v_mul_f32_e32 v12, v12, v8
	v_mov_b32_e32 v8, v128
	v_pk_mul_f32 v[8:9], v[8:9], s[18:19] op_sel_hi:[1,0]
	v_mov_b32_e32 v124, v129
	v_mul_f32_e32 v10, 0xbfb8aa3b, v8
	v_exp_f32_e32 v13, v10
	v_pk_mul_f32 v[10:11], v[124:125], s[18:19] op_sel_hi:[1,0]
	v_mul_f32_e32 v15, v8, v9
	v_mul_f32_e32 v14, 0xbfb8aa3b, v10
	v_exp_f32_e32 v14, v14
	v_add_f32_e32 v8, 1.0, v13
	v_rcp_f32_e32 v13, v8
	v_mov_b32_e32 v9, v114
	v_add_f32_e32 v8, 1.0, v14
	v_rcp_f32_e32 v14, v8
	v_mov_b32_e32 v8, v118
	v_pk_mul_f32 v[8:9], v[8:9], s[18:19] op_sel_hi:[1,0]
	v_mul_f32_e32 v10, v10, v11
	v_mul_f32_e32 v16, 0xbfb8aa3b, v8
	v_exp_f32_e32 v16, v16
	v_mul_f32_e32 v14, v14, v10
	v_mov_b32_e32 v114, v119
	v_mul_f32_e32 v13, v13, v15
	v_add_f32_e32 v10, 1.0, v16
	v_rcp_f32_e32 v15, v10
	v_pk_mul_f32 v[10:11], v[114:115], s[18:19] op_sel_hi:[1,0]
	v_mul_f32_e32 v8, v8, v9
	v_mul_f32_e32 v16, 0xbfb8aa3b, v10
	v_exp_f32_e32 v16, v16
	v_mul_f32_e32 v15, v15, v8
	v_mov_b32_e32 v9, v116
	v_mul_f32_e32 v17, v10, v11
	v_add_f32_e32 v8, 1.0, v16
	v_rcp_f32_e32 v16, v8
	v_mov_b32_e32 v8, v120
	v_pk_mul_f32 v[8:9], v[8:9], s[18:19] op_sel_hi:[1,0]
	v_mov_b32_e32 v116, v121
	v_mul_f32_e32 v10, 0xbfb8aa3b, v8
	v_exp_f32_e32 v18, v10
	v_pk_mul_f32 v[10:11], v[116:117], s[18:19] op_sel_hi:[1,0]
	v_mul_f32_e32 v16, v16, v17
	v_mul_f32_e32 v19, 0xbfb8aa3b, v10
	v_exp_f32_e32 v19, v19
	v_add_f32_e32 v17, 1.0, v18
	v_rcp_f32_e32 v17, v17
	v_mul_f32_e32 v8, v8, v9
	v_add_f32_e32 v18, 1.0, v19
	v_rcp_f32_e32 v18, v18
	v_mul_f32_e32 v9, v10, v11
	v_mul_f32_e32 v8, v17, v8
	v_mul_f32_e32 v5, 4.0, v5
	v_mul_f32_e32 v9, v18, v9
	v_mul_f32_e32 v10, 4.0, v12
	v_mul_f32_e32 v11, 4.0, v13
	v_mul_f32_e32 v12, 4.0, v14
	v_mul_f32_e32 v13, 4.0, v15
	v_mul_f32_e32 v14, 4.0, v16
	v_mul_f32_e32 v15, 4.0, v8
	v_mul_f32_e32 v16, 4.0, v9
	v_med3_f32 v5, v5, s41, v205
	v_med3_f32 v9, v10, s41, v205
	v_mov_b32_e32 v8, v163
	v_cvt_pk_fp8_f32 v8, v5, v9
	v_med3_f32 v5, v11, s41, v205
	v_med3_f32 v10, v12, s41, v205
	v_med3_f32 v11, v13, s41, v205
	v_med3_f32 v12, v14, s41, v205
	v_mov_b32_e32 v9, v163
	v_cvt_pk_fp8_f32 v9, v11, v12
	v_or_b32_e32 v6, 32, v4
	v_cvt_pk_fp8_f32 v8, v5, v10 op_sel:[0,0,1]
	v_med3_f32 v5, v15, s41, v205
	v_med3_f32 v10, v16, s41, v205
	v_ashrrev_i32_e32 v7, 31, v6
	v_cvt_pk_fp8_f32 v9, v5, v10 op_sel:[0,0,1]
	v_lshlrev_b64 v[6:7], 11, v[6:7]
	v_lshl_add_u64 v[6:7], s[12:13], 0, v[6:7]
	v_lshl_add_u64 v[6:7], v[6:7], 0, v[162:163]
	global_store_dwordx2 v[6:7], v[8:9], off
	v_mov_b32_e32 v6, v110
	v_mov_b32_e32 v7, v106
	v_pk_mul_f32 v[6:7], v[6:7], s[18:19] op_sel_hi:[1,0]
	v_mov_b32_e32 v106, v111
	v_mul_f32_e32 v8, 0xbfb8aa3b, v6
	v_exp_f32_e32 v10, v8
	v_pk_mul_f32 v[8:9], v[106:107], s[18:19] op_sel_hi:[1,0]
	v_mul_f32_e32 v6, v6, v7
	v_mul_f32_e32 v11, 0xbfb8aa3b, v8
	v_exp_f32_e32 v11, v11
	v_add_f32_e32 v10, 1.0, v10
	v_rcp_f32_e32 v10, v10
	v_mov_b32_e32 v7, v108
	v_add_f32_e32 v11, 1.0, v11
	v_rcp_f32_e32 v11, v11
	v_mul_f32_e32 v10, v10, v6
	v_mul_f32_e32 v6, v8, v9
	v_mov_b32_e32 v108, v113
	v_mul_f32_e32 v11, v11, v6
	v_mov_b32_e32 v6, v112
	v_pk_mul_f32 v[6:7], v[6:7], s[18:19] op_sel_hi:[1,0]
	v_or_b32_e32 v4, 48, v4
	v_mul_f32_e32 v8, 0xbfb8aa3b, v6
	v_exp_f32_e32 v12, v8
	v_pk_mul_f32 v[8:9], v[108:109], s[18:19] op_sel_hi:[1,0]
	v_mul_f32_e32 v14, v6, v7
	v_mul_f32_e32 v13, 0xbfb8aa3b, v8
	v_exp_f32_e32 v13, v13
	v_add_f32_e32 v6, 1.0, v12
	v_rcp_f32_e32 v12, v6
	v_mov_b32_e32 v7, v98
	v_add_f32_e32 v6, 1.0, v13
	v_rcp_f32_e32 v13, v6
	v_mov_b32_e32 v6, v102
	v_pk_mul_f32 v[6:7], v[6:7], s[18:19] op_sel_hi:[1,0]
	v_mul_f32_e32 v8, v8, v9
	v_mul_f32_e32 v15, 0xbfb8aa3b, v6
	v_exp_f32_e32 v15, v15
	v_mul_f32_e32 v13, v13, v8
	v_mov_b32_e32 v98, v103
	v_mul_f32_e32 v12, v12, v14
	v_add_f32_e32 v8, 1.0, v15
	v_rcp_f32_e32 v14, v8
	v_pk_mul_f32 v[8:9], v[98:99], s[18:19] op_sel_hi:[1,0]
	v_mul_f32_e32 v6, v6, v7
	v_mul_f32_e32 v15, 0xbfb8aa3b, v8
	v_exp_f32_e32 v15, v15
	v_mul_f32_e32 v14, v14, v6
	v_mov_b32_e32 v7, v100
	v_mul_f32_e32 v16, v8, v9
	v_add_f32_e32 v6, 1.0, v15
	v_rcp_f32_e32 v15, v6
	v_mov_b32_e32 v6, v104
	v_pk_mul_f32 v[6:7], v[6:7], s[18:19] op_sel_hi:[1,0]
	v_mov_b32_e32 v100, v105
	v_mul_f32_e32 v8, 0xbfb8aa3b, v6
	v_exp_f32_e32 v17, v8
	v_pk_mul_f32 v[8:9], v[100:101], s[18:19] op_sel_hi:[1,0]
	v_mul_f32_e32 v15, v15, v16
	v_mul_f32_e32 v18, 0xbfb8aa3b, v8
	v_exp_f32_e32 v18, v18
	v_add_f32_e32 v16, 1.0, v17
	v_rcp_f32_e32 v16, v16
	v_mul_f32_e32 v6, v6, v7
	v_add_f32_e32 v17, 1.0, v18
	v_rcp_f32_e32 v17, v17
	v_mul_f32_e32 v7, v8, v9
	v_mul_f32_e32 v6, v16, v6
	v_mul_f32_e32 v8, 4.0, v10
	v_mul_f32_e32 v7, v17, v7
	v_mul_f32_e32 v9, 4.0, v11
	v_mul_f32_e32 v10, 4.0, v12
	v_mul_f32_e32 v11, 4.0, v13
	v_mul_f32_e32 v12, 4.0, v14
	v_mul_f32_e32 v13, 4.0, v15
	v_mul_f32_e32 v14, 4.0, v6
	v_mul_f32_e32 v15, 4.0, v7
	v_med3_f32 v7, v8, s41, v205
	v_med3_f32 v8, v9, s41, v205
	v_mov_b32_e32 v6, v163
	v_cvt_pk_fp8_f32 v6, v7, v8
	v_med3_f32 v8, v10, s41, v205
	v_med3_f32 v9, v11, s41, v205
	v_med3_f32 v10, v12, s41, v205
	v_med3_f32 v11, v13, s41, v205
	v_mov_b32_e32 v7, v163
	v_cvt_pk_fp8_f32 v7, v10, v11
	v_cvt_pk_fp8_f32 v6, v8, v9 op_sel:[0,0,1]
	v_med3_f32 v8, v14, s41, v205
	v_med3_f32 v9, v15, s41, v205
	v_cvt_pk_fp8_f32 v7, v8, v9 op_sel:[0,0,1]
	v_mov_b32_e32 v8, v94
	v_mov_b32_e32 v9, v90
	v_pk_mul_f32 v[8:9], v[8:9], s[18:19] op_sel_hi:[1,0]
	v_mov_b32_e32 v90, v95
	v_mul_f32_e32 v10, 0xbfb8aa3b, v8
	v_exp_f32_e32 v12, v10
	v_pk_mul_f32 v[10:11], v[90:91], s[18:19] op_sel_hi:[1,0]
	v_ashrrev_i32_e32 v5, 31, v4
	v_mul_f32_e32 v13, 0xbfb8aa3b, v10
	v_lshlrev_b64 v[4:5], 11, v[4:5]
	v_exp_f32_e32 v13, v13
	v_lshl_add_u64 v[4:5], s[12:13], 0, v[4:5]
	v_lshl_add_u64 v[4:5], v[4:5], 0, v[162:163]
	global_store_dwordx2 v[4:5], v[6:7], off
	v_add_f32_e32 v4, 1.0, v12
	v_rcp_f32_e32 v4, v4
	v_add_f32_e32 v5, 1.0, v13
	v_rcp_f32_e32 v5, v5
	v_mul_f32_e32 v6, v8, v9
	v_mul_f32_e32 v8, v4, v6
	v_mul_f32_e32 v4, v10, v11
	v_mul_f32_e32 v9, v5, v4
	v_mov_b32_e32 v4, v96
	v_mov_b32_e32 v5, v92
	v_pk_mul_f32 v[4:5], v[4:5], s[18:19] op_sel_hi:[1,0]
	v_mov_b32_e32 v92, v97
	v_mul_f32_e32 v6, 0xbfb8aa3b, v4
	v_exp_f32_e32 v10, v6
	v_pk_mul_f32 v[6:7], v[92:93], s[18:19] op_sel_hi:[1,0]
	v_mul_f32_e32 v12, v4, v5
	v_mul_f32_e32 v11, 0xbfb8aa3b, v6
	v_exp_f32_e32 v11, v11
	v_add_f32_e32 v4, 1.0, v10
	v_rcp_f32_e32 v10, v4
	v_mov_b32_e32 v5, v82
	v_add_f32_e32 v4, 1.0, v11
	v_rcp_f32_e32 v11, v4
	v_mov_b32_e32 v4, v86
	v_pk_mul_f32 v[4:5], v[4:5], s[18:19] op_sel_hi:[1,0]
	v_mul_f32_e32 v6, v6, v7
	v_mul_f32_e32 v13, 0xbfb8aa3b, v4
	v_exp_f32_e32 v13, v13
	v_mul_f32_e32 v11, v11, v6
	v_mov_b32_e32 v82, v87
	v_mul_f32_e32 v10, v10, v12
	v_add_f32_e32 v6, 1.0, v13
	v_rcp_f32_e32 v12, v6
	v_pk_mul_f32 v[6:7], v[82:83], s[18:19] op_sel_hi:[1,0]
	v_mul_f32_e32 v4, v4, v5
	v_mul_f32_e32 v13, 0xbfb8aa3b, v6
	v_exp_f32_e32 v13, v13
	v_mul_f32_e32 v12, v12, v4
	v_mov_b32_e32 v5, v84
	v_mul_f32_e32 v14, v6, v7
	v_add_f32_e32 v4, 1.0, v13
	v_rcp_f32_e32 v13, v4
	v_mov_b32_e32 v4, v88
	v_pk_mul_f32 v[4:5], v[4:5], s[18:19] op_sel_hi:[1,0]
	v_mov_b32_e32 v84, v89
	v_mul_f32_e32 v6, 0xbfb8aa3b, v4
	v_exp_f32_e32 v15, v6
	v_pk_mul_f32 v[6:7], v[84:85], s[18:19] op_sel_hi:[1,0]
	v_mul_f32_e32 v13, v13, v14
	v_mul_f32_e32 v16, 0xbfb8aa3b, v6
	v_exp_f32_e32 v16, v16
	v_add_f32_e32 v14, 1.0, v15
	v_rcp_f32_e32 v14, v14
	v_mul_f32_e32 v4, v4, v5
	v_add_f32_e32 v15, 1.0, v16
	v_rcp_f32_e32 v15, v15
	v_mul_f32_e32 v5, v6, v7
	v_mul_f32_e32 v4, v14, v4
	v_mul_f32_e32 v6, 4.0, v8
	v_mul_f32_e32 v5, v15, v5
	v_mul_f32_e32 v7, 4.0, v9
	v_mul_f32_e32 v8, 4.0, v10
	v_mul_f32_e32 v9, 4.0, v11
	v_mul_f32_e32 v10, 4.0, v12
	v_mul_f32_e32 v11, 4.0, v13
	v_mul_f32_e32 v12, 4.0, v4
	v_mul_f32_e32 v13, 4.0, v5
	v_med3_f32 v5, v6, s41, v205
	v_med3_f32 v6, v7, s41, v205
	v_mov_b32_e32 v4, v163
	v_cvt_pk_fp8_f32 v4, v5, v6
	v_med3_f32 v6, v8, s41, v205
	v_med3_f32 v7, v9, s41, v205
	v_med3_f32 v8, v10, s41, v205
	v_med3_f32 v9, v11, s41, v205
	v_mov_b32_e32 v5, v163
	v_cvt_pk_fp8_f32 v5, v8, v9
	v_mov_b32_e32 v8, v78
	v_mov_b32_e32 v9, v74
	v_pk_mul_f32 v[8:9], v[8:9], s[18:19] op_sel_hi:[1,0]
	v_mov_b32_e32 v74, v79
	v_mul_f32_e32 v10, 0xbfb8aa3b, v8
	v_cvt_pk_fp8_f32 v4, v6, v7 op_sel:[0,0,1]
	v_med3_f32 v6, v12, s41, v205
	v_med3_f32 v7, v13, s41, v205
	v_exp_f32_e32 v12, v10
	v_pk_mul_f32 v[10:11], v[74:75], s[18:19] op_sel_hi:[1,0]
	v_cvt_pk_fp8_f32 v5, v6, v7 op_sel:[0,0,1]
	v_mul_f32_e32 v13, 0xbfb8aa3b, v10
	v_exp_f32_e32 v13, v13
	v_add_co_u32_e32 v6, vcc, s42, v2
	v_mov_b32_e32 v182, v176
	s_nop 0
	v_addc_co_u32_e32 v7, vcc, 0, v3, vcc
	global_store_dwordx2 v[6:7], v[4:5], off
	v_add_f32_e32 v4, 1.0, v12
	v_rcp_f32_e32 v4, v4
	v_add_f32_e32 v5, 1.0, v13
	v_rcp_f32_e32 v5, v5
	v_mul_f32_e32 v6, v8, v9
	v_mul_f32_e32 v8, v4, v6
	v_mul_f32_e32 v4, v10, v11
	v_mul_f32_e32 v9, v5, v4
	v_mov_b32_e32 v4, v80
	v_mov_b32_e32 v5, v76
	v_pk_mul_f32 v[4:5], v[4:5], s[18:19] op_sel_hi:[1,0]
	v_mov_b32_e32 v76, v81
	v_mul_f32_e32 v6, 0xbfb8aa3b, v4
	v_exp_f32_e32 v10, v6
	v_pk_mul_f32 v[6:7], v[76:77], s[18:19] op_sel_hi:[1,0]
	v_mul_f32_e32 v12, v4, v5
	v_mul_f32_e32 v11, 0xbfb8aa3b, v6
	v_exp_f32_e32 v11, v11
	v_add_f32_e32 v4, 1.0, v10
	v_rcp_f32_e32 v10, v4
	v_mov_b32_e32 v5, v66
	v_add_f32_e32 v4, 1.0, v11
	v_rcp_f32_e32 v11, v4
	v_mov_b32_e32 v4, v70
	v_pk_mul_f32 v[4:5], v[4:5], s[18:19] op_sel_hi:[1,0]
	v_mul_f32_e32 v6, v6, v7
	v_mul_f32_e32 v13, 0xbfb8aa3b, v4
	v_exp_f32_e32 v13, v13
	v_mul_f32_e32 v11, v11, v6
	v_mov_b32_e32 v66, v71
	v_mul_f32_e32 v10, v10, v12
	v_add_f32_e32 v6, 1.0, v13
	v_rcp_f32_e32 v12, v6
	v_pk_mul_f32 v[6:7], v[66:67], s[18:19] op_sel_hi:[1,0]
	v_mul_f32_e32 v4, v4, v5
	v_mul_f32_e32 v13, 0xbfb8aa3b, v6
	v_exp_f32_e32 v13, v13
	v_mul_f32_e32 v12, v12, v4
	v_mov_b32_e32 v5, v68
	v_mul_f32_e32 v14, v6, v7
	v_add_f32_e32 v4, 1.0, v13
	v_rcp_f32_e32 v13, v4
	v_mov_b32_e32 v4, v72
	v_pk_mul_f32 v[4:5], v[4:5], s[18:19] op_sel_hi:[1,0]
	v_mov_b32_e32 v68, v73
	v_mul_f32_e32 v6, 0xbfb8aa3b, v4
	v_exp_f32_e32 v15, v6
	v_pk_mul_f32 v[6:7], v[68:69], s[18:19] op_sel_hi:[1,0]
	v_mul_f32_e32 v13, v13, v14
	v_mul_f32_e32 v16, 0xbfb8aa3b, v6
	v_exp_f32_e32 v16, v16
	v_add_f32_e32 v14, 1.0, v15
	v_rcp_f32_e32 v14, v14
	v_mul_f32_e32 v4, v4, v5
	v_add_f32_e32 v15, 1.0, v16
	v_rcp_f32_e32 v15, v15
	v_mul_f32_e32 v5, v6, v7
	v_mul_f32_e32 v4, v14, v4
	v_mul_f32_e32 v6, 4.0, v8
	v_mul_f32_e32 v5, v15, v5
	v_mul_f32_e32 v7, 4.0, v9
	v_mul_f32_e32 v8, 4.0, v10
	v_mul_f32_e32 v9, 4.0, v11
	v_mul_f32_e32 v10, 4.0, v12
	v_mul_f32_e32 v11, 4.0, v13
	v_mul_f32_e32 v12, 4.0, v4
	v_mul_f32_e32 v13, 4.0, v5
	v_med3_f32 v5, v6, s41, v205
	v_med3_f32 v6, v7, s41, v205
	v_mov_b32_e32 v4, v163
	v_cvt_pk_fp8_f32 v4, v5, v6
	v_med3_f32 v6, v8, s41, v205
	v_med3_f32 v7, v9, s41, v205
	v_med3_f32 v8, v10, s41, v205
	v_med3_f32 v9, v11, s41, v205
	v_mov_b32_e32 v5, v163
	v_cvt_pk_fp8_f32 v5, v8, v9
	v_mov_b32_e32 v8, v62
	v_mov_b32_e32 v9, v58
	v_pk_mul_f32 v[8:9], v[8:9], s[18:19] op_sel_hi:[1,0]
	v_mov_b32_e32 v58, v63
	v_mul_f32_e32 v10, 0xbfb8aa3b, v8
	v_cvt_pk_fp8_f32 v4, v6, v7 op_sel:[0,0,1]
	v_med3_f32 v6, v12, s41, v205
	v_med3_f32 v7, v13, s41, v205
	v_exp_f32_e32 v12, v10
	v_pk_mul_f32 v[10:11], v[58:59], s[18:19] op_sel_hi:[1,0]
	v_cvt_pk_fp8_f32 v5, v6, v7 op_sel:[0,0,1]
	v_mul_f32_e32 v13, 0xbfb8aa3b, v10
	v_exp_f32_e32 v13, v13
	v_add_co_u32_e32 v6, vcc, s43, v2
	v_mov_b32_e32 v180, v174
	s_nop 0
	v_addc_co_u32_e32 v7, vcc, 0, v3, vcc
	global_store_dwordx2 v[6:7], v[4:5], off
	v_add_f32_e32 v4, 1.0, v12
	v_rcp_f32_e32 v4, v4
	v_add_f32_e32 v5, 1.0, v13
	v_rcp_f32_e32 v5, v5
	v_mul_f32_e32 v6, v8, v9
	v_mul_f32_e32 v8, v4, v6
	v_mul_f32_e32 v4, v10, v11
	v_mul_f32_e32 v9, v5, v4
	v_mov_b32_e32 v4, v64
	v_mov_b32_e32 v5, v60
	v_pk_mul_f32 v[4:5], v[4:5], s[18:19] op_sel_hi:[1,0]
	v_mov_b32_e32 v60, v65
	v_mul_f32_e32 v6, 0xbfb8aa3b, v4
	v_exp_f32_e32 v10, v6
	v_pk_mul_f32 v[6:7], v[60:61], s[18:19] op_sel_hi:[1,0]
	v_mul_f32_e32 v12, v4, v5
	v_mul_f32_e32 v11, 0xbfb8aa3b, v6
	v_exp_f32_e32 v11, v11
	v_add_f32_e32 v4, 1.0, v10
	v_rcp_f32_e32 v10, v4
	v_mov_b32_e32 v5, v50
	v_add_f32_e32 v4, 1.0, v11
	v_rcp_f32_e32 v11, v4
	v_mov_b32_e32 v4, v54
	v_pk_mul_f32 v[4:5], v[4:5], s[18:19] op_sel_hi:[1,0]
	v_mul_f32_e32 v6, v6, v7
	v_mul_f32_e32 v13, 0xbfb8aa3b, v4
	v_exp_f32_e32 v13, v13
	v_mul_f32_e32 v11, v11, v6
	v_mov_b32_e32 v50, v55
	v_mul_f32_e32 v10, v10, v12
	v_add_f32_e32 v6, 1.0, v13
	v_rcp_f32_e32 v12, v6
	v_pk_mul_f32 v[6:7], v[50:51], s[18:19] op_sel_hi:[1,0]
	v_mul_f32_e32 v4, v4, v5
	v_mul_f32_e32 v13, 0xbfb8aa3b, v6
	v_exp_f32_e32 v13, v13
	v_mul_f32_e32 v12, v12, v4
	v_mov_b32_e32 v5, v52
	v_mul_f32_e32 v14, v6, v7
	v_add_f32_e32 v4, 1.0, v13
	v_rcp_f32_e32 v13, v4
	v_mov_b32_e32 v4, v56
	v_pk_mul_f32 v[4:5], v[4:5], s[18:19] op_sel_hi:[1,0]
	v_mov_b32_e32 v52, v57
	v_mul_f32_e32 v6, 0xbfb8aa3b, v4
	v_exp_f32_e32 v15, v6
	v_pk_mul_f32 v[6:7], v[52:53], s[18:19] op_sel_hi:[1,0]
	v_mul_f32_e32 v13, v13, v14
	v_mul_f32_e32 v16, 0xbfb8aa3b, v6
	v_exp_f32_e32 v16, v16
	v_add_f32_e32 v14, 1.0, v15
	v_rcp_f32_e32 v14, v14
	v_mul_f32_e32 v4, v4, v5
	v_add_f32_e32 v15, 1.0, v16
	v_rcp_f32_e32 v15, v15
	v_mul_f32_e32 v5, v6, v7
	v_mul_f32_e32 v4, v14, v4
	v_mul_f32_e32 v6, 4.0, v8
	v_mul_f32_e32 v5, v15, v5
	v_mul_f32_e32 v7, 4.0, v9
	v_mul_f32_e32 v8, 4.0, v10
	v_mul_f32_e32 v9, 4.0, v11
	v_mul_f32_e32 v10, 4.0, v12
	v_mul_f32_e32 v11, 4.0, v13
	v_mul_f32_e32 v12, 4.0, v4
	v_mul_f32_e32 v13, 4.0, v5
	v_med3_f32 v5, v6, s41, v205
	v_med3_f32 v6, v7, s41, v205
	v_mov_b32_e32 v4, v163
	v_cvt_pk_fp8_f32 v4, v5, v6
	v_med3_f32 v6, v8, s41, v205
	v_med3_f32 v7, v9, s41, v205
	v_med3_f32 v8, v10, s41, v205
	v_med3_f32 v9, v11, s41, v205
	v_mov_b32_e32 v5, v163
	v_cvt_pk_fp8_f32 v5, v8, v9
	v_mov_b32_e32 v8, v46
	v_mov_b32_e32 v9, v42
	v_pk_mul_f32 v[8:9], v[8:9], s[18:19] op_sel_hi:[1,0]
	v_mov_b32_e32 v42, v47
	v_mul_f32_e32 v10, 0xbfb8aa3b, v8
	v_cvt_pk_fp8_f32 v4, v6, v7 op_sel:[0,0,1]
	v_med3_f32 v6, v12, s41, v205
	v_med3_f32 v7, v13, s41, v205
	v_exp_f32_e32 v12, v10
	v_pk_mul_f32 v[10:11], v[42:43], s[18:19] op_sel_hi:[1,0]
	v_cvt_pk_fp8_f32 v5, v6, v7 op_sel:[0,0,1]
	v_mul_f32_e32 v13, 0xbfb8aa3b, v10
	v_exp_f32_e32 v13, v13
	v_add_co_u32_e32 v6, vcc, s44, v2
	v_mov_b32_e32 v178, v207
	s_nop 0
	v_addc_co_u32_e32 v7, vcc, 0, v3, vcc
	global_store_dwordx2 v[6:7], v[4:5], off
	v_add_f32_e32 v4, 1.0, v12
	v_rcp_f32_e32 v4, v4
	v_add_f32_e32 v5, 1.0, v13
	v_rcp_f32_e32 v5, v5
	v_mul_f32_e32 v6, v8, v9
	v_mul_f32_e32 v8, v4, v6
	v_mul_f32_e32 v4, v10, v11
	v_mul_f32_e32 v9, v5, v4
	v_mov_b32_e32 v4, v48
	v_mov_b32_e32 v5, v44
	v_pk_mul_f32 v[4:5], v[4:5], s[18:19] op_sel_hi:[1,0]
	v_mov_b32_e32 v44, v49
	v_mul_f32_e32 v6, 0xbfb8aa3b, v4
	v_exp_f32_e32 v10, v6
	v_pk_mul_f32 v[6:7], v[44:45], s[18:19] op_sel_hi:[1,0]
	v_mul_f32_e32 v12, v4, v5
	v_mul_f32_e32 v11, 0xbfb8aa3b, v6
	v_exp_f32_e32 v11, v11
	v_add_f32_e32 v4, 1.0, v10
	v_rcp_f32_e32 v10, v4
	v_mov_b32_e32 v5, v34
	v_add_f32_e32 v4, 1.0, v11
	v_rcp_f32_e32 v11, v4
	v_mov_b32_e32 v4, v38
	v_pk_mul_f32 v[4:5], v[4:5], s[18:19] op_sel_hi:[1,0]
	v_mul_f32_e32 v6, v6, v7
	v_mul_f32_e32 v13, 0xbfb8aa3b, v4
	v_exp_f32_e32 v13, v13
	v_mul_f32_e32 v11, v11, v6
	v_mov_b32_e32 v34, v39
	v_mul_f32_e32 v10, v10, v12
	v_add_f32_e32 v6, 1.0, v13
	v_rcp_f32_e32 v12, v6
	v_pk_mul_f32 v[6:7], v[34:35], s[18:19] op_sel_hi:[1,0]
	v_mul_f32_e32 v4, v4, v5
	v_mul_f32_e32 v13, 0xbfb8aa3b, v6
	v_exp_f32_e32 v13, v13
	v_mul_f32_e32 v12, v12, v4
	v_mov_b32_e32 v5, v36
	v_mul_f32_e32 v14, v6, v7
	v_add_f32_e32 v4, 1.0, v13
	v_rcp_f32_e32 v13, v4
	v_mov_b32_e32 v4, v40
	v_pk_mul_f32 v[4:5], v[4:5], s[18:19] op_sel_hi:[1,0]
	v_mov_b32_e32 v36, v41
	v_mul_f32_e32 v6, 0xbfb8aa3b, v4
	v_exp_f32_e32 v15, v6
	v_pk_mul_f32 v[6:7], v[36:37], s[18:19] op_sel_hi:[1,0]
	v_mul_f32_e32 v13, v13, v14
	v_mul_f32_e32 v16, 0xbfb8aa3b, v6
	v_exp_f32_e32 v16, v16
	v_add_f32_e32 v14, 1.0, v15
	v_rcp_f32_e32 v14, v14
	v_mul_f32_e32 v4, v4, v5
	v_add_f32_e32 v15, 1.0, v16
	v_rcp_f32_e32 v15, v15
	v_mul_f32_e32 v5, v6, v7
	v_mul_f32_e32 v4, v14, v4
	v_mul_f32_e32 v6, 4.0, v8
	v_mul_f32_e32 v5, v15, v5
	v_mul_f32_e32 v7, 4.0, v9
	v_mul_f32_e32 v8, 4.0, v10
	v_mul_f32_e32 v9, 4.0, v11
	v_mul_f32_e32 v10, 4.0, v12
	v_mul_f32_e32 v11, 4.0, v13
	v_mul_f32_e32 v12, 4.0, v4
	v_mul_f32_e32 v13, 4.0, v5
	v_med3_f32 v5, v6, s41, v205
	v_med3_f32 v6, v7, s41, v205
	v_mov_b32_e32 v4, v163
	v_cvt_pk_fp8_f32 v4, v5, v6
	v_med3_f32 v6, v8, s41, v205
	v_med3_f32 v7, v9, s41, v205
	v_med3_f32 v8, v10, s41, v205
	v_med3_f32 v9, v11, s41, v205
	v_mov_b32_e32 v5, v163
	v_cvt_pk_fp8_f32 v5, v8, v9
	v_cvt_pk_fp8_f32 v4, v6, v7 op_sel:[0,0,1]
	v_med3_f32 v6, v12, s41, v205
	v_med3_f32 v7, v13, s41, v205
	v_cvt_pk_fp8_f32 v5, v6, v7 op_sel:[0,0,1]
	v_add_co_u32_e32 v2, vcc, 0x58000, v2
	v_mov_b32_e32 v208, v206
	s_nop 0
	v_addc_co_u32_e32 v3, vcc, 0, v3, vcc
	s_and_b64 vcc, exec, s[0:1]
	s_mov_b32 s48, s47
	s_mov_b32 s22, s20
	s_mov_b64 s[24:25], s[6:7]
	s_mov_b32 s21, s45
	global_store_dwordx2 v[2:3], v[4:5], off
	s_cbranch_vccz .LBB0_1042
	s_waitcnt vmcnt(0)
	s_cmpk_gt_u32 s19, 0xff
	s_cbranch_scc1 .LBB0_1064
	s_barrier

.LBB0_1128:
	ds_read_b128 v[2:5], v176
	ds_read_b128 v[6:9], v176 offset:1024
	ds_read_b128 v[10:13], v176 offset:2048
	ds_read_b128 v[14:17], v176 offset:3072
	s_add_u32 s34, s30, 0xfffc0080
	s_addc_u32 s35, s31, -1
	s_cmp_eq_u32 s60, 12
	s_cselect_b32 s37, s19, s35
	s_cselect_b32 s36, s56, s34
	s_cselect_b32 s35, s21, s59
	s_cselect_b32 s34, s57, s58
	v_lshl_add_u64 v[164:165], s[30:31], 0, v[156:157]
	s_add_i32 m0, s27, 0xc000
	ds_read_b128 v[184:187], v177
	ds_read_b128 v[188:191], v177 offset:1024
	ds_read_b128 v[198:201], v177 offset:2048
	ds_read_b128 v[202:205], v177 offset:3072
	ds_read_b128 v[206:209], v177 offset:4096
	ds_read_b128 v[210:213], v177 offset:5120
	ds_read_b128 v[214:217], v177 offset:6144
	ds_read_b128 v[218:221], v177 offset:7168
	global_load_lds_dwordx4 v[164:165], off
	v_lshl_add_u64 v[164:165], s[30:31], 0, v[158:159]
	s_add_i32 m0, s27, 0xe000
	s_nop 0
	global_load_lds_dwordx4 v[164:165], off
	s_waitcnt lgkmcnt(8)
	s_barrier
	s_waitcnt lgkmcnt(0)
	s_waitcnt lgkmcnt(0)
	v_mfma_f32_16x16x128_f8f6f4 v[142:145], v[2:9], v[184:191], v[142:145]
	v_mfma_f32_16x16x128_f8f6f4 v[138:141], v[10:17], v[184:191], v[138:141]
	v_mfma_f32_16x16x128_f8f6f4 v[126:129], v[2:9], v[198:205], v[126:129]
	v_mfma_f32_16x16x128_f8f6f4 v[122:125], v[10:17], v[198:205], v[122:125]
	v_mfma_f32_16x16x128_f8f6f4 v[110:113], v[2:9], v[206:213], v[110:113]
	v_mfma_f32_16x16x128_f8f6f4 v[106:109], v[10:17], v[206:213], v[106:109]
	v_mfma_f32_16x16x128_f8f6f4 v[94:97], v[2:9], v[214:221], v[94:97]
	v_mfma_f32_16x16x128_f8f6f4 v[90:93], v[10:17], v[214:221], v[90:93]
	s_barrier
	s_add_i32 s61, s50, s42
	v_lshl_add_u64 v[164:165], s[34:35], 0, v[148:149]
	s_mov_b32 m0, s61
	ds_read_b128 v[222:225], v178
	ds_read_b128 v[226:229], v178 offset:1024
	ds_read_b128 v[230:233], v178 offset:2048
	ds_read_b128 v[234:237], v178 offset:3072
	global_load_lds_dwordx4 v[164:165], off
	v_lshl_add_u64 v[166:167], s[34:35], 0, v[152:153]
	s_add_i32 m0, s61, 0x2000
	s_nop 0
	global_load_lds_dwordx4 v[166:167], off
	s_barrier
	s_waitcnt lgkmcnt(0)
	s_waitcnt lgkmcnt(0)
	v_mfma_f32_16x16x128_f8f6f4 v[134:137], v[222:229], v[184:191], v[134:137]
	v_mfma_f32_16x16x128_f8f6f4 v[130:133], v[230:237], v[184:191], v[130:133]
	v_mfma_f32_16x16x128_f8f6f4 v[118:121], v[222:229], v[198:205], v[118:121]
	v_mfma_f32_16x16x128_f8f6f4 v[114:117], v[230:237], v[198:205], v[114:117]
	v_mfma_f32_16x16x128_f8f6f4 v[102:105], v[222:229], v[206:213], v[102:105]
	v_mfma_f32_16x16x128_f8f6f4 v[98:101], v[230:237], v[206:213], v[98:101]
	v_mfma_f32_16x16x128_f8f6f4 v[86:89], v[222:229], v[214:221], v[86:89]
	v_mfma_f32_16x16x128_f8f6f4 v[82:85], v[230:237], v[214:221], v[82:85]
	s_mov_b32 m0, s27
	v_lshl_add_u64 v[168:169], s[36:37], 0, v[146:147]
	s_barrier
	ds_read_b128 v[184:187], v177 offset:16384
	ds_read_b128 v[188:191], v177 offset:17408
	ds_read_b128 v[198:201], v177 offset:18432
	ds_read_b128 v[202:205], v177 offset:19456
	ds_read_b128 v[206:209], v177 offset:20480
	ds_read_b128 v[210:213], v177 offset:21504
	ds_read_b128 v[214:217], v177 offset:22528
	ds_read_b128 v[218:221], v177 offset:23552
	global_load_lds_dwordx4 v[168:169], off
	v_lshl_add_u64 v[170:171], s[36:37], 0, v[150:151]
	s_mov_b32 m0, s29
	s_nop 0
	global_load_lds_dwordx4 v[170:171], off
	s_barrier
	s_waitcnt lgkmcnt(0)
	s_waitcnt lgkmcnt(0)
	v_mfma_f32_16x16x128_f8f6f4 v[78:81], v[2:9], v[184:191], v[78:81]
	v_mfma_f32_16x16x128_f8f6f4 v[74:77], v[10:17], v[184:191], v[74:77]
	v_mfma_f32_16x16x128_f8f6f4 v[66:69], v[2:9], v[198:205], v[66:69]
	v_mfma_f32_16x16x128_f8f6f4 v[58:61], v[10:17], v[198:205], v[58:61]
	v_mfma_f32_16x16x128_f8f6f4 v[50:53], v[2:9], v[206:213], v[50:53]
	v_mfma_f32_16x16x128_f8f6f4 v[42:45], v[10:17], v[206:213], v[42:45]
	v_mfma_f32_16x16x128_f8f6f4 v[34:37], v[2:9], v[214:221], v[34:37]
	v_mfma_f32_16x16x128_f8f6f4 v[26:29], v[10:17], v[214:221], v[26:29]
	s_barrier
	s_add_u32 s64, s34, 0x40000
	s_addc_u32 s65, s35, 0
	s_add_i32 s61, s51, s42
	v_lshl_add_u64 v[2:3], s[64:65], 0, v[148:149]
	s_mov_b32 m0, s61
	s_nop 0
	global_load_lds_dwordx4 v[2:3], off
	v_lshl_add_u64 v[2:3], s[64:65], 0, v[152:153]
	s_add_i32 m0, s61, 0x2000
	s_nop 0
	global_load_lds_dwordx4 v[2:3], off
	s_waitcnt vmcnt(6)
	s_barrier
	v_mfma_f32_16x16x128_f8f6f4 v[70:73], v[222:229], v[184:191], v[70:73]
	v_mfma_f32_16x16x128_f8f6f4 v[62:65], v[230:237], v[184:191], v[62:65]
	v_mfma_f32_16x16x128_f8f6f4 v[54:57], v[222:229], v[198:205], v[54:57]
	v_mfma_f32_16x16x128_f8f6f4 v[46:49], v[230:237], v[198:205], v[46:49]
	v_mfma_f32_16x16x128_f8f6f4 v[38:41], v[222:229], v[206:213], v[38:41]
	v_mfma_f32_16x16x128_f8f6f4 v[30:33], v[230:237], v[206:213], v[30:33]
	v_mfma_f32_16x16x128_f8f6f4 v[22:25], v[222:229], v[214:221], v[22:25]
	v_mfma_f32_16x16x128_f8f6f4 v[18:21], v[230:237], v[214:221], v[18:21]
	s_add_i32 s61, 0, 0x18000
	v_add_u32_e32 v14, s61, v174
	s_barrier
	ds_read_b128 v[2:5], v14
	ds_read_b128 v[6:9], v14 offset:1024
	ds_read_b128 v[10:13], v14 offset:2048
	ds_read_b128 v[14:17], v14 offset:3072
	s_add_u32 s36, s36, 0x40000
	s_addc_u32 s37, s37, 0
	s_mov_b32 m0, s44
	v_lshl_add_u64 v[192:193], s[36:37], 0, v[146:147]
	ds_read_b128 v[184:187], v177 offset:32768
	ds_read_b128 v[188:191], v177 offset:33792
	ds_read_b128 v[198:201], v177 offset:34816
	ds_read_b128 v[202:205], v177 offset:35840
	ds_read_b128 v[206:209], v177 offset:36864
	ds_read_b128 v[210:213], v177 offset:37888
	ds_read_b128 v[214:217], v177 offset:38912
	ds_read_b128 v[218:221], v177 offset:39936
	global_load_lds_dwordx4 v[192:193], off
	v_lshl_add_u64 v[192:193], s[36:37], 0, v[150:151]
	s_mov_b32 m0, s45
	s_nop 0
	global_load_lds_dwordx4 v[192:193], off
	s_waitcnt lgkmcnt(8)
	s_barrier
	s_waitcnt lgkmcnt(0)
	s_waitcnt lgkmcnt(0)
	v_mfma_f32_16x16x128_f8f6f4 v[142:145], v[2:9], v[184:191], v[142:145]
	v_mfma_f32_16x16x128_f8f6f4 v[138:141], v[10:17], v[184:191], v[138:141]
	v_mfma_f32_16x16x128_f8f6f4 v[126:129], v[2:9], v[198:205], v[126:129]
	v_mfma_f32_16x16x128_f8f6f4 v[122:125], v[10:17], v[198:205], v[122:125]
	v_mfma_f32_16x16x128_f8f6f4 v[110:113], v[2:9], v[206:213], v[110:113]
	v_mfma_f32_16x16x128_f8f6f4 v[106:109], v[10:17], v[206:213], v[106:109]
	v_mfma_f32_16x16x128_f8f6f4 v[94:97], v[2:9], v[214:221], v[94:97]
	v_mfma_f32_16x16x128_f8f6f4 v[90:93], v[10:17], v[214:221], v[90:93]
	s_barrier
	s_add_i32 s36, 0, 0x1c000
	s_add_i32 s37, s61, s42
	v_add_u32_e32 v192, s36, v174
	v_lshl_add_u64 v[164:165], v[164:165], 0, s[8:9]
	s_mov_b32 m0, s37
	ds_read_b128 v[222:225], v192
	ds_read_b128 v[226:229], v192 offset:1024
	ds_read_b128 v[230:233], v192 offset:2048
	ds_read_b128 v[234:237], v192 offset:3072
	global_load_lds_dwordx4 v[164:165], off
	v_lshl_add_u64 v[164:165], v[166:167], 0, s[8:9]
	s_add_i32 m0, s37, 0x2000
	s_nop 0
	global_load_lds_dwordx4 v[164:165], off
	s_barrier
	s_waitcnt lgkmcnt(0)
	s_waitcnt lgkmcnt(0)
	v_mfma_f32_16x16x128_f8f6f4 v[134:137], v[222:229], v[184:191], v[134:137]
	v_mfma_f32_16x16x128_f8f6f4 v[130:133], v[230:237], v[184:191], v[130:133]
	v_mfma_f32_16x16x128_f8f6f4 v[118:121], v[222:229], v[198:205], v[118:121]
	v_mfma_f32_16x16x128_f8f6f4 v[114:117], v[230:237], v[198:205], v[114:117]
	v_mfma_f32_16x16x128_f8f6f4 v[102:105], v[222:229], v[206:213], v[102:105]
	v_mfma_f32_16x16x128_f8f6f4 v[98:101], v[230:237], v[206:213], v[98:101]
	v_mfma_f32_16x16x128_f8f6f4 v[86:89], v[222:229], v[214:221], v[86:89]
	v_mfma_f32_16x16x128_f8f6f4 v[82:85], v[230:237], v[214:221], v[82:85]
	s_mov_b32 m0, s48
	v_lshl_add_u64 v[164:165], v[168:169], 0, s[8:9]
	s_barrier
	ds_read_b128 v[184:187], v177 offset:49152
	ds_read_b128 v[188:191], v177 offset:50176
	ds_read_b128 v[198:201], v177 offset:51200
	ds_read_b128 v[202:205], v177 offset:52224
	ds_read_b128 v[206:209], v177 offset:53248
	ds_read_b128 v[210:213], v177 offset:54272
	ds_read_b128 v[214:217], v177 offset:55296
	ds_read_b128 v[218:221], v177 offset:56320
	global_load_lds_dwordx4 v[164:165], off
	v_lshl_add_u64 v[164:165], v[170:171], 0, s[8:9]
	s_mov_b32 m0, s49
	s_nop 0
	global_load_lds_dwordx4 v[164:165], off
	s_barrier
	s_waitcnt lgkmcnt(0)
	s_waitcnt lgkmcnt(0)
	v_mfma_f32_16x16x128_f8f6f4 v[78:81], v[2:9], v[184:191], v[78:81]
	v_mfma_f32_16x16x128_f8f6f4 v[74:77], v[10:17], v[184:191], v[74:77]
	v_mfma_f32_16x16x128_f8f6f4 v[66:69], v[2:9], v[198:205], v[66:69]
	v_mfma_f32_16x16x128_f8f6f4 v[58:61], v[10:17], v[198:205], v[58:61]
	v_mfma_f32_16x16x128_f8f6f4 v[50:53], v[2:9], v[206:213], v[50:53]
	v_mfma_f32_16x16x128_f8f6f4 v[42:45], v[10:17], v[206:213], v[42:45]
	v_mfma_f32_16x16x128_f8f6f4 v[34:37], v[2:9], v[214:221], v[34:37]
	v_mfma_f32_16x16x128_f8f6f4 v[26:29], v[10:17], v[214:221], v[26:29]
	s_barrier
	s_add_u32 s34, s34, 0x40080
	s_addc_u32 s35, s35, 0
	s_add_i32 s36, s36, s42
	v_lshl_add_u64 v[2:3], s[34:35], 0, v[148:149]
	s_mov_b32 m0, s36
	s_nop 0
	global_load_lds_dwordx4 v[2:3], off
	v_lshl_add_u64 v[2:3], s[34:35], 0, v[152:153]
	s_add_i32 m0, s36, 0x2000
	s_nop 0
	global_load_lds_dwordx4 v[2:3], off
	s_waitcnt vmcnt(6)
	s_barrier
	v_mfma_f32_16x16x128_f8f6f4 v[70:73], v[222:229], v[184:191], v[70:73]
	v_mfma_f32_16x16x128_f8f6f4 v[62:65], v[230:237], v[184:191], v[62:65]
	v_mfma_f32_16x16x128_f8f6f4 v[54:57], v[222:229], v[198:205], v[54:57]
	v_mfma_f32_16x16x128_f8f6f4 v[46:49], v[230:237], v[198:205], v[46:49]
	v_mfma_f32_16x16x128_f8f6f4 v[38:41], v[222:229], v[206:213], v[38:41]
	v_mfma_f32_16x16x128_f8f6f4 v[30:33], v[230:237], v[206:213], v[30:33]
	v_mfma_f32_16x16x128_f8f6f4 v[22:25], v[222:229], v[214:221], v[22:25]
	v_mfma_f32_16x16x128_f8f6f4 v[18:21], v[230:237], v[214:221], v[18:21]
	s_add_i32 s60, s60, 2
	s_add_u32 s30, s30, 0x100
	s_addc_u32 s31, s31, 0
	s_add_u32 s58, s58, 0x100
	s_addc_u32 s59, s59, 0
	s_cmp_gt_u32 s60, 13
	s_barrier
	s_cbranch_scc0 .LBB0_1128
	v_lshl_add_u32 v8, s26, 8, v172
	s_lshl_b32 s19, s28, 8
	s_and_b32 s19, s19, 0x700
	v_ashrrev_i32_e32 v9, 31, v8
	v_or_b32_e32 v4, s19, v175
	s_waitcnt vmcnt(0)
	v_mul_f32_e32 v10, 0x3b800000, v154
	v_lshlrev_b64 v[2:3], 12, v[8:9]
	v_lshl_add_u64 v[2:3], s[6:7], 0, v[2:3]
	v_lshlrev_b32_e32 v154, 1, v4
	v_pk_mul_f32 v[4:5], v[10:11], v[142:143] op_sel_hi:[0,1]
	s_nop 15
	s_nop 15
	v_lshl_add_u64 v[2:3], v[2:3], 0, v[154:155]
	v_pk_mul_f32 v[6:7], v[10:11], v[144:145] op_sel_hi:[0,1]
	v_cvt_pk_bf16_f32 v4, v4, v5
	v_cvt_pk_bf16_f32 v5, v6, v7
	v_pk_mul_f32 v[12:13], v[10:11], v[140:141] op_sel_hi:[0,1]
	v_pk_mul_f32 v[14:15], v[10:11], v[138:139] op_sel_hi:[0,1]
	v_cvt_pk_bf16_f32 v6, v14, v15
	v_cvt_pk_bf16_f32 v7, v12, v13
	global_store_dwordx4 v[2:3], v[4:7], off
	v_pk_mul_f32 v[12:13], v[10:11], v[132:133] op_sel_hi:[0,1]
	s_nop 0
	v_pk_mul_f32 v[4:5], v[10:11], v[134:135] op_sel_hi:[0,1]
	v_pk_mul_f32 v[6:7], v[10:11], v[136:137] op_sel_hi:[0,1]
	v_cvt_pk_bf16_f32 v4, v4, v5
	v_pk_mul_f32 v[10:11], v[10:11], v[130:131] op_sel_hi:[0,1]
	v_cvt_pk_bf16_f32 v5, v6, v7
	v_cvt_pk_bf16_f32 v6, v10, v11
	v_cvt_pk_bf16_f32 v7, v12, v13
	global_store_dwordx4 v[2:3], v[4:7], off offset:256
	v_mul_f32_e32 v10, 0x3b800000, v183
	v_pk_mul_f32 v[14:15], v[10:11], v[124:125] op_sel_hi:[0,1]
	v_or_b32_e32 v4, 16, v8
	v_ashrrev_i32_e32 v5, 31, v4
	v_lshlrev_b64 v[4:5], 12, v[4:5]
	v_lshl_add_u64 v[4:5], s[6:7], 0, v[4:5]
	v_lshl_add_u64 v[12:13], v[4:5], 0, v[154:155]
	v_pk_mul_f32 v[4:5], v[10:11], v[126:127] op_sel_hi:[0,1]
	v_pk_mul_f32 v[6:7], v[10:11], v[128:129] op_sel_hi:[0,1]
	v_cvt_pk_bf16_f32 v4, v4, v5
	v_cvt_pk_bf16_f32 v5, v6, v7
	v_pk_mul_f32 v[16:17], v[10:11], v[122:123] op_sel_hi:[0,1]
	v_cvt_pk_bf16_f32 v6, v16, v17
	v_cvt_pk_bf16_f32 v7, v14, v15
	global_store_dwordx4 v[12:13], v[4:7], off
	v_pk_mul_f32 v[14:15], v[10:11], v[116:117] op_sel_hi:[0,1]
	s_nop 0
	v_pk_mul_f32 v[4:5], v[10:11], v[118:119] op_sel_hi:[0,1]
	v_pk_mul_f32 v[6:7], v[10:11], v[120:121] op_sel_hi:[0,1]
	v_cvt_pk_bf16_f32 v4, v4, v5
	v_pk_mul_f32 v[10:11], v[10:11], v[114:115] op_sel_hi:[0,1]
	v_cvt_pk_bf16_f32 v5, v6, v7
	v_cvt_pk_bf16_f32 v6, v10, v11
	v_cvt_pk_bf16_f32 v7, v14, v15
	global_store_dwordx4 v[12:13], v[4:7], off offset:256
	v_mul_f32_e32 v10, 0x3b800000, v182
	v_pk_mul_f32 v[14:15], v[10:11], v[108:109] op_sel_hi:[0,1]
	v_or_b32_e32 v4, 32, v8
	v_ashrrev_i32_e32 v5, 31, v4
	v_lshlrev_b64 v[4:5], 12, v[4:5]
	v_lshl_add_u64 v[4:5], s[6:7], 0, v[4:5]
	v_lshl_add_u64 v[12:13], v[4:5], 0, v[154:155]
	v_pk_mul_f32 v[4:5], v[10:11], v[110:111] op_sel_hi:[0,1]
	v_pk_mul_f32 v[6:7], v[10:11], v[112:113] op_sel_hi:[0,1]
	v_cvt_pk_bf16_f32 v4, v4, v5
	v_cvt_pk_bf16_f32 v5, v6, v7
	v_pk_mul_f32 v[16:17], v[10:11], v[106:107] op_sel_hi:[0,1]
	v_cvt_pk_bf16_f32 v6, v16, v17
	v_cvt_pk_bf16_f32 v7, v14, v15
	global_store_dwordx4 v[12:13], v[4:7], off
	v_pk_mul_f32 v[14:15], v[10:11], v[100:101] op_sel_hi:[0,1]
	s_nop 0
	v_pk_mul_f32 v[4:5], v[10:11], v[102:103] op_sel_hi:[0,1]
	v_pk_mul_f32 v[6:7], v[10:11], v[104:105] op_sel_hi:[0,1]
	v_cvt_pk_bf16_f32 v4, v4, v5
	v_pk_mul_f32 v[10:11], v[10:11], v[98:99] op_sel_hi:[0,1]
	v_cvt_pk_bf16_f32 v5, v6, v7
	v_cvt_pk_bf16_f32 v6, v10, v11
	v_cvt_pk_bf16_f32 v7, v14, v15
	global_store_dwordx4 v[12:13], v[4:7], off offset:256
	s_nop 1
	v_or_b32_e32 v4, 48, v8
	v_ashrrev_i32_e32 v5, 31, v4
	v_lshlrev_b64 v[4:5], 12, v[4:5]
	v_mul_f32_e32 v8, 0x3b800000, v181
	v_lshl_add_u64 v[4:5], s[6:7], 0, v[4:5]
	v_lshl_add_u64 v[10:11], v[4:5], 0, v[154:155]
	v_pk_mul_f32 v[6:7], v[8:9], v[96:97] op_sel_hi:[0,1]
	v_pk_mul_f32 v[4:5], v[8:9], v[94:95] op_sel_hi:[0,1]
	v_pk_mul_f32 v[12:13], v[8:9], v[92:93] op_sel_hi:[0,1]
	v_pk_mul_f32 v[14:15], v[8:9], v[90:91] op_sel_hi:[0,1]
	v_cvt_pk_bf16_f32 v4, v4, v5
	v_cvt_pk_bf16_f32 v5, v6, v7
	v_cvt_pk_bf16_f32 v6, v14, v15
	v_cvt_pk_bf16_f32 v7, v12, v13
	global_store_dwordx4 v[10:11], v[4:7], off
	v_pk_mul_f32 v[12:13], v[8:9], v[84:85] op_sel_hi:[0,1]
	s_nop 0
	v_pk_mul_f32 v[6:7], v[8:9], v[88:89] op_sel_hi:[0,1]
	v_pk_mul_f32 v[4:5], v[8:9], v[86:87] op_sel_hi:[0,1]
	v_pk_mul_f32 v[8:9], v[8:9], v[82:83] op_sel_hi:[0,1]
	v_cvt_pk_bf16_f32 v4, v4, v5
	v_cvt_pk_bf16_f32 v5, v6, v7
	v_cvt_pk_bf16_f32 v6, v8, v9
	v_cvt_pk_bf16_f32 v7, v12, v13
	v_mul_f32_e32 v8, 0x3b800000, v180
	global_store_dwordx4 v[10:11], v[4:7], off offset:256
	v_pk_mul_f32 v[12:13], v[8:9], v[76:77] op_sel_hi:[0,1]
	v_pk_mul_f32 v[14:15], v[8:9], v[74:75] op_sel_hi:[0,1]
	v_pk_mul_f32 v[6:7], v[8:9], v[80:81] op_sel_hi:[0,1]
	v_pk_mul_f32 v[4:5], v[8:9], v[78:79] op_sel_hi:[0,1]
	v_cvt_pk_bf16_f32 v4, v4, v5
	v_cvt_pk_bf16_f32 v5, v6, v7
	v_cvt_pk_bf16_f32 v6, v14, v15
	v_cvt_pk_bf16_f32 v7, v12, v13
	v_add_co_u32_e32 v12, vcc, s52, v2
	v_lshl_add_u64 v[10:11], v[2:3], 0, s[10:11]
	s_nop 0
	v_addc_co_u32_e32 v13, vcc, 0, v3, vcc
	global_store_dwordx4 v[12:13], v[4:7], off
	v_pk_mul_f32 v[12:13], v[8:9], v[64:65] op_sel_hi:[0,1]
	s_nop 0
	v_pk_mul_f32 v[6:7], v[8:9], v[72:73] op_sel_hi:[0,1]
	v_pk_mul_f32 v[4:5], v[8:9], v[70:71] op_sel_hi:[0,1]
	v_pk_mul_f32 v[8:9], v[8:9], v[62:63] op_sel_hi:[0,1]
	v_cvt_pk_bf16_f32 v4, v4, v5
	v_cvt_pk_bf16_f32 v5, v6, v7
	v_cvt_pk_bf16_f32 v6, v8, v9
	v_cvt_pk_bf16_f32 v7, v12, v13
	v_mul_f32_e32 v8, 0x3b800000, v179
	global_store_dwordx4 v[10:11], v[4:7], off offset:256
	v_pk_mul_f32 v[12:13], v[8:9], v[60:61] op_sel_hi:[0,1]
	v_pk_mul_f32 v[14:15], v[8:9], v[58:59] op_sel_hi:[0,1]
	v_pk_mul_f32 v[6:7], v[8:9], v[68:69] op_sel_hi:[0,1]
	v_pk_mul_f32 v[4:5], v[8:9], v[66:67] op_sel_hi:[0,1]
	v_cvt_pk_bf16_f32 v4, v4, v5
	v_cvt_pk_bf16_f32 v5, v6, v7
	v_cvt_pk_bf16_f32 v6, v14, v15
	v_cvt_pk_bf16_f32 v7, v12, v13
	v_add_co_u32_e32 v12, vcc, s53, v2
	v_lshl_add_u64 v[10:11], v[2:3], 0, s[12:13]
	s_nop 0
	v_addc_co_u32_e32 v13, vcc, 0, v3, vcc
	global_store_dwordx4 v[12:13], v[4:7], off
	v_pk_mul_f32 v[12:13], v[8:9], v[48:49] op_sel_hi:[0,1]
	s_nop 0
	v_pk_mul_f32 v[6:7], v[8:9], v[56:57] op_sel_hi:[0,1]
	v_pk_mul_f32 v[4:5], v[8:9], v[54:55] op_sel_hi:[0,1]
	v_pk_mul_f32 v[8:9], v[8:9], v[46:47] op_sel_hi:[0,1]
	v_cvt_pk_bf16_f32 v4, v4, v5
	v_cvt_pk_bf16_f32 v5, v6, v7
	v_cvt_pk_bf16_f32 v6, v8, v9
	v_cvt_pk_bf16_f32 v7, v12, v13
	v_mul_f32_e32 v8, 0x3b800000, v173
	global_store_dwordx4 v[10:11], v[4:7], off offset:256
	v_pk_mul_f32 v[12:13], v[8:9], v[44:45] op_sel_hi:[0,1]
	v_pk_mul_f32 v[14:15], v[8:9], v[42:43] op_sel_hi:[0,1]
	v_pk_mul_f32 v[6:7], v[8:9], v[52:53] op_sel_hi:[0,1]
	v_pk_mul_f32 v[4:5], v[8:9], v[50:51] op_sel_hi:[0,1]
	v_cvt_pk_bf16_f32 v4, v4, v5
	v_cvt_pk_bf16_f32 v5, v6, v7
	v_cvt_pk_bf16_f32 v6, v14, v15
	v_cvt_pk_bf16_f32 v7, v12, v13
	v_add_co_u32_e32 v12, vcc, s54, v2
	v_lshl_add_u64 v[10:11], v[2:3], 0, s[14:15]
	s_nop 0
	v_addc_co_u32_e32 v13, vcc, 0, v3, vcc
	global_store_dwordx4 v[12:13], v[4:7], off
	v_pk_mul_f32 v[12:13], v[8:9], v[32:33] op_sel_hi:[0,1]
	s_nop 0
	v_pk_mul_f32 v[6:7], v[8:9], v[40:41] op_sel_hi:[0,1]
	v_pk_mul_f32 v[4:5], v[8:9], v[38:39] op_sel_hi:[0,1]
	v_pk_mul_f32 v[8:9], v[8:9], v[30:31] op_sel_hi:[0,1]
	v_cvt_pk_bf16_f32 v4, v4, v5
	v_cvt_pk_bf16_f32 v5, v6, v7
	v_cvt_pk_bf16_f32 v6, v8, v9
	v_mul_f32_e32 v8, 0x3b800000, v1
	v_cvt_pk_bf16_f32 v7, v12, v13
	global_store_dwordx4 v[10:11], v[4:7], off offset:256
	v_lshl_add_u64 v[10:11], v[2:3], 0, s[16:17]
	v_add_co_u32_e32 v2, vcc, s55, v2
	v_pk_mul_f32 v[4:5], v[8:9], v[34:35] op_sel_hi:[0,1]
	v_pk_mul_f32 v[6:7], v[8:9], v[36:37] op_sel_hi:[0,1]
	v_cvt_pk_bf16_f32 v4, v4, v5
	v_cvt_pk_bf16_f32 v5, v6, v7
	v_addc_co_u32_e32 v3, vcc, 0, v3, vcc
	v_pk_mul_f32 v[12:13], v[8:9], v[28:29] op_sel_hi:[0,1]
	v_pk_mul_f32 v[14:15], v[8:9], v[26:27] op_sel_hi:[0,1]
	v_cvt_pk_bf16_f32 v6, v14, v15
	v_cvt_pk_bf16_f32 v7, v12, v13
	global_store_dwordx4 v[2:3], v[4:7], off
	v_pk_mul_f32 v[2:3], v[8:9], v[22:23] op_sel_hi:[0,1]
	s_andn2_b64 vcc, exec, s[0:1]
	v_pk_mul_f32 v[4:5], v[8:9], v[24:25] op_sel_hi:[0,1]
	s_mov_b64 s[0:1], -1
	v_pk_mul_f32 v[6:7], v[8:9], v[20:21] op_sel_hi:[0,1]
	v_pk_mul_f32 v[8:9], v[8:9], v[18:19] op_sel_hi:[0,1]
	v_cvt_pk_bf16_f32 v2, v2, v3
	v_cvt_pk_bf16_f32 v3, v4, v5
	v_cvt_pk_bf16_f32 v4, v8, v9
	v_cvt_pk_bf16_f32 v5, v6, v7
	global_store_dwordx4 v[10:11], v[2:5], off offset:256
	s_cbranch_vccnz .LBB0_1120
	s_nop 0
	v_lshl_add_u32 v2, s18, 8, v172
	v_ashrrev_i32_e32 v3, 31, v2
	v_lshl_add_u64 v[2:3], v[2:3], 2, s[4:5]
	global_load_dword v154, v[2:3], off
	global_load_dword v183, v[2:3], off offset:64
	global_load_dword v182, v[2:3], off offset:128
	global_load_dword v181, v[2:3], off offset:192
	global_load_dword v180, v[2:3], off offset:512
	global_load_dword v179, v[2:3], off offset:576
	global_load_dword v173, v[2:3], off offset:640
	global_load_dword v1, v[2:3], off offset:704
	s_mov_b64 s[0:1], 0
	s_branch .LBB0_1120
